# hand-scheduled RWKV recurrence chunk body (2-step LDS prefetch) + converter waves keep second tile in flight (counted vmcnt)
# speedup vs baseline: 1.0027x; 1.0027x over previous
.LBB0_443:
	v_cndmask_b32_e64 v0, 0, 1, s[40:41]
	v_lshl_add_u32 v4, s21, 2, v145
	v_cmp_ne_u32_e64 s[8:9], 1, v0
	v_xor_b32_e32 v0, v155, v143
	s_mov_b64 s[44:45], -1
	s_andn2_b64 vcc, exec, s[40:41]
	v_lshl_add_u32 v158, v0, 4, v146
	v_or_b32_e32 v157, 1, v4
	s_cbranch_vccnz .LBB0_445
	s_waitcnt vmcnt(62)
	v_mul_f32_e32 v1, 0x43800000, v12
	s_waitcnt vmcnt(62)
	v_mul_f32_e32 v2, 0x43800000, v14
	v_mov_b32_e32 v0, 0
	v_cvt_pk_fp8_f32 v0, v1, v2
	s_waitcnt vmcnt(61)
	v_mul_f32_e32 v3, 0x43800000, v16
	s_waitcnt vmcnt(60)
	v_mul_f32_e32 v5, 0x43800000, v18
	s_waitcnt vmcnt(59)
	v_mul_f32_e32 v2, 0x43800000, v20
	v_cvt_pk_fp8_f32 v0, v3, v5 op_sel:[0,0,1]
	s_waitcnt vmcnt(58)
	v_mul_f32_e32 v3, 0x43800000, v22
	v_mov_b32_e32 v1, 0
	v_cvt_pk_fp8_f32 v1, v2, v3
	s_waitcnt vmcnt(57)
	v_mul_f32_e32 v5, 0x43800000, v24
	s_waitcnt vmcnt(56)
	v_mul_f32_e32 v6, 0x43800000, v26
	s_waitcnt vmcnt(55)
	v_mul_f32_e32 v3, 0x43800000, v28
	v_cvt_pk_fp8_f32 v1, v5, v6 op_sel:[0,0,1]
	s_waitcnt vmcnt(54)
	v_mul_f32_e32 v5, 0x43800000, v30
	v_mov_b32_e32 v2, 0
	v_cvt_pk_fp8_f32 v2, v3, v5
	s_waitcnt vmcnt(53)
	v_mul_f32_e32 v6, 0x43800000, v32
	s_waitcnt vmcnt(52)
	v_mul_f32_e32 v7, 0x43800000, v34
	s_waitcnt vmcnt(51)
	v_mul_f32_e32 v5, 0x43800000, v36
	v_cvt_pk_fp8_f32 v2, v6, v7 op_sel:[0,0,1]
	s_waitcnt vmcnt(50)
	v_mul_f32_e32 v6, 0x43800000, v38
	v_mov_b32_e32 v3, 0
	v_cvt_pk_fp8_f32 v3, v5, v6
	s_waitcnt vmcnt(49)
	v_mul_f32_e32 v7, 0x43800000, v40
	s_waitcnt vmcnt(48)
	v_mul_f32_e32 v159, 0x43800000, v42
	s_waitcnt vmcnt(44)
	v_mul_f32_e32 v5, 0x43800000, v50
	v_cvt_pk_fp8_f32 v3, v7, v159 op_sel:[0,0,1]
	s_waitcnt vmcnt(40)
	v_mul_f32_e32 v6, 0x43800000, v58
	s_waitcnt vmcnt(36)
	v_mul_f32_e32 v7, 0x43800000, v74
	s_waitcnt vmcnt(32)
	v_mul_f32_e32 v159, 0x43800000, v88
	ds_write_b128 v158, v[0:3]
	v_mul_f32_e32 v1, 0x43800000, v44
	v_mul_f32_e32 v2, 0x43800000, v46
	v_mov_b32_e32 v0, 0
	v_cvt_pk_fp8_f32 v0, v1, v2
	v_mul_f32_e32 v3, 0x43800000, v48
	v_mul_f32_e32 v2, 0x43800000, v52
	v_mov_b32_e32 v1, 0
	v_cvt_pk_fp8_f32 v0, v3, v5 op_sel:[0,0,1]
	v_mul_f32_e32 v3, 0x43800000, v54
	v_cvt_pk_fp8_f32 v1, v2, v3
	v_mul_f32_e32 v5, 0x43800000, v56
	v_mul_f32_e32 v3, 0x43800000, v60
	v_mov_b32_e32 v2, 0
	v_cvt_pk_fp8_f32 v1, v5, v6 op_sel:[0,0,1]
	v_mul_f32_e32 v5, 0x43800000, v62
	v_cvt_pk_fp8_f32 v2, v3, v5
	v_mul_f32_e32 v6, 0x43800000, v64
	v_mul_f32_e32 v5, 0x43800000, v76
	v_mov_b32_e32 v3, 0
	v_cvt_pk_fp8_f32 v2, v6, v7 op_sel:[0,0,1]
	v_mul_f32_e32 v6, 0x43800000, v78
	v_cvt_pk_fp8_f32 v3, v5, v6
	v_mul_f32_e32 v7, 0x43800000, v80
	v_or_b32_e32 v5, 1, v4
	s_mov_b64 s[44:45], 0
	v_cvt_pk_fp8_f32 v3, v7, v159 op_sel:[0,0,1]
.LBB0_445:
	s_andn2_b64 vcc, exec, s[44:45]
	v_add_u32_e32 v159, -8, v156
	s_cbranch_vccnz .LBB0_459
	s_waitcnt vmcnt(62)
	v_cvt_pk_bf16_f32 v0, v12, v14
	s_waitcnt vmcnt(60)
	v_cvt_pk_bf16_f32 v1, v16, v18
	s_waitcnt vmcnt(58)
	v_cvt_pk_bf16_f32 v2, v20, v22
	v_cndmask_b32_e64 v0, 0, v0, s[4:5]
	v_cndmask_b32_e64 v1, 0, v1, s[4:5]
	v_cndmask_b32_e64 v2, 0, v2, s[4:5]
	s_and_saveexec_b64 s[44:45], s[6:7]
	s_xor_b64 s[44:45], exec, s[44:45]
	v_xor_b32_e32 v4, v159, v143
	v_mov_b32_e32 v3, s15
	v_lshl_add_u32 v4, v4, 4, v146
	ds_write_b128 v4, v[0:3]
	s_or_saveexec_b64 s[44:45], s[44:45]
	v_mov_b32_e32 v4, 0
	s_xor_b64 exec, exec, s[44:45]
	s_cbranch_execz .LBB0_450
	v_xor_b32_e32 v4, v159, v143
	s_waitcnt vmcnt(56)
	v_cvt_pk_bf16_f32 v3, v24, v26
	v_lshl_add_u32 v4, v4, 4, v146
	ds_write_b128 v4, v[0:3]
	s_waitcnt vmcnt(54)
	v_cvt_pk_bf16_f32 v4, v28, v30
.LBB0_450:
	s_or_b64 exec, exec, s[44:45]
	s_waitcnt vmcnt(52)
	v_cvt_pk_bf16_f32 v0, v32, v34
	v_cndmask_b32_e64 v5, 0, v0, s[4:5]
	s_waitcnt vmcnt(50)
	v_cvt_pk_bf16_f32 v0, v36, v38
	v_cndmask_b32_e64 v6, 0, v0, s[4:5]
	s_and_saveexec_b64 s[44:45], s[6:7]
	s_xor_b64 s[44:45], exec, s[44:45]
	v_add_u32_e32 v0, -7, v156
	v_xor_b32_e32 v0, v0, v143
	v_mov_b32_e32 v7, s15
	v_lshl_add_u32 v0, v0, 4, v146
	ds_write_b128 v0, v[4:7]
	s_or_saveexec_b64 s[44:45], s[44:45]
	v_mov_b32_e32 v2, 0
	s_xor_b64 exec, exec, s[44:45]
	s_cbranch_execz .LBB0_454
	v_add_u32_e32 v0, -7, v156
	v_xor_b32_e32 v0, v0, v143
	s_waitcnt vmcnt(48)
	v_cvt_pk_bf16_f32 v7, v40, v42
	v_lshl_add_u32 v0, v0, 4, v146
	s_waitcnt vmcnt(46)
	v_cvt_pk_bf16_f32 v2, v44, v46
	ds_write_b128 v0, v[4:7]
.LBB0_454:
	s_or_b64 exec, exec, s[44:45]
	s_waitcnt vmcnt(44)
	v_cvt_pk_bf16_f32 v0, v48, v50
	v_cndmask_b32_e64 v3, 0, v0, s[4:5]
	s_waitcnt vmcnt(42)
	v_cvt_pk_bf16_f32 v0, v52, v54
	v_cndmask_b32_e64 v4, 0, v0, s[4:5]
	s_and_saveexec_b64 s[44:45], s[6:7]
	s_xor_b64 s[44:45], exec, s[44:45]
	v_add_u32_e32 v0, -6, v156
	v_xor_b32_e32 v0, v0, v143
	v_mov_b32_e32 v5, s15
	v_lshl_add_u32 v0, v0, 4, v146
	ds_write_b128 v0, v[2:5]
	s_or_saveexec_b64 s[44:45], s[44:45]
	v_mov_b32_e32 v0, 0
	s_xor_b64 exec, exec, s[44:45]
	s_cbranch_execz .LBB0_458
	v_add_u32_e32 v0, -6, v156
	v_xor_b32_e32 v0, v0, v143
	s_waitcnt vmcnt(40)
	v_cvt_pk_bf16_f32 v5, v56, v58
	v_lshl_add_u32 v0, v0, 4, v146
	ds_write_b128 v0, v[2:5]
	s_waitcnt vmcnt(38)
	v_cvt_pk_bf16_f32 v0, v60, v62
.LBB0_458:
	s_or_b64 exec, exec, s[44:45]
	s_waitcnt vmcnt(36)
	v_cvt_pk_bf16_f32 v1, v64, v74
	s_waitcnt vmcnt(34)
	v_cvt_pk_bf16_f32 v2, v76, v78
	s_waitcnt vmcnt(32)
	v_cvt_pk_bf16_f32 v3, v80, v88
	v_cndmask_b32_e64 v1, 0, v1, s[4:5]
	v_cndmask_b32_e64 v2, 0, v2, s[4:5]
	v_cndmask_b32_e64 v3, 0, v3, s[4:5]
	v_add_u32_e32 v5, -5, v156
.LBB0_459:
	v_xor_b32_e32 v4, v5, v143
	v_lshl_add_u32 v4, v4, 4, v146
	s_and_b64 vcc, exec, s[8:9]
	s_mov_b64 s[44:45], -1
	ds_write_b128 v4, v[0:3]
	s_cbranch_vccnz .LBB0_461
	s_waitcnt vmcnt(62)
	v_mul_f32_e32 v1, 0x43800000, v13
	s_waitcnt vmcnt(62)
	v_mul_f32_e32 v2, 0x43800000, v15
	v_mov_b32_e32 v0, 0
	v_cvt_pk_fp8_f32 v0, v1, v2
	s_waitcnt vmcnt(61)
	v_mul_f32_e32 v3, 0x43800000, v17
	s_waitcnt vmcnt(60)
	v_mul_f32_e32 v4, 0x43800000, v19
	s_waitcnt vmcnt(59)
	v_mul_f32_e32 v2, 0x43800000, v21
	v_cvt_pk_fp8_f32 v0, v3, v4 op_sel:[0,0,1]
	s_waitcnt vmcnt(58)
	v_mul_f32_e32 v3, 0x43800000, v23
	v_mov_b32_e32 v1, 0
	v_cvt_pk_fp8_f32 v1, v2, v3
	s_waitcnt vmcnt(57)
	v_mul_f32_e32 v4, 0x43800000, v25
	s_waitcnt vmcnt(56)
	v_mul_f32_e32 v5, 0x43800000, v27
	s_waitcnt vmcnt(55)
	v_mul_f32_e32 v3, 0x43800000, v29
	v_cvt_pk_fp8_f32 v1, v4, v5 op_sel:[0,0,1]
	s_waitcnt vmcnt(54)
	v_mul_f32_e32 v4, 0x43800000, v31
	v_mov_b32_e32 v2, 0
	v_cvt_pk_fp8_f32 v2, v3, v4
	s_waitcnt vmcnt(53)
	v_mul_f32_e32 v5, 0x43800000, v33
	s_waitcnt vmcnt(52)
	v_mul_f32_e32 v6, 0x43800000, v35
	s_waitcnt vmcnt(51)
	v_mul_f32_e32 v4, 0x43800000, v37
	v_cvt_pk_fp8_f32 v2, v5, v6 op_sel:[0,0,1]
	s_waitcnt vmcnt(50)
	v_mul_f32_e32 v5, 0x43800000, v39
	v_mov_b32_e32 v3, 0
	v_cvt_pk_fp8_f32 v3, v4, v5
	s_waitcnt vmcnt(49)
	v_mul_f32_e32 v6, 0x43800000, v41
	s_waitcnt vmcnt(48)
	v_mul_f32_e32 v7, 0x43800000, v43
	s_waitcnt vmcnt(44)
	v_mul_f32_e32 v4, 0x43800000, v51
	v_cvt_pk_fp8_f32 v3, v6, v7 op_sel:[0,0,1]
	s_waitcnt vmcnt(40)
	v_mul_f32_e32 v5, 0x43800000, v59
	s_waitcnt vmcnt(36)
	v_mul_f32_e32 v6, 0x43800000, v75
	s_waitcnt vmcnt(32)
	v_mul_f32_e32 v7, 0x43800000, v89
	ds_write_b128 v158, v[0:3] offset:512
	v_mul_f32_e32 v1, 0x43800000, v45
	v_mul_f32_e32 v2, 0x43800000, v47
	v_mov_b32_e32 v0, 0
	v_cvt_pk_fp8_f32 v0, v1, v2
	v_mul_f32_e32 v3, 0x43800000, v49
	v_mul_f32_e32 v2, 0x43800000, v53
	v_mov_b32_e32 v1, 0
	v_cvt_pk_fp8_f32 v0, v3, v4 op_sel:[0,0,1]
	v_mul_f32_e32 v3, 0x43800000, v55
	v_cvt_pk_fp8_f32 v1, v2, v3
	v_mul_f32_e32 v4, 0x43800000, v57
	v_mul_f32_e32 v3, 0x43800000, v61
	v_mov_b32_e32 v2, 0
	v_cvt_pk_fp8_f32 v1, v4, v5 op_sel:[0,0,1]
	v_mul_f32_e32 v4, 0x43800000, v63
	v_cvt_pk_fp8_f32 v2, v3, v4
	v_mul_f32_e32 v5, 0x43800000, v65
	v_mul_f32_e32 v4, 0x43800000, v77
	v_mov_b32_e32 v3, 0
	v_cvt_pk_fp8_f32 v2, v5, v6 op_sel:[0,0,1]
	v_mul_f32_e32 v5, 0x43800000, v79
	v_cvt_pk_fp8_f32 v3, v4, v5
	v_mul_f32_e32 v6, 0x43800000, v81
	s_mov_b64 s[44:45], 0
	v_cvt_pk_fp8_f32 v3, v6, v7 op_sel:[0,0,1]
.LBB0_461:
	s_andn2_b64 vcc, exec, s[44:45]
	s_cbranch_vccnz .LBB0_475
	s_waitcnt vmcnt(62)
	v_cvt_pk_bf16_f32 v0, v13, v15
	s_waitcnt vmcnt(60)
	v_cvt_pk_bf16_f32 v1, v17, v19
	s_waitcnt vmcnt(58)
	v_cvt_pk_bf16_f32 v2, v21, v23
	v_xor_b32_e32 v3, v159, v143
	v_cndmask_b32_e64 v0, 0, v0, s[4:5]
	v_cndmask_b32_e64 v1, 0, v1, s[4:5]
	v_cndmask_b32_e64 v2, 0, v2, s[4:5]
	v_lshl_add_u32 v5, v3, 4, v146
	s_and_saveexec_b64 s[44:45], s[6:7]
	s_xor_b64 s[44:45], exec, s[44:45]
	v_mov_b32_e32 v3, s15
	ds_write_b128 v5, v[0:3] offset:512
	s_or_saveexec_b64 s[44:45], s[44:45]
	v_mov_b32_e32 v4, 0
	s_xor_b64 exec, exec, s[44:45]
	s_cbranch_execz .LBB0_466
	s_waitcnt vmcnt(56)
	v_cvt_pk_bf16_f32 v3, v25, v27
	s_waitcnt vmcnt(54)
	v_cvt_pk_bf16_f32 v4, v29, v31
	ds_write_b128 v5, v[0:3] offset:512
.LBB0_466:
	s_or_b64 exec, exec, s[44:45]
	s_waitcnt vmcnt(52)
	v_cvt_pk_bf16_f32 v0, v33, v35
	v_cndmask_b32_e64 v5, 0, v0, s[4:5]
	s_waitcnt vmcnt(50)
	v_cvt_pk_bf16_f32 v0, v37, v39
	v_cndmask_b32_e64 v6, 0, v0, s[4:5]
	v_add_u32_e32 v0, -7, v156
	v_xor_b32_e32 v0, v0, v143
	s_and_saveexec_b64 s[44:45], s[6:7]
	s_xor_b64 s[44:45], exec, s[44:45]
	v_mov_b32_e32 v7, s15
	v_lshl_add_u32 v0, v0, 4, v146
	ds_write_b128 v0, v[4:7] offset:512
	s_or_saveexec_b64 s[44:45], s[44:45]
	v_mov_b32_e32 v2, 0
	s_xor_b64 exec, exec, s[44:45]
	s_cbranch_execz .LBB0_470
	s_waitcnt vmcnt(48)
	v_cvt_pk_bf16_f32 v7, v41, v43
	v_lshl_add_u32 v0, v0, 4, v146
	s_waitcnt vmcnt(46)
	v_cvt_pk_bf16_f32 v2, v45, v47
	ds_write_b128 v0, v[4:7] offset:512
.LBB0_470:
	s_or_b64 exec, exec, s[44:45]
	s_waitcnt vmcnt(44)
	v_cvt_pk_bf16_f32 v0, v49, v51
	v_cndmask_b32_e64 v3, 0, v0, s[4:5]
	s_waitcnt vmcnt(42)
	v_cvt_pk_bf16_f32 v0, v53, v55
	v_cndmask_b32_e64 v4, 0, v0, s[4:5]
	v_add_u32_e32 v0, -6, v156
	v_xor_b32_e32 v1, v0, v143
	s_and_saveexec_b64 s[44:45], s[6:7]
	s_xor_b64 s[44:45], exec, s[44:45]
	v_mov_b32_e32 v5, s15
	v_lshl_add_u32 v0, v1, 4, v146
	ds_write_b128 v0, v[2:5] offset:512
	s_or_saveexec_b64 s[44:45], s[44:45]
	v_mov_b32_e32 v0, 0
	s_xor_b64 exec, exec, s[44:45]
	s_cbranch_execz .LBB0_474
	s_waitcnt vmcnt(40)
	v_cvt_pk_bf16_f32 v5, v57, v59
	v_lshl_add_u32 v0, v1, 4, v146
	ds_write_b128 v0, v[2:5] offset:512
	s_waitcnt vmcnt(38)
	v_cvt_pk_bf16_f32 v0, v61, v63
.LBB0_474:
	s_or_b64 exec, exec, s[44:45]
	s_waitcnt vmcnt(36)
	v_cvt_pk_bf16_f32 v1, v65, v75
	s_waitcnt vmcnt(34)
	v_cvt_pk_bf16_f32 v2, v77, v79
	s_waitcnt vmcnt(32)
	v_cvt_pk_bf16_f32 v3, v81, v89
	v_cndmask_b32_e64 v1, 0, v1, s[4:5]
	v_cndmask_b32_e64 v2, 0, v2, s[4:5]
	v_cndmask_b32_e64 v3, 0, v3, s[4:5]
	v_add_u32_e32 v157, -5, v156

.LBB0_477:
	s_lshl_b32 s0, s21, 2
	v_add_u32_e32 v0, 4, v155
	v_add3_u32 v4, v145, s0, 4
	v_xor_b32_e32 v0, v0, v143
	s_mov_b64 s[44:45], -1
	s_and_b64 vcc, exec, s[8:9]
	v_lshl_add_u32 v158, v0, 4, v146
	v_or_b32_e32 v157, 1, v4
	s_cbranch_vccnz .LBB0_479
	s_waitcnt vmcnt(62)
	v_mul_f32_e32 v1, 0x43800000, v66
	s_waitcnt vmcnt(62)
	v_mul_f32_e32 v2, 0x43800000, v68
	v_mov_b32_e32 v0, 0
	v_cvt_pk_fp8_f32 v0, v1, v2
	s_waitcnt vmcnt(61)
	v_mul_f32_e32 v3, 0x43800000, v70
	s_waitcnt vmcnt(60)
	v_mul_f32_e32 v5, 0x43800000, v72
	s_waitcnt vmcnt(59)
	v_mul_f32_e32 v2, 0x43800000, v82
	v_cvt_pk_fp8_f32 v0, v3, v5 op_sel:[0,0,1]
	s_waitcnt vmcnt(58)
	v_mul_f32_e32 v3, 0x43800000, v84
	v_mov_b32_e32 v1, 0
	v_cvt_pk_fp8_f32 v1, v2, v3
	s_waitcnt vmcnt(57)
	v_mul_f32_e32 v5, 0x43800000, v86
	s_waitcnt vmcnt(56)
	v_mul_f32_e32 v6, 0x43800000, v90
	s_waitcnt vmcnt(55)
	v_mul_f32_e32 v3, 0x43800000, v92
	v_cvt_pk_fp8_f32 v1, v5, v6 op_sel:[0,0,1]
	s_waitcnt vmcnt(54)
	v_mul_f32_e32 v5, 0x43800000, v94
	v_mov_b32_e32 v2, 0
	v_cvt_pk_fp8_f32 v2, v3, v5
	s_waitcnt vmcnt(53)
	v_mul_f32_e32 v6, 0x43800000, v96
	s_waitcnt vmcnt(52)
	v_mul_f32_e32 v7, 0x43800000, v98
	s_waitcnt vmcnt(51)
	v_mul_f32_e32 v5, 0x43800000, v100
	v_cvt_pk_fp8_f32 v2, v6, v7 op_sel:[0,0,1]
	s_waitcnt vmcnt(50)
	v_mul_f32_e32 v6, 0x43800000, v102
	v_mov_b32_e32 v3, 0
	v_cvt_pk_fp8_f32 v3, v5, v6
	s_waitcnt vmcnt(49)
	v_mul_f32_e32 v7, 0x43800000, v104
	s_waitcnt vmcnt(48)
	v_mul_f32_e32 v159, 0x43800000, v106
	s_waitcnt vmcnt(44)
	v_mul_f32_e32 v5, 0x43800000, v114
	v_cvt_pk_fp8_f32 v3, v7, v159 op_sel:[0,0,1]
	s_waitcnt vmcnt(40)
	v_mul_f32_e32 v6, 0x43800000, v122
	s_waitcnt vmcnt(36)
	v_mul_f32_e32 v7, 0x43800000, v130
	s_waitcnt vmcnt(32)
	v_mul_f32_e32 v159, 0x43800000, v138
	ds_write_b128 v158, v[0:3]
	v_mul_f32_e32 v1, 0x43800000, v108
	v_mul_f32_e32 v2, 0x43800000, v110
	v_mov_b32_e32 v0, 0
	v_cvt_pk_fp8_f32 v0, v1, v2
	v_mul_f32_e32 v3, 0x43800000, v112
	v_mul_f32_e32 v2, 0x43800000, v116
	v_mov_b32_e32 v1, 0
	v_cvt_pk_fp8_f32 v0, v3, v5 op_sel:[0,0,1]
	v_mul_f32_e32 v3, 0x43800000, v118
	v_cvt_pk_fp8_f32 v1, v2, v3
	v_mul_f32_e32 v5, 0x43800000, v120
	v_mul_f32_e32 v3, 0x43800000, v124
	v_mov_b32_e32 v2, 0
	v_cvt_pk_fp8_f32 v1, v5, v6 op_sel:[0,0,1]
	v_mul_f32_e32 v5, 0x43800000, v126
	v_cvt_pk_fp8_f32 v2, v3, v5
	v_mul_f32_e32 v6, 0x43800000, v128
	v_mul_f32_e32 v5, 0x43800000, v132
	v_mov_b32_e32 v3, 0
	v_cvt_pk_fp8_f32 v2, v6, v7 op_sel:[0,0,1]
	v_mul_f32_e32 v6, 0x43800000, v134
	v_cvt_pk_fp8_f32 v3, v5, v6
	v_mul_f32_e32 v7, 0x43800000, v136
	v_or_b32_e32 v5, 1, v4
	s_mov_b64 s[44:45], 0
	v_cvt_pk_fp8_f32 v3, v7, v159 op_sel:[0,0,1]
.LBB0_479:
	s_andn2_b64 vcc, exec, s[44:45]
	s_cbranch_vccnz .LBB0_493
	s_waitcnt vmcnt(62)
	v_cvt_pk_bf16_f32 v0, v66, v68
	s_waitcnt vmcnt(60)
	v_cvt_pk_bf16_f32 v1, v70, v72
	s_waitcnt vmcnt(58)
	v_cvt_pk_bf16_f32 v2, v82, v84
	v_cndmask_b32_e64 v0, 0, v0, s[4:5]
	v_cndmask_b32_e64 v1, 0, v1, s[4:5]
	v_cndmask_b32_e64 v2, 0, v2, s[4:5]
	s_and_saveexec_b64 s[44:45], s[6:7]
	s_xor_b64 s[44:45], exec, s[44:45]
	v_xor_b32_e32 v4, v156, v143
	v_mov_b32_e32 v3, s15
	v_lshl_add_u32 v4, v4, 4, v146
	ds_write_b128 v4, v[0:3]
	s_or_saveexec_b64 s[44:45], s[44:45]
	v_mov_b32_e32 v4, 0
	s_xor_b64 exec, exec, s[44:45]
	s_cbranch_execz .LBB0_484
	v_xor_b32_e32 v4, v156, v143
	s_waitcnt vmcnt(56)
	v_cvt_pk_bf16_f32 v3, v86, v90
	v_lshl_add_u32 v4, v4, 4, v146
	ds_write_b128 v4, v[0:3]
	s_waitcnt vmcnt(54)
	v_cvt_pk_bf16_f32 v4, v92, v94
.LBB0_484:
	s_or_b64 exec, exec, s[44:45]
	s_waitcnt vmcnt(52)
	v_cvt_pk_bf16_f32 v0, v96, v98
	v_cndmask_b32_e64 v5, 0, v0, s[4:5]
	s_waitcnt vmcnt(50)
	v_cvt_pk_bf16_f32 v0, v100, v102
	v_cndmask_b32_e64 v6, 0, v0, s[4:5]
	s_and_saveexec_b64 s[44:45], s[6:7]
	s_xor_b64 s[44:45], exec, s[44:45]
	v_add_u32_e32 v0, 1, v156
	v_xor_b32_e32 v0, v0, v143
	v_mov_b32_e32 v7, s15
	v_lshl_add_u32 v0, v0, 4, v146
	ds_write_b128 v0, v[4:7]
	s_or_saveexec_b64 s[44:45], s[44:45]
	v_mov_b32_e32 v2, 0
	s_xor_b64 exec, exec, s[44:45]
	s_cbranch_execz .LBB0_488
	v_add_u32_e32 v0, 1, v156
	v_xor_b32_e32 v0, v0, v143
	s_waitcnt vmcnt(48)
	v_cvt_pk_bf16_f32 v7, v104, v106
	v_lshl_add_u32 v0, v0, 4, v146
	s_waitcnt vmcnt(46)
	v_cvt_pk_bf16_f32 v2, v108, v110
	ds_write_b128 v0, v[4:7]
.LBB0_488:
	s_or_b64 exec, exec, s[44:45]
	s_waitcnt vmcnt(44)
	v_cvt_pk_bf16_f32 v0, v112, v114
	v_cndmask_b32_e64 v3, 0, v0, s[4:5]
	s_waitcnt vmcnt(42)
	v_cvt_pk_bf16_f32 v0, v116, v118
	v_cndmask_b32_e64 v4, 0, v0, s[4:5]
	s_and_saveexec_b64 s[44:45], s[6:7]
	s_xor_b64 s[44:45], exec, s[44:45]
	v_add_u32_e32 v0, 2, v156
	v_xor_b32_e32 v0, v0, v143
	v_mov_b32_e32 v5, s15
	v_lshl_add_u32 v0, v0, 4, v146
	ds_write_b128 v0, v[2:5]
	s_or_saveexec_b64 s[44:45], s[44:45]
	v_mov_b32_e32 v0, 0
	s_xor_b64 exec, exec, s[44:45]
	s_cbranch_execz .LBB0_492
	v_add_u32_e32 v0, 2, v156
	v_xor_b32_e32 v0, v0, v143
	s_waitcnt vmcnt(40)
	v_cvt_pk_bf16_f32 v5, v120, v122
	v_lshl_add_u32 v0, v0, 4, v146
	ds_write_b128 v0, v[2:5]
	s_waitcnt vmcnt(38)
	v_cvt_pk_bf16_f32 v0, v124, v126
.LBB0_492:
	s_or_b64 exec, exec, s[44:45]
	s_waitcnt vmcnt(36)
	v_cvt_pk_bf16_f32 v1, v128, v130
	s_waitcnt vmcnt(34)
	v_cvt_pk_bf16_f32 v2, v132, v134
	s_waitcnt vmcnt(32)
	v_cvt_pk_bf16_f32 v3, v136, v138
	v_cndmask_b32_e64 v1, 0, v1, s[4:5]
	v_cndmask_b32_e64 v2, 0, v2, s[4:5]
	v_cndmask_b32_e64 v3, 0, v3, s[4:5]
	v_add_u32_e32 v5, 3, v156
.LBB0_493:
	v_xor_b32_e32 v4, v5, v143
	v_lshl_add_u32 v4, v4, 4, v146
	s_and_b64 vcc, exec, s[8:9]
	s_mov_b64 s[8:9], -1
	ds_write_b128 v4, v[0:3]
	s_cbranch_vccnz .LBB0_495
	s_waitcnt vmcnt(62)
	v_mul_f32_e32 v1, 0x43800000, v67
	s_waitcnt vmcnt(62)
	v_mul_f32_e32 v2, 0x43800000, v69
	v_mov_b32_e32 v0, 0
	v_cvt_pk_fp8_f32 v0, v1, v2
	s_waitcnt vmcnt(61)
	v_mul_f32_e32 v3, 0x43800000, v71
	s_waitcnt vmcnt(60)
	v_mul_f32_e32 v4, 0x43800000, v73
	s_waitcnt vmcnt(59)
	v_mul_f32_e32 v2, 0x43800000, v83
	v_cvt_pk_fp8_f32 v0, v3, v4 op_sel:[0,0,1]
	s_waitcnt vmcnt(58)
	v_mul_f32_e32 v3, 0x43800000, v85
	v_mov_b32_e32 v1, 0
	v_cvt_pk_fp8_f32 v1, v2, v3
	s_waitcnt vmcnt(57)
	v_mul_f32_e32 v4, 0x43800000, v87
	s_waitcnt vmcnt(56)
	v_mul_f32_e32 v5, 0x43800000, v91
	s_waitcnt vmcnt(55)
	v_mul_f32_e32 v3, 0x43800000, v93
	v_cvt_pk_fp8_f32 v1, v4, v5 op_sel:[0,0,1]
	s_waitcnt vmcnt(54)
	v_mul_f32_e32 v4, 0x43800000, v95
	v_mov_b32_e32 v2, 0
	v_cvt_pk_fp8_f32 v2, v3, v4
	s_waitcnt vmcnt(53)
	v_mul_f32_e32 v5, 0x43800000, v97
	s_waitcnt vmcnt(52)
	v_mul_f32_e32 v6, 0x43800000, v99
	s_waitcnt vmcnt(51)
	v_mul_f32_e32 v4, 0x43800000, v101
	v_cvt_pk_fp8_f32 v2, v5, v6 op_sel:[0,0,1]
	s_waitcnt vmcnt(50)
	v_mul_f32_e32 v5, 0x43800000, v103
	v_mov_b32_e32 v3, 0
	v_cvt_pk_fp8_f32 v3, v4, v5
	s_waitcnt vmcnt(49)
	v_mul_f32_e32 v6, 0x43800000, v105
	s_waitcnt vmcnt(48)
	v_mul_f32_e32 v7, 0x43800000, v107
	s_waitcnt vmcnt(44)
	v_mul_f32_e32 v4, 0x43800000, v115
	v_cvt_pk_fp8_f32 v3, v6, v7 op_sel:[0,0,1]
	s_waitcnt vmcnt(40)
	v_mul_f32_e32 v5, 0x43800000, v123
	s_waitcnt vmcnt(36)
	v_mul_f32_e32 v6, 0x43800000, v131
	s_waitcnt vmcnt(32)
	v_mul_f32_e32 v7, 0x43800000, v139
	ds_write_b128 v158, v[0:3] offset:512
	v_mul_f32_e32 v1, 0x43800000, v109
	v_mul_f32_e32 v2, 0x43800000, v111
	v_mov_b32_e32 v0, 0
	v_cvt_pk_fp8_f32 v0, v1, v2
	v_mul_f32_e32 v3, 0x43800000, v113
	v_mul_f32_e32 v2, 0x43800000, v117
	v_mov_b32_e32 v1, 0
	v_cvt_pk_fp8_f32 v0, v3, v4 op_sel:[0,0,1]
	v_mul_f32_e32 v3, 0x43800000, v119
	v_cvt_pk_fp8_f32 v1, v2, v3
	v_mul_f32_e32 v4, 0x43800000, v121
	v_mul_f32_e32 v3, 0x43800000, v125
	v_mov_b32_e32 v2, 0
	v_cvt_pk_fp8_f32 v1, v4, v5 op_sel:[0,0,1]
	v_mul_f32_e32 v4, 0x43800000, v127
	v_cvt_pk_fp8_f32 v2, v3, v4
	v_mul_f32_e32 v5, 0x43800000, v129
	v_mul_f32_e32 v4, 0x43800000, v133
	v_mov_b32_e32 v3, 0
	v_cvt_pk_fp8_f32 v2, v5, v6 op_sel:[0,0,1]
	v_mul_f32_e32 v5, 0x43800000, v135
	v_cvt_pk_fp8_f32 v3, v4, v5
	v_mul_f32_e32 v6, 0x43800000, v137
	s_mov_b64 s[8:9], 0
	v_cvt_pk_fp8_f32 v3, v6, v7 op_sel:[0,0,1]
.LBB0_495:
	s_andn2_b64 vcc, exec, s[8:9]
	s_cbranch_vccnz .LBB0_509
	s_waitcnt vmcnt(62)
	v_cvt_pk_bf16_f32 v0, v67, v69
	s_waitcnt vmcnt(60)
	v_cvt_pk_bf16_f32 v1, v71, v73
	s_waitcnt vmcnt(58)
	v_cvt_pk_bf16_f32 v2, v83, v85
	v_xor_b32_e32 v3, v156, v143
	v_cndmask_b32_e64 v0, 0, v0, s[4:5]
	v_cndmask_b32_e64 v1, 0, v1, s[4:5]
	v_cndmask_b32_e64 v2, 0, v2, s[4:5]
	v_lshl_add_u32 v5, v3, 4, v146
	s_and_saveexec_b64 s[8:9], s[6:7]
	s_xor_b64 s[8:9], exec, s[8:9]
	v_mov_b32_e32 v3, s15
	ds_write_b128 v5, v[0:3] offset:512
	s_or_saveexec_b64 s[8:9], s[8:9]
	v_mov_b32_e32 v4, 0
	s_xor_b64 exec, exec, s[8:9]
	s_cbranch_execz .LBB0_500
	s_waitcnt vmcnt(56)
	v_cvt_pk_bf16_f32 v3, v87, v91
	s_waitcnt vmcnt(54)
	v_cvt_pk_bf16_f32 v4, v93, v95
	ds_write_b128 v5, v[0:3] offset:512
.LBB0_500:
	s_or_b64 exec, exec, s[8:9]
	s_waitcnt vmcnt(52)
	v_cvt_pk_bf16_f32 v0, v97, v99
	v_cndmask_b32_e64 v5, 0, v0, s[4:5]
	s_waitcnt vmcnt(50)
	v_cvt_pk_bf16_f32 v0, v101, v103
	v_cndmask_b32_e64 v6, 0, v0, s[4:5]
	v_add_u32_e32 v0, 1, v156
	v_xor_b32_e32 v0, v0, v143
	s_and_saveexec_b64 s[8:9], s[6:7]
	s_xor_b64 s[8:9], exec, s[8:9]
	v_mov_b32_e32 v7, s15
	v_lshl_add_u32 v0, v0, 4, v146
	ds_write_b128 v0, v[4:7] offset:512
	s_or_saveexec_b64 s[8:9], s[8:9]
	v_mov_b32_e32 v2, 0
	s_xor_b64 exec, exec, s[8:9]
	s_cbranch_execz .LBB0_504
	s_waitcnt vmcnt(48)
	v_cvt_pk_bf16_f32 v7, v105, v107
	v_lshl_add_u32 v0, v0, 4, v146
	s_waitcnt vmcnt(46)
	v_cvt_pk_bf16_f32 v2, v109, v111
	ds_write_b128 v0, v[4:7] offset:512
.LBB0_504:
	s_or_b64 exec, exec, s[8:9]
	s_waitcnt vmcnt(44)
	v_cvt_pk_bf16_f32 v0, v113, v115
	v_cndmask_b32_e64 v3, 0, v0, s[4:5]
	s_waitcnt vmcnt(42)
	v_cvt_pk_bf16_f32 v0, v117, v119
	v_cndmask_b32_e64 v4, 0, v0, s[4:5]
	v_add_u32_e32 v0, 2, v156
	v_xor_b32_e32 v1, v0, v143
	s_and_saveexec_b64 s[8:9], s[6:7]
	s_xor_b64 s[8:9], exec, s[8:9]
	v_mov_b32_e32 v5, s15
	v_lshl_add_u32 v0, v1, 4, v146
	ds_write_b128 v0, v[2:5] offset:512
	s_or_saveexec_b64 s[8:9], s[8:9]
	v_mov_b32_e32 v0, 0
	s_xor_b64 exec, exec, s[8:9]
	s_cbranch_execz .LBB0_508
	s_waitcnt vmcnt(40)
	v_cvt_pk_bf16_f32 v5, v121, v123
	v_lshl_add_u32 v0, v1, 4, v146
	ds_write_b128 v0, v[2:5] offset:512
	s_waitcnt vmcnt(38)
	v_cvt_pk_bf16_f32 v0, v125, v127
.LBB0_508:
	s_or_b64 exec, exec, s[8:9]
	s_waitcnt vmcnt(36)
	v_cvt_pk_bf16_f32 v1, v129, v131
	s_waitcnt vmcnt(34)
	v_cvt_pk_bf16_f32 v2, v133, v135
	s_waitcnt vmcnt(32)
	v_cvt_pk_bf16_f32 v3, v137, v139
	v_cndmask_b32_e64 v1, 0, v1, s[4:5]
	v_cndmask_b32_e64 v2, 0, v2, s[4:5]
	v_cndmask_b32_e64 v3, 0, v3, s[4:5]
	v_add_u32_e32 v157, 3, v156

.Lcv_drain_0:
	s_waitcnt vmcnt(0)
	s_branch .LBB0_477

.LBB0_725:
	s_and_b32 s0, s16, 1
	s_mul_i32 s1, s0, 0xa000
	v_add_u32_e32 v8, s1, v4
	s_lshl_b32 s14, s0, 11
	v_add_u32_e32 v9, s14, v5
	s_add_i32 s16, s16, 1
	ds_read_b128 v[12:15], v8 offset:0
	ds_read_b128 v[16:19], v8 offset:256
	ds_read_b128 v[20:23], v8 offset:512
	ds_read_b128 v[24:27], v8 offset:768
	ds_read2_b32 v[72:73], v9 offset1:16
	ds_read_b128 v[32:35], v8 offset:1280
	ds_read_b128 v[36:39], v8 offset:1536
	ds_read_b128 v[40:43], v8 offset:1792
	ds_read_b128 v[44:47], v8 offset:2048
	v_add_u32_e32 v10, 0x400, v9
	v_add_u32_e32 v11, s14, v6
	ds_read_b128 v[28:31], v8 offset:1024
	ds_read_b128 v[48:51], v8 offset:2304
	s_waitcnt lgkmcnt(6)
	v_pk_mul_f32 v[76:77], v[24:25], v[72:73] op_sel_hi:[1,0]
	v_pk_mul_f32 v[78:79], v[26:27], v[72:73] op_sel_hi:[1,0]
	v_pk_mul_f32 v[84:85], v[0:1], v[12:13]
	ds_read_b128 v[52:55], v8 offset:2560
	ds_read_b128 v[56:59], v8 offset:2816
	v_pk_fma_f32 v[84:85], v[2:3], v[14:15], v[84:85]
	v_pk_fma_f32 v[76:77], v[0:1], v[16:17], v[76:77]
	v_add_f32_e32 v86, v84, v85
	v_pk_fma_f32 v[78:79], v[2:3], v[18:19], v[78:79]
	ds_read_b128 v[68:71], v8 offset:3584
	v_add_f32_dpp v86, v86, v86 quad_perm:[1,0,3,2] row_mask:0xf bank_mask:0xf bound_ctrl:1
	ds_read_b128 v[60:63], v8 offset:3072
	ds_read_b128 v[64:67], v8 offset:3328
	v_add_f32_dpp v86, v86, v86 quad_perm:[2,3,0,1] row_mask:0xf bank_mask:0xf bound_ctrl:1
	ds_read2_b32 v[74:75], v9 offset0:32 offset1:48
	s_waitcnt lgkmcnt(8)
	v_pk_mul_f32 v[80:81], v[44:45], v[72:73] op_sel:[0,1] op_sel_hi:[1,1]
	v_add_f32_dpp v86, v86, v86 row_half_mirror row_mask:0xf bank_mask:0xf bound_ctrl:1
	v_pk_mul_f32 v[82:83], v[46:47], v[72:73] op_sel:[0,1] op_sel_hi:[1,1]
	ds_read_b128 v[12:15], v8 offset:3840
	v_add_f32_dpp v86, v86, v86 row_mirror row_mask:0xf bank_mask:0xf bound_ctrl:1
	ds_read_b128 v[16:19], v8 offset:4096
	v_pk_fma_f32 v[0:1], v[20:21], v[86:87], v[76:77] op_sel_hi:[1,0,1]
	v_pk_fma_f32 v[2:3], v[22:23], v[86:87], v[78:79] op_sel_hi:[1,0,1]
	v_pk_mul_f32 v[84:85], v[0:1], v[32:33]
	v_pk_fma_f32 v[80:81], v[0:1], v[36:37], v[80:81]
	v_pk_fma_f32 v[84:85], v[2:3], v[34:35], v[84:85]
	s_waitcnt lgkmcnt(9)
	v_pk_mul_f32 v[88:89], v[0:1], v[28:29]
	v_add_f32_e32 v86, v84, v85
	v_pk_fma_f32 v[82:83], v[2:3], v[38:39], v[82:83]
	v_pk_fma_f32 v[88:89], v[2:3], v[30:31], v[88:89]
	v_add_f32_dpp v86, v86, v86 quad_perm:[1,0,3,2] row_mask:0xf bank_mask:0xf bound_ctrl:1
	ds_read_b128 v[28:31], v8 offset:4864
	v_add_f32_e32 v90, v88, v89
	v_add_f32_dpp v86, v86, v86 quad_perm:[2,3,0,1] row_mask:0xf bank_mask:0xf bound_ctrl:1
	ds_read_b128 v[20:23], v8 offset:4352
	ds_read_b128 v[24:27], v8 offset:4608
	v_add_f32_dpp v86, v86, v86 row_half_mirror row_mask:0xf bank_mask:0xf bound_ctrl:1
	s_waitcnt lgkmcnt(5)
	v_pk_mul_f32 v[76:77], v[64:65], v[74:75] op_sel_hi:[1,0]
	v_pk_mul_f32 v[78:79], v[66:67], v[74:75] op_sel_hi:[1,0]
	v_add_f32_dpp v86, v86, v86 row_mirror row_mask:0xf bank_mask:0xf bound_ctrl:1
	ds_read_b128 v[32:35], v8 offset:5120
	v_pk_fma_f32 v[0:1], v[40:41], v[86:87], v[80:81] op_sel_hi:[1,0,1]
	v_pk_fma_f32 v[2:3], v[42:43], v[86:87], v[82:83] op_sel_hi:[1,0,1]
	v_pk_mul_f32 v[84:85], v[0:1], v[52:53]
	ds_read_b128 v[36:39], v8 offset:5376
	v_pk_fma_f32 v[84:85], v[2:3], v[54:55], v[84:85]
	v_pk_fma_f32 v[76:77], v[0:1], v[56:57], v[76:77]
	v_add_f32_e32 v86, v84, v85
	v_pk_mul_f32 v[88:89], v[0:1], v[48:49]
	v_pk_fma_f32 v[78:79], v[2:3], v[58:59], v[78:79]
	v_add_f32_dpp v86, v86, v86 quad_perm:[1,0,3,2] row_mask:0xf bank_mask:0xf bound_ctrl:1
	v_pk_fma_f32 v[88:89], v[2:3], v[50:51], v[88:89]
	ds_read_b128 v[48:51], v8 offset:6144
	v_add_f32_dpp v86, v86, v86 quad_perm:[2,3,0,1] row_mask:0xf bank_mask:0xf bound_ctrl:1
	v_add_f32_e32 v91, v88, v89
	ds_read_b128 v[40:43], v8 offset:5632
	v_add_f32_dpp v86, v86, v86 row_half_mirror row_mask:0xf bank_mask:0xf bound_ctrl:1
	ds_read_b128 v[44:47], v8 offset:5888
	ds_read2_b32 v[72:73], v9 offset0:64 offset1:80
	v_add_f32_dpp v86, v86, v86 row_mirror row_mask:0xf bank_mask:0xf bound_ctrl:1
	s_waitcnt lgkmcnt(6)
	v_pk_mul_f32 v[80:81], v[24:25], v[74:75] op_sel:[0,1] op_sel_hi:[1,1]
	v_pk_mul_f32 v[82:83], v[26:27], v[74:75] op_sel:[0,1] op_sel_hi:[1,1]
	v_pk_fma_f32 v[0:1], v[60:61], v[86:87], v[76:77] op_sel_hi:[1,0,1]
	v_pk_fma_f32 v[2:3], v[62:63], v[86:87], v[78:79] op_sel_hi:[1,0,1]
	v_pk_mul_f32 v[84:85], v[0:1], v[12:13]
	ds_read_b128 v[52:55], v8 offset:6400
	ds_read_b128 v[56:59], v8 offset:6656
	v_pk_fma_f32 v[84:85], v[2:3], v[14:15], v[84:85]
	v_pk_fma_f32 v[80:81], v[0:1], v[16:17], v[80:81]
	v_add_f32_e32 v86, v84, v85
	v_pk_mul_f32 v[88:89], v[0:1], v[68:69]
	v_pk_fma_f32 v[82:83], v[2:3], v[18:19], v[82:83]
	v_add_f32_dpp v86, v86, v86 quad_perm:[1,0,3,2] row_mask:0xf bank_mask:0xf bound_ctrl:1
	v_pk_fma_f32 v[88:89], v[2:3], v[70:71], v[88:89]
	ds_read_b128 v[68:71], v8 offset:7424
	v_add_f32_dpp v86, v86, v86 quad_perm:[2,3,0,1] row_mask:0xf bank_mask:0xf bound_ctrl:1
	v_add_f32_e32 v92, v88, v89
	ds_read_b128 v[60:63], v8 offset:6912
	v_add_f32_dpp v86, v86, v86 row_half_mirror row_mask:0xf bank_mask:0xf bound_ctrl:1
	ds_read_b128 v[64:67], v8 offset:7168
	s_waitcnt lgkmcnt(5)
	v_pk_mul_f32 v[76:77], v[44:45], v[72:73] op_sel_hi:[1,0]
	v_add_f32_dpp v86, v86, v86 row_mirror row_mask:0xf bank_mask:0xf bound_ctrl:1
	v_pk_mul_f32 v[78:79], v[46:47], v[72:73] op_sel_hi:[1,0]
	v_pk_fma_f32 v[0:1], v[20:21], v[86:87], v[80:81] op_sel_hi:[1,0,1]
	v_pk_fma_f32 v[2:3], v[22:23], v[86:87], v[82:83] op_sel_hi:[1,0,1]
	v_pk_mul_f32 v[84:85], v[0:1], v[32:33]
	ds_read_b128 v[12:15], v8 offset:7680
	ds_read_b128 v[16:19], v8 offset:7936
	v_pk_fma_f32 v[84:85], v[2:3], v[34:35], v[84:85]
	v_pk_fma_f32 v[76:77], v[0:1], v[36:37], v[76:77]
	v_add_f32_e32 v86, v84, v85
	v_pk_mul_f32 v[88:89], v[0:1], v[28:29]
	v_pk_fma_f32 v[78:79], v[2:3], v[38:39], v[78:79]
	v_add_f32_dpp v86, v86, v86 quad_perm:[1,0,3,2] row_mask:0xf bank_mask:0xf bound_ctrl:1
	v_pk_fma_f32 v[88:89], v[2:3], v[30:31], v[88:89]
	ds_read_b128 v[28:31], v8 offset:8704
	v_add_f32_dpp v86, v86, v86 quad_perm:[2,3,0,1] row_mask:0xf bank_mask:0xf bound_ctrl:1
	v_add_f32_e32 v93, v88, v89
	ds_read_b128 v[20:23], v8 offset:8192
	v_add_f32_dpp v86, v86, v86 row_half_mirror row_mask:0xf bank_mask:0xf bound_ctrl:1
	ds_read_b128 v[24:27], v8 offset:8448
	ds_read2_b32 v[74:75], v9 offset0:96 offset1:112
	v_add_f32_dpp v86, v86, v86 row_mirror row_mask:0xf bank_mask:0xf bound_ctrl:1
	s_waitcnt lgkmcnt(6)
	v_pk_mul_f32 v[80:81], v[64:65], v[72:73] op_sel:[0,1] op_sel_hi:[1,1]
	v_pk_mul_f32 v[82:83], v[66:67], v[72:73] op_sel:[0,1] op_sel_hi:[1,1]
	v_pk_fma_f32 v[0:1], v[40:41], v[86:87], v[76:77] op_sel_hi:[1,0,1]
	v_pk_fma_f32 v[2:3], v[42:43], v[86:87], v[78:79] op_sel_hi:[1,0,1]
	v_pk_mul_f32 v[84:85], v[0:1], v[52:53]
	ds_read_b128 v[32:35], v8 offset:8960
	ds_read_b128 v[36:39], v8 offset:9216
	v_pk_fma_f32 v[84:85], v[2:3], v[54:55], v[84:85]
	v_pk_fma_f32 v[80:81], v[0:1], v[56:57], v[80:81]
	v_add_f32_e32 v86, v84, v85
	v_pk_mul_f32 v[88:89], v[0:1], v[48:49]
	v_pk_fma_f32 v[82:83], v[2:3], v[58:59], v[82:83]
	v_add_f32_dpp v86, v86, v86 quad_perm:[1,0,3,2] row_mask:0xf bank_mask:0xf bound_ctrl:1
	v_pk_fma_f32 v[88:89], v[2:3], v[50:51], v[88:89]
	ds_read_b128 v[48:51], v8 offset:9984
	v_add_f32_dpp v86, v86, v86 quad_perm:[2,3,0,1] row_mask:0xf bank_mask:0xf bound_ctrl:1
	v_add_f32_e32 v94, v88, v89
	ds_read_b128 v[40:43], v8 offset:9472
	v_add_f32_dpp v86, v86, v86 row_half_mirror row_mask:0xf bank_mask:0xf bound_ctrl:1
	ds_read_b128 v[44:47], v8 offset:9728
	s_waitcnt lgkmcnt(5)
	v_pk_mul_f32 v[76:77], v[24:25], v[74:75] op_sel_hi:[1,0]
	v_add_f32_dpp v86, v86, v86 row_mirror row_mask:0xf bank_mask:0xf bound_ctrl:1
	v_pk_mul_f32 v[78:79], v[26:27], v[74:75] op_sel_hi:[1,0]
	v_pk_fma_f32 v[0:1], v[60:61], v[86:87], v[80:81] op_sel_hi:[1,0,1]
	v_pk_fma_f32 v[2:3], v[62:63], v[86:87], v[82:83] op_sel_hi:[1,0,1]
	v_pk_mul_f32 v[84:85], v[0:1], v[12:13]
	ds_read_b128 v[52:55], v8 offset:10240
	ds_read_b128 v[56:59], v8 offset:10496
	v_pk_fma_f32 v[84:85], v[2:3], v[14:15], v[84:85]
	v_pk_fma_f32 v[76:77], v[0:1], v[16:17], v[76:77]
	v_add_f32_e32 v86, v84, v85
	v_pk_mul_f32 v[88:89], v[0:1], v[68:69]
	v_pk_fma_f32 v[78:79], v[2:3], v[18:19], v[78:79]
	v_add_f32_dpp v86, v86, v86 quad_perm:[1,0,3,2] row_mask:0xf bank_mask:0xf bound_ctrl:1
	v_pk_fma_f32 v[88:89], v[2:3], v[70:71], v[88:89]
	ds_read_b128 v[68:71], v8 offset:11264
	v_add_f32_dpp v86, v86, v86 quad_perm:[2,3,0,1] row_mask:0xf bank_mask:0xf bound_ctrl:1
	v_add_f32_e32 v95, v88, v89
	ds_read_b128 v[60:63], v8 offset:10752
	v_add_f32_dpp v86, v86, v86 row_half_mirror row_mask:0xf bank_mask:0xf bound_ctrl:1
	ds_read_b128 v[64:67], v8 offset:11008
	ds_read2_b32 v[72:73], v9 offset0:128 offset1:144
	v_add_f32_dpp v86, v86, v86 row_mirror row_mask:0xf bank_mask:0xf bound_ctrl:1
	s_waitcnt lgkmcnt(6)
	v_pk_mul_f32 v[80:81], v[44:45], v[74:75] op_sel:[0,1] op_sel_hi:[1,1]
	v_pk_mul_f32 v[82:83], v[46:47], v[74:75] op_sel:[0,1] op_sel_hi:[1,1]
	v_pk_fma_f32 v[0:1], v[20:21], v[86:87], v[76:77] op_sel_hi:[1,0,1]
	v_pk_fma_f32 v[2:3], v[22:23], v[86:87], v[78:79] op_sel_hi:[1,0,1]
	v_pk_mul_f32 v[84:85], v[0:1], v[32:33]
	ds_read_b128 v[12:15], v8 offset:11520
	ds_read_b128 v[16:19], v8 offset:11776
	v_pk_fma_f32 v[84:85], v[2:3], v[34:35], v[84:85]
	v_pk_fma_f32 v[80:81], v[0:1], v[36:37], v[80:81]
	v_add_f32_e32 v86, v84, v85
	v_pk_mul_f32 v[88:89], v[0:1], v[28:29]
	v_pk_fma_f32 v[82:83], v[2:3], v[38:39], v[82:83]
	v_add_f32_dpp v86, v86, v86 quad_perm:[1,0,3,2] row_mask:0xf bank_mask:0xf bound_ctrl:1
	v_pk_fma_f32 v[88:89], v[2:3], v[30:31], v[88:89]
	ds_read_b128 v[28:31], v8 offset:12544
	v_add_f32_dpp v86, v86, v86 quad_perm:[2,3,0,1] row_mask:0xf bank_mask:0xf bound_ctrl:1
	v_add_f32_e32 v96, v88, v89
	ds_read_b128 v[20:23], v8 offset:12032
	v_add_f32_dpp v86, v86, v86 row_half_mirror row_mask:0xf bank_mask:0xf bound_ctrl:1
	ds_read_b128 v[24:27], v8 offset:12288
	s_waitcnt lgkmcnt(5)
	v_pk_mul_f32 v[76:77], v[64:65], v[72:73] op_sel_hi:[1,0]
	v_add_f32_dpp v86, v86, v86 row_mirror row_mask:0xf bank_mask:0xf bound_ctrl:1
	v_pk_mul_f32 v[78:79], v[66:67], v[72:73] op_sel_hi:[1,0]
	v_pk_fma_f32 v[0:1], v[40:41], v[86:87], v[80:81] op_sel_hi:[1,0,1]
	v_pk_fma_f32 v[2:3], v[42:43], v[86:87], v[82:83] op_sel_hi:[1,0,1]
	v_pk_mul_f32 v[84:85], v[0:1], v[52:53]
	ds_read_b128 v[32:35], v8 offset:12800
	ds_read_b128 v[36:39], v8 offset:13056
	v_pk_fma_f32 v[84:85], v[2:3], v[54:55], v[84:85]
	v_pk_fma_f32 v[76:77], v[0:1], v[56:57], v[76:77]
	v_add_f32_e32 v86, v84, v85
	v_pk_mul_f32 v[88:89], v[0:1], v[48:49]
	v_pk_fma_f32 v[78:79], v[2:3], v[58:59], v[78:79]
	v_add_f32_dpp v86, v86, v86 quad_perm:[1,0,3,2] row_mask:0xf bank_mask:0xf bound_ctrl:1
	v_pk_fma_f32 v[88:89], v[2:3], v[50:51], v[88:89]
	ds_read_b128 v[48:51], v8 offset:13824
	v_add_f32_dpp v86, v86, v86 quad_perm:[2,3,0,1] row_mask:0xf bank_mask:0xf bound_ctrl:1
	v_add_f32_e32 v97, v88, v89
	ds_read_b128 v[40:43], v8 offset:13312
	v_add_f32_dpp v86, v86, v86 row_half_mirror row_mask:0xf bank_mask:0xf bound_ctrl:1
	ds_read_b128 v[44:47], v8 offset:13568
	ds_read2_b32 v[74:75], v9 offset0:160 offset1:176
	v_add_f32_dpp v86, v86, v86 row_mirror row_mask:0xf bank_mask:0xf bound_ctrl:1
	s_waitcnt lgkmcnt(6)
	v_pk_mul_f32 v[80:81], v[24:25], v[72:73] op_sel:[0,1] op_sel_hi:[1,1]
	v_pk_mul_f32 v[82:83], v[26:27], v[72:73] op_sel:[0,1] op_sel_hi:[1,1]
	v_pk_fma_f32 v[0:1], v[60:61], v[86:87], v[76:77] op_sel_hi:[1,0,1]
	v_pk_fma_f32 v[2:3], v[62:63], v[86:87], v[78:79] op_sel_hi:[1,0,1]
	v_pk_mul_f32 v[84:85], v[0:1], v[12:13]
	ds_read_b128 v[52:55], v8 offset:14080
	ds_read_b128 v[56:59], v8 offset:14336
	v_pk_fma_f32 v[84:85], v[2:3], v[14:15], v[84:85]
	v_pk_fma_f32 v[80:81], v[0:1], v[16:17], v[80:81]
	v_add_f32_e32 v86, v84, v85
	v_pk_mul_f32 v[88:89], v[0:1], v[68:69]
	v_pk_fma_f32 v[82:83], v[2:3], v[18:19], v[82:83]
	v_add_f32_dpp v86, v86, v86 quad_perm:[1,0,3,2] row_mask:0xf bank_mask:0xf bound_ctrl:1
	v_pk_fma_f32 v[88:89], v[2:3], v[70:71], v[88:89]
	ds_read_b128 v[68:71], v8 offset:15104
	v_add_f32_dpp v86, v86, v86 quad_perm:[2,3,0,1] row_mask:0xf bank_mask:0xf bound_ctrl:1
	v_add_f32_e32 v98, v88, v89
	ds_read_b128 v[60:63], v8 offset:14592
	v_add_f32_dpp v86, v86, v86 row_half_mirror row_mask:0xf bank_mask:0xf bound_ctrl:1
	ds_read_b128 v[64:67], v8 offset:14848
	s_waitcnt lgkmcnt(5)
	v_pk_mul_f32 v[76:77], v[44:45], v[74:75] op_sel_hi:[1,0]
	v_add_f32_dpp v86, v86, v86 row_mirror row_mask:0xf bank_mask:0xf bound_ctrl:1
	v_pk_mul_f32 v[78:79], v[46:47], v[74:75] op_sel_hi:[1,0]
	v_pk_fma_f32 v[0:1], v[20:21], v[86:87], v[80:81] op_sel_hi:[1,0,1]
	v_pk_fma_f32 v[2:3], v[22:23], v[86:87], v[82:83] op_sel_hi:[1,0,1]
	v_pk_mul_f32 v[84:85], v[0:1], v[32:33]
	ds_read_b128 v[12:15], v8 offset:15360
	ds_read_b128 v[16:19], v8 offset:15616
	v_pk_fma_f32 v[84:85], v[2:3], v[34:35], v[84:85]
	v_pk_fma_f32 v[76:77], v[0:1], v[36:37], v[76:77]
	v_cndmask_b32_e64 v122, v98, v90, s[4:5]
	v_add_f32_e32 v86, v84, v85
	v_pk_mul_f32 v[88:89], v[0:1], v[28:29]
	v_pk_fma_f32 v[78:79], v[2:3], v[38:39], v[78:79]
	v_add_f32_dpp v86, v86, v86 quad_perm:[1,0,3,2] row_mask:0xf bank_mask:0xf bound_ctrl:1
	v_pk_fma_f32 v[88:89], v[2:3], v[30:31], v[88:89]
	ds_read_b128 v[28:31], v8 offset:16384
	v_add_f32_dpp v86, v86, v86 quad_perm:[2,3,0,1] row_mask:0xf bank_mask:0xf bound_ctrl:1
	v_add_f32_e32 v99, v88, v89
	ds_read_b128 v[20:23], v8 offset:15872
	v_add_f32_dpp v86, v86, v86 row_half_mirror row_mask:0xf bank_mask:0xf bound_ctrl:1
	ds_read_b128 v[24:27], v8 offset:16128
	ds_read2_b32 v[72:73], v9 offset0:192 offset1:208
	v_cndmask_b32_e64 v123, v90, v98, s[4:5]
	v_add_f32_dpp v86, v86, v86 row_mirror row_mask:0xf bank_mask:0xf bound_ctrl:1
	s_waitcnt lgkmcnt(6)
	v_pk_mul_f32 v[80:81], v[64:65], v[74:75] op_sel:[0,1] op_sel_hi:[1,1]
	v_pk_mul_f32 v[82:83], v[66:67], v[74:75] op_sel:[0,1] op_sel_hi:[1,1]
	v_pk_fma_f32 v[0:1], v[40:41], v[86:87], v[76:77] op_sel_hi:[1,0,1]
	v_pk_fma_f32 v[2:3], v[42:43], v[86:87], v[78:79] op_sel_hi:[1,0,1]
	v_add_f32_dpp v90, v123, v122 row_mirror row_mask:0xf bank_mask:0xf bound_ctrl:1
	v_pk_mul_f32 v[84:85], v[0:1], v[52:53]
	ds_read_b128 v[32:35], v8 offset:16640
	ds_read_b128 v[36:39], v8 offset:16896
	v_pk_fma_f32 v[84:85], v[2:3], v[54:55], v[84:85]
	v_pk_fma_f32 v[80:81], v[0:1], v[56:57], v[80:81]
	v_cndmask_b32_e64 v124, v99, v91, s[4:5]
	v_add_f32_e32 v86, v84, v85
	v_pk_mul_f32 v[88:89], v[0:1], v[48:49]
	v_pk_fma_f32 v[82:83], v[2:3], v[58:59], v[82:83]
	v_add_f32_dpp v86, v86, v86 quad_perm:[1,0,3,2] row_mask:0xf bank_mask:0xf bound_ctrl:1
	v_pk_fma_f32 v[88:89], v[2:3], v[50:51], v[88:89]
	ds_read_b128 v[48:51], v8 offset:17664
	v_add_f32_dpp v86, v86, v86 quad_perm:[2,3,0,1] row_mask:0xf bank_mask:0xf bound_ctrl:1
	v_add_f32_e32 v100, v88, v89
	ds_read_b128 v[40:43], v8 offset:17152
	v_add_f32_dpp v86, v86, v86 row_half_mirror row_mask:0xf bank_mask:0xf bound_ctrl:1
	ds_read_b128 v[44:47], v8 offset:17408
	v_cndmask_b32_e64 v125, v91, v99, s[4:5]
	v_add_f32_dpp v86, v86, v86 row_mirror row_mask:0xf bank_mask:0xf bound_ctrl:1
	s_waitcnt lgkmcnt(5)
	v_pk_mul_f32 v[76:77], v[24:25], v[72:73] op_sel_hi:[1,0]
	v_pk_mul_f32 v[78:79], v[26:27], v[72:73] op_sel_hi:[1,0]
	v_pk_fma_f32 v[0:1], v[60:61], v[86:87], v[80:81] op_sel_hi:[1,0,1]
	v_pk_fma_f32 v[2:3], v[62:63], v[86:87], v[82:83] op_sel_hi:[1,0,1]
	v_add_f32_dpp v91, v125, v124 row_mirror row_mask:0xf bank_mask:0xf bound_ctrl:1
	v_pk_mul_f32 v[84:85], v[0:1], v[12:13]
	ds_read_b128 v[52:55], v8 offset:17920
	ds_read_b128 v[56:59], v8 offset:18176
	v_pk_fma_f32 v[84:85], v[2:3], v[14:15], v[84:85]
	v_pk_fma_f32 v[76:77], v[0:1], v[16:17], v[76:77]
	v_cndmask_b32_e64 v126, v100, v92, s[4:5]
	v_add_f32_e32 v86, v84, v85
	v_pk_mul_f32 v[88:89], v[0:1], v[68:69]
	v_pk_fma_f32 v[78:79], v[2:3], v[18:19], v[78:79]
	v_add_f32_dpp v86, v86, v86 quad_perm:[1,0,3,2] row_mask:0xf bank_mask:0xf bound_ctrl:1
	v_pk_fma_f32 v[88:89], v[2:3], v[70:71], v[88:89]
	ds_read_b128 v[68:71], v8 offset:18944
	v_add_f32_dpp v86, v86, v86 quad_perm:[2,3,0,1] row_mask:0xf bank_mask:0xf bound_ctrl:1
	v_add_f32_e32 v101, v88, v89
	ds_read_b128 v[60:63], v8 offset:18432
	v_add_f32_dpp v86, v86, v86 row_half_mirror row_mask:0xf bank_mask:0xf bound_ctrl:1
	ds_read_b128 v[64:67], v8 offset:18688
	ds_read2_b32 v[74:75], v9 offset0:224 offset1:240
	v_cndmask_b32_e64 v127, v92, v100, s[4:5]
	v_add_f32_dpp v86, v86, v86 row_mirror row_mask:0xf bank_mask:0xf bound_ctrl:1
	s_waitcnt lgkmcnt(6)
	v_pk_mul_f32 v[80:81], v[44:45], v[72:73] op_sel:[0,1] op_sel_hi:[1,1]
	v_pk_mul_f32 v[82:83], v[46:47], v[72:73] op_sel:[0,1] op_sel_hi:[1,1]
	v_pk_fma_f32 v[0:1], v[20:21], v[86:87], v[76:77] op_sel_hi:[1,0,1]
	v_pk_fma_f32 v[2:3], v[22:23], v[86:87], v[78:79] op_sel_hi:[1,0,1]
	v_add_f32_dpp v92, v127, v126 row_mirror row_mask:0xf bank_mask:0xf bound_ctrl:1
	v_pk_mul_f32 v[84:85], v[0:1], v[32:33]
	ds_read_b128 v[12:15], v8 offset:19200
	ds_read_b128 v[16:19], v8 offset:19456
	v_pk_fma_f32 v[84:85], v[2:3], v[34:35], v[84:85]
	v_pk_fma_f32 v[80:81], v[0:1], v[36:37], v[80:81]
	v_cndmask_b32_e64 v128, v101, v93, s[4:5]
	v_add_f32_e32 v86, v84, v85
	v_pk_mul_f32 v[88:89], v[0:1], v[28:29]
	v_pk_fma_f32 v[82:83], v[2:3], v[38:39], v[82:83]
	v_add_f32_dpp v86, v86, v86 quad_perm:[1,0,3,2] row_mask:0xf bank_mask:0xf bound_ctrl:1
	v_pk_fma_f32 v[88:89], v[2:3], v[30:31], v[88:89]
	ds_read_b128 v[28:31], v8 offset:20224
	v_add_f32_dpp v86, v86, v86 quad_perm:[2,3,0,1] row_mask:0xf bank_mask:0xf bound_ctrl:1
	v_add_f32_e32 v102, v88, v89
	ds_read_b128 v[20:23], v8 offset:19712
	v_add_f32_dpp v86, v86, v86 row_half_mirror row_mask:0xf bank_mask:0xf bound_ctrl:1
	ds_read_b128 v[24:27], v8 offset:19968
	v_cndmask_b32_e64 v129, v93, v101, s[4:5]
	v_add_f32_dpp v86, v86, v86 row_mirror row_mask:0xf bank_mask:0xf bound_ctrl:1
	s_waitcnt lgkmcnt(5)
	v_pk_mul_f32 v[76:77], v[64:65], v[74:75] op_sel_hi:[1,0]
	v_pk_mul_f32 v[78:79], v[66:67], v[74:75] op_sel_hi:[1,0]
	v_pk_fma_f32 v[0:1], v[40:41], v[86:87], v[80:81] op_sel_hi:[1,0,1]
	v_pk_fma_f32 v[2:3], v[42:43], v[86:87], v[82:83] op_sel_hi:[1,0,1]
	v_add_f32_dpp v93, v129, v128 row_mirror row_mask:0xf bank_mask:0xf bound_ctrl:1
	v_pk_mul_f32 v[84:85], v[0:1], v[52:53]
	ds_read_b128 v[32:35], v8 offset:20480
	ds_read_b128 v[36:39], v8 offset:20736
	v_pk_fma_f32 v[84:85], v[2:3], v[54:55], v[84:85]
	v_pk_fma_f32 v[76:77], v[0:1], v[56:57], v[76:77]
	v_cndmask_b32_e64 v130, v102, v94, s[4:5]
	v_add_f32_e32 v86, v84, v85
	v_pk_mul_f32 v[88:89], v[0:1], v[48:49]
	v_pk_fma_f32 v[78:79], v[2:3], v[58:59], v[78:79]
	v_cndmask_b32_e64 v131, v94, v102, s[4:5]
	v_add_f32_dpp v86, v86, v86 quad_perm:[1,0,3,2] row_mask:0xf bank_mask:0xf bound_ctrl:1
	v_pk_fma_f32 v[88:89], v[2:3], v[50:51], v[88:89]
	ds_read_b128 v[48:51], v8 offset:21504
	v_add_f32_dpp v86, v86, v86 quad_perm:[2,3,0,1] row_mask:0xf bank_mask:0xf bound_ctrl:1
	v_add_f32_e32 v103, v88, v89
	ds_read_b128 v[40:43], v8 offset:20992
	v_add_f32_dpp v86, v86, v86 row_half_mirror row_mask:0xf bank_mask:0xf bound_ctrl:1
	ds_read_b128 v[44:47], v8 offset:21248
	ds_read2_b32 v[72:73], v10 offset1:16
	v_add_f32_dpp v94, v131, v130 row_mirror row_mask:0xf bank_mask:0xf bound_ctrl:1
	v_add_f32_dpp v86, v86, v86 row_mirror row_mask:0xf bank_mask:0xf bound_ctrl:1
	s_waitcnt lgkmcnt(6)
	v_pk_mul_f32 v[80:81], v[24:25], v[74:75] op_sel:[0,1] op_sel_hi:[1,1]
	v_pk_mul_f32 v[82:83], v[26:27], v[74:75] op_sel:[0,1] op_sel_hi:[1,1]
	v_cndmask_b32_e64 v126, v94, v90, s[6:7]
	v_pk_fma_f32 v[0:1], v[60:61], v[86:87], v[76:77] op_sel_hi:[1,0,1]
	v_pk_fma_f32 v[2:3], v[62:63], v[86:87], v[78:79] op_sel_hi:[1,0,1]
	v_cndmask_b32_e64 v127, v90, v94, s[6:7]
	v_pk_mul_f32 v[84:85], v[0:1], v[12:13]
	ds_read_b128 v[52:55], v8 offset:21760
	v_add_f32_dpp v90, v127, v126 row_half_mirror row_mask:0xf bank_mask:0xf bound_ctrl:1
	ds_read_b128 v[56:59], v8 offset:22016
	v_pk_fma_f32 v[84:85], v[2:3], v[14:15], v[84:85]
	v_pk_fma_f32 v[80:81], v[0:1], v[16:17], v[80:81]
	v_cndmask_b32_e64 v132, v103, v95, s[4:5]
	v_add_f32_e32 v86, v84, v85
	v_pk_mul_f32 v[88:89], v[0:1], v[68:69]
	v_pk_fma_f32 v[82:83], v[2:3], v[18:19], v[82:83]
	v_cndmask_b32_e64 v133, v95, v103, s[4:5]
	v_add_f32_dpp v86, v86, v86 quad_perm:[1,0,3,2] row_mask:0xf bank_mask:0xf bound_ctrl:1
	v_pk_fma_f32 v[88:89], v[2:3], v[70:71], v[88:89]
	ds_read_b128 v[68:71], v8 offset:22784
	v_add_f32_dpp v86, v86, v86 quad_perm:[2,3,0,1] row_mask:0xf bank_mask:0xf bound_ctrl:1
	v_add_f32_e32 v104, v88, v89
	ds_read_b128 v[60:63], v8 offset:22272
	v_add_f32_dpp v86, v86, v86 row_half_mirror row_mask:0xf bank_mask:0xf bound_ctrl:1
	ds_read_b128 v[64:67], v8 offset:22528
	v_add_f32_dpp v95, v133, v132 row_mirror row_mask:0xf bank_mask:0xf bound_ctrl:1
	v_add_f32_dpp v86, v86, v86 row_mirror row_mask:0xf bank_mask:0xf bound_ctrl:1
	s_waitcnt lgkmcnt(5)
	v_pk_mul_f32 v[76:77], v[44:45], v[72:73] op_sel_hi:[1,0]
	v_pk_mul_f32 v[78:79], v[46:47], v[72:73] op_sel_hi:[1,0]
	v_cndmask_b32_e64 v128, v95, v91, s[6:7]
	v_pk_fma_f32 v[0:1], v[20:21], v[86:87], v[80:81] op_sel_hi:[1,0,1]
	v_pk_fma_f32 v[2:3], v[22:23], v[86:87], v[82:83] op_sel_hi:[1,0,1]
	v_cndmask_b32_e64 v129, v91, v95, s[6:7]
	v_pk_mul_f32 v[84:85], v[0:1], v[32:33]
	ds_read_b128 v[12:15], v8 offset:23040
	v_add_f32_dpp v91, v129, v128 row_half_mirror row_mask:0xf bank_mask:0xf bound_ctrl:1
	ds_read_b128 v[16:19], v8 offset:23296
	v_pk_fma_f32 v[84:85], v[2:3], v[34:35], v[84:85]
	v_pk_fma_f32 v[76:77], v[0:1], v[36:37], v[76:77]
	v_cndmask_b32_e64 v122, v104, v96, s[4:5]
	v_add_f32_e32 v86, v84, v85
	v_pk_mul_f32 v[88:89], v[0:1], v[28:29]
	v_pk_fma_f32 v[78:79], v[2:3], v[38:39], v[78:79]
	v_cndmask_b32_e64 v123, v96, v104, s[4:5]
	v_add_f32_dpp v86, v86, v86 quad_perm:[1,0,3,2] row_mask:0xf bank_mask:0xf bound_ctrl:1
	v_pk_fma_f32 v[88:89], v[2:3], v[30:31], v[88:89]
	ds_read_b128 v[28:31], v8 offset:24064
	v_add_f32_dpp v96, v123, v122 row_mirror row_mask:0xf bank_mask:0xf bound_ctrl:1
	v_add_f32_dpp v86, v86, v86 quad_perm:[2,3,0,1] row_mask:0xf bank_mask:0xf bound_ctrl:1
	v_add_f32_e32 v105, v88, v89
	ds_read_b128 v[20:23], v8 offset:23552
	v_cndmask_b32_e64 v130, v96, v92, s[6:7]
	v_add_f32_dpp v86, v86, v86 row_half_mirror row_mask:0xf bank_mask:0xf bound_ctrl:1
	ds_read_b128 v[24:27], v8 offset:23808
	ds_read2_b32 v[74:75], v10 offset0:32 offset1:48
	v_cndmask_b32_e64 v131, v92, v96, s[6:7]
	v_add_f32_dpp v86, v86, v86 row_mirror row_mask:0xf bank_mask:0xf bound_ctrl:1
	s_waitcnt lgkmcnt(6)
	v_pk_mul_f32 v[80:81], v[64:65], v[72:73] op_sel:[0,1] op_sel_hi:[1,1]
	v_pk_mul_f32 v[82:83], v[66:67], v[72:73] op_sel:[0,1] op_sel_hi:[1,1]
	v_add_f32_dpp v92, v131, v130 row_half_mirror row_mask:0xf bank_mask:0xf bound_ctrl:1
	v_pk_fma_f32 v[0:1], v[40:41], v[86:87], v[76:77] op_sel_hi:[1,0,1]
	v_pk_fma_f32 v[2:3], v[42:43], v[86:87], v[78:79] op_sel_hi:[1,0,1]
	v_cndmask_b32_e64 v122, v92, v90, s[8:9]
	v_cndmask_b32_e64 v123, v90, v92, s[8:9]
	v_pk_mul_f32 v[84:85], v[0:1], v[52:53]
	ds_read_b128 v[32:35], v8 offset:24320
	v_add_f32_dpp v90, v123, v122 quad_perm:[2,3,0,1] row_mask:0xf bank_mask:0xf bound_ctrl:1
	ds_read_b128 v[36:39], v8 offset:24576
	v_cndmask_b32_e64 v124, v105, v97, s[4:5]
	v_pk_fma_f32 v[84:85], v[2:3], v[54:55], v[84:85]
	v_pk_fma_f32 v[80:81], v[0:1], v[56:57], v[80:81]
	v_cndmask_b32_e64 v125, v97, v105, s[4:5]
	v_add_f32_e32 v86, v84, v85
	v_pk_mul_f32 v[88:89], v[0:1], v[48:49]
	v_add_f32_dpp v97, v125, v124 row_mirror row_mask:0xf bank_mask:0xf bound_ctrl:1
	v_pk_fma_f32 v[82:83], v[2:3], v[58:59], v[82:83]
	v_cndmask_b32_e64 v132, v97, v93, s[6:7]
	v_add_f32_dpp v86, v86, v86 quad_perm:[1,0,3,2] row_mask:0xf bank_mask:0xf bound_ctrl:1
	v_pk_fma_f32 v[88:89], v[2:3], v[50:51], v[88:89]
	ds_read_b128 v[48:51], v8 offset:25344
	v_cndmask_b32_e64 v133, v93, v97, s[6:7]
	v_add_f32_dpp v86, v86, v86 quad_perm:[2,3,0,1] row_mask:0xf bank_mask:0xf bound_ctrl:1
	v_add_f32_e32 v106, v88, v89
	ds_read_b128 v[40:43], v8 offset:24832
	v_add_f32_dpp v93, v133, v132 row_half_mirror row_mask:0xf bank_mask:0xf bound_ctrl:1
	v_add_f32_dpp v86, v86, v86 row_half_mirror row_mask:0xf bank_mask:0xf bound_ctrl:1
	ds_read_b128 v[44:47], v8 offset:25088
	v_cndmask_b32_e64 v124, v93, v91, s[8:9]
	v_cndmask_b32_e64 v125, v91, v93, s[8:9]
	v_add_f32_dpp v86, v86, v86 row_mirror row_mask:0xf bank_mask:0xf bound_ctrl:1
	s_waitcnt lgkmcnt(5)
	v_pk_mul_f32 v[76:77], v[24:25], v[74:75] op_sel_hi:[1,0]
	v_pk_mul_f32 v[78:79], v[26:27], v[74:75] op_sel_hi:[1,0]
	v_add_f32_dpp v91, v125, v124 quad_perm:[2,3,0,1] row_mask:0xf bank_mask:0xf bound_ctrl:1
	v_pk_fma_f32 v[0:1], v[60:61], v[86:87], v[80:81] op_sel_hi:[1,0,1]
	v_pk_fma_f32 v[2:3], v[62:63], v[86:87], v[82:83] op_sel_hi:[1,0,1]
	v_cndmask_b32_e64 v126, v91, v90, s[10:11]
	v_cndmask_b32_e64 v127, v90, v91, s[10:11]
	v_pk_mul_f32 v[84:85], v[0:1], v[12:13]
	v_pk_fma_f32 v[76:77], v[0:1], v[16:17], v[76:77]
	v_add_f32_dpp v90, v127, v126 quad_perm:[1,0,3,2] row_mask:0xf bank_mask:0xf bound_ctrl:1
	ds_write_b32 v11, v90
	ds_read_b128 v[52:55], v8 offset:25600
	ds_read_b128 v[56:59], v8 offset:25856
	v_pk_fma_f32 v[84:85], v[2:3], v[14:15], v[84:85]
	v_pk_mul_f32 v[88:89], v[0:1], v[68:69]
	v_add_f32_e32 v86, v84, v85
	v_pk_fma_f32 v[78:79], v[2:3], v[18:19], v[78:79]
	v_pk_fma_f32 v[88:89], v[2:3], v[70:71], v[88:89]
	v_add_f32_dpp v86, v86, v86 quad_perm:[1,0,3,2] row_mask:0xf bank_mask:0xf bound_ctrl:1
	ds_read_b128 v[68:71], v8 offset:26624
	v_add_f32_e32 v107, v88, v89
	v_add_f32_dpp v86, v86, v86 quad_perm:[2,3,0,1] row_mask:0xf bank_mask:0xf bound_ctrl:1
	ds_read_b128 v[60:63], v8 offset:26112
	ds_read_b128 v[64:67], v8 offset:26368
	v_add_f32_dpp v86, v86, v86 row_half_mirror row_mask:0xf bank_mask:0xf bound_ctrl:1
	ds_read2_b32 v[72:73], v10 offset0:64 offset1:80
	s_waitcnt lgkmcnt(7)
	v_pk_mul_f32 v[80:81], v[44:45], v[74:75] op_sel:[0,1] op_sel_hi:[1,1]
	v_add_f32_dpp v86, v86, v86 row_mirror row_mask:0xf bank_mask:0xf bound_ctrl:1
	v_pk_mul_f32 v[82:83], v[46:47], v[74:75] op_sel:[0,1] op_sel_hi:[1,1]
	v_pk_fma_f32 v[0:1], v[20:21], v[86:87], v[76:77] op_sel_hi:[1,0,1]
	v_pk_fma_f32 v[2:3], v[22:23], v[86:87], v[78:79] op_sel_hi:[1,0,1]
	v_pk_mul_f32 v[84:85], v[0:1], v[32:33]
	ds_read_b128 v[12:15], v8 offset:26880
	ds_read_b128 v[16:19], v8 offset:27136
	v_pk_fma_f32 v[84:85], v[2:3], v[34:35], v[84:85]
	v_pk_fma_f32 v[80:81], v[0:1], v[36:37], v[80:81]
	v_add_f32_e32 v86, v84, v85
	v_pk_mul_f32 v[88:89], v[0:1], v[28:29]
	v_pk_fma_f32 v[82:83], v[2:3], v[38:39], v[82:83]
	v_add_f32_dpp v86, v86, v86 quad_perm:[1,0,3,2] row_mask:0xf bank_mask:0xf bound_ctrl:1
	v_pk_fma_f32 v[88:89], v[2:3], v[30:31], v[88:89]
	ds_read_b128 v[28:31], v8 offset:27904
	v_add_f32_dpp v86, v86, v86 quad_perm:[2,3,0,1] row_mask:0xf bank_mask:0xf bound_ctrl:1
	v_add_f32_e32 v108, v88, v89
	ds_read_b128 v[20:23], v8 offset:27392
	v_add_f32_dpp v86, v86, v86 row_half_mirror row_mask:0xf bank_mask:0xf bound_ctrl:1
	ds_read_b128 v[24:27], v8 offset:27648
	s_waitcnt lgkmcnt(5)
	v_pk_mul_f32 v[76:77], v[64:65], v[72:73] op_sel_hi:[1,0]
	v_add_f32_dpp v86, v86, v86 row_mirror row_mask:0xf bank_mask:0xf bound_ctrl:1
	v_pk_mul_f32 v[78:79], v[66:67], v[72:73] op_sel_hi:[1,0]
	v_pk_fma_f32 v[0:1], v[40:41], v[86:87], v[80:81] op_sel_hi:[1,0,1]
	v_pk_fma_f32 v[2:3], v[42:43], v[86:87], v[82:83] op_sel_hi:[1,0,1]
	v_pk_mul_f32 v[84:85], v[0:1], v[52:53]
	ds_read_b128 v[32:35], v8 offset:28160
	ds_read_b128 v[36:39], v8 offset:28416
	v_pk_fma_f32 v[84:85], v[2:3], v[54:55], v[84:85]
	v_pk_fma_f32 v[76:77], v[0:1], v[56:57], v[76:77]
	v_add_f32_e32 v86, v84, v85
	v_pk_mul_f32 v[88:89], v[0:1], v[48:49]
	v_pk_fma_f32 v[78:79], v[2:3], v[58:59], v[78:79]
	v_add_f32_dpp v86, v86, v86 quad_perm:[1,0,3,2] row_mask:0xf bank_mask:0xf bound_ctrl:1
	v_pk_fma_f32 v[88:89], v[2:3], v[50:51], v[88:89]
	ds_read_b128 v[48:51], v8 offset:29184
	v_add_f32_dpp v86, v86, v86 quad_perm:[2,3,0,1] row_mask:0xf bank_mask:0xf bound_ctrl:1
	v_add_f32_e32 v109, v88, v89
	ds_read_b128 v[40:43], v8 offset:28672
	v_add_f32_dpp v86, v86, v86 row_half_mirror row_mask:0xf bank_mask:0xf bound_ctrl:1
	ds_read_b128 v[44:47], v8 offset:28928
	ds_read2_b32 v[74:75], v10 offset0:96 offset1:112
	v_add_f32_dpp v86, v86, v86 row_mirror row_mask:0xf bank_mask:0xf bound_ctrl:1
	s_waitcnt lgkmcnt(6)
	v_pk_mul_f32 v[80:81], v[24:25], v[72:73] op_sel:[0,1] op_sel_hi:[1,1]
	v_pk_mul_f32 v[82:83], v[26:27], v[72:73] op_sel:[0,1] op_sel_hi:[1,1]
	v_pk_fma_f32 v[0:1], v[60:61], v[86:87], v[76:77] op_sel_hi:[1,0,1]
	v_pk_fma_f32 v[2:3], v[62:63], v[86:87], v[78:79] op_sel_hi:[1,0,1]
	v_pk_mul_f32 v[84:85], v[0:1], v[12:13]
	ds_read_b128 v[52:55], v8 offset:29440
	ds_read_b128 v[56:59], v8 offset:29696
	v_pk_fma_f32 v[84:85], v[2:3], v[14:15], v[84:85]
	v_pk_fma_f32 v[80:81], v[0:1], v[16:17], v[80:81]
	v_add_f32_e32 v86, v84, v85
	v_pk_mul_f32 v[88:89], v[0:1], v[68:69]
	v_pk_fma_f32 v[82:83], v[2:3], v[18:19], v[82:83]
	v_add_f32_dpp v86, v86, v86 quad_perm:[1,0,3,2] row_mask:0xf bank_mask:0xf bound_ctrl:1
	v_pk_fma_f32 v[88:89], v[2:3], v[70:71], v[88:89]
	ds_read_b128 v[68:71], v8 offset:30464
	v_add_f32_dpp v86, v86, v86 quad_perm:[2,3,0,1] row_mask:0xf bank_mask:0xf bound_ctrl:1
	v_add_f32_e32 v110, v88, v89
	ds_read_b128 v[60:63], v8 offset:29952
	v_add_f32_dpp v86, v86, v86 row_half_mirror row_mask:0xf bank_mask:0xf bound_ctrl:1
	ds_read_b128 v[64:67], v8 offset:30208
	s_waitcnt lgkmcnt(5)
	v_pk_mul_f32 v[76:77], v[44:45], v[74:75] op_sel_hi:[1,0]
	v_add_f32_dpp v86, v86, v86 row_mirror row_mask:0xf bank_mask:0xf bound_ctrl:1
	v_pk_mul_f32 v[78:79], v[46:47], v[74:75] op_sel_hi:[1,0]
	v_pk_fma_f32 v[0:1], v[20:21], v[86:87], v[80:81] op_sel_hi:[1,0,1]
	v_pk_fma_f32 v[2:3], v[22:23], v[86:87], v[82:83] op_sel_hi:[1,0,1]
	v_pk_mul_f32 v[84:85], v[0:1], v[32:33]
	ds_read_b128 v[12:15], v8 offset:30720
	ds_read_b128 v[16:19], v8 offset:30976
	v_pk_fma_f32 v[84:85], v[2:3], v[34:35], v[84:85]
	v_pk_fma_f32 v[76:77], v[0:1], v[36:37], v[76:77]
	v_add_f32_e32 v86, v84, v85
	v_pk_mul_f32 v[88:89], v[0:1], v[28:29]
	v_pk_fma_f32 v[78:79], v[2:3], v[38:39], v[78:79]
	v_add_f32_dpp v86, v86, v86 quad_perm:[1,0,3,2] row_mask:0xf bank_mask:0xf bound_ctrl:1
	v_pk_fma_f32 v[88:89], v[2:3], v[30:31], v[88:89]
	ds_read_b128 v[28:31], v8 offset:31744
	v_add_f32_dpp v86, v86, v86 quad_perm:[2,3,0,1] row_mask:0xf bank_mask:0xf bound_ctrl:1
	v_add_f32_e32 v111, v88, v89
	ds_read_b128 v[20:23], v8 offset:31232
	v_add_f32_dpp v86, v86, v86 row_half_mirror row_mask:0xf bank_mask:0xf bound_ctrl:1
	ds_read_b128 v[24:27], v8 offset:31488
	ds_read2_b32 v[72:73], v10 offset0:128 offset1:144
	v_add_f32_dpp v86, v86, v86 row_mirror row_mask:0xf bank_mask:0xf bound_ctrl:1
	s_waitcnt lgkmcnt(6)
	v_pk_mul_f32 v[80:81], v[64:65], v[74:75] op_sel:[0,1] op_sel_hi:[1,1]
	v_pk_mul_f32 v[82:83], v[66:67], v[74:75] op_sel:[0,1] op_sel_hi:[1,1]
	v_pk_fma_f32 v[0:1], v[40:41], v[86:87], v[76:77] op_sel_hi:[1,0,1]
	v_pk_fma_f32 v[2:3], v[42:43], v[86:87], v[78:79] op_sel_hi:[1,0,1]
	v_pk_mul_f32 v[84:85], v[0:1], v[52:53]
	ds_read_b128 v[32:35], v8 offset:32000
	ds_read_b128 v[36:39], v8 offset:32256
	v_pk_fma_f32 v[84:85], v[2:3], v[54:55], v[84:85]
	v_pk_fma_f32 v[80:81], v[0:1], v[56:57], v[80:81]
	v_add_f32_e32 v86, v84, v85
	v_pk_mul_f32 v[88:89], v[0:1], v[48:49]
	v_pk_fma_f32 v[82:83], v[2:3], v[58:59], v[82:83]
	v_add_f32_dpp v86, v86, v86 quad_perm:[1,0,3,2] row_mask:0xf bank_mask:0xf bound_ctrl:1
	v_pk_fma_f32 v[88:89], v[2:3], v[50:51], v[88:89]
	ds_read_b128 v[48:51], v8 offset:33024
	v_add_f32_dpp v86, v86, v86 quad_perm:[2,3,0,1] row_mask:0xf bank_mask:0xf bound_ctrl:1
	v_add_f32_e32 v112, v88, v89
	ds_read_b128 v[40:43], v8 offset:32512
	v_add_f32_dpp v86, v86, v86 row_half_mirror row_mask:0xf bank_mask:0xf bound_ctrl:1
	ds_read_b128 v[44:47], v8 offset:32768
	s_waitcnt lgkmcnt(5)
	v_pk_mul_f32 v[76:77], v[24:25], v[72:73] op_sel_hi:[1,0]
	v_add_f32_dpp v86, v86, v86 row_mirror row_mask:0xf bank_mask:0xf bound_ctrl:1
	v_pk_mul_f32 v[78:79], v[26:27], v[72:73] op_sel_hi:[1,0]
	v_pk_fma_f32 v[0:1], v[60:61], v[86:87], v[80:81] op_sel_hi:[1,0,1]
	v_pk_fma_f32 v[2:3], v[62:63], v[86:87], v[82:83] op_sel_hi:[1,0,1]
	v_pk_mul_f32 v[84:85], v[0:1], v[12:13]
	ds_read_b128 v[52:55], v8 offset:33280
	ds_read_b128 v[56:59], v8 offset:33536
	v_pk_fma_f32 v[84:85], v[2:3], v[14:15], v[84:85]
	v_pk_fma_f32 v[76:77], v[0:1], v[16:17], v[76:77]
	v_add_f32_e32 v86, v84, v85
	v_pk_mul_f32 v[88:89], v[0:1], v[68:69]
	v_pk_fma_f32 v[78:79], v[2:3], v[18:19], v[78:79]
	v_add_f32_dpp v86, v86, v86 quad_perm:[1,0,3,2] row_mask:0xf bank_mask:0xf bound_ctrl:1
	v_pk_fma_f32 v[88:89], v[2:3], v[70:71], v[88:89]
	ds_read_b128 v[68:71], v8 offset:34304
	v_add_f32_dpp v86, v86, v86 quad_perm:[2,3,0,1] row_mask:0xf bank_mask:0xf bound_ctrl:1
	v_add_f32_e32 v113, v88, v89
	ds_read_b128 v[60:63], v8 offset:33792
	v_add_f32_dpp v86, v86, v86 row_half_mirror row_mask:0xf bank_mask:0xf bound_ctrl:1
	ds_read_b128 v[64:67], v8 offset:34048
	ds_read2_b32 v[74:75], v10 offset0:160 offset1:176
	v_add_f32_dpp v86, v86, v86 row_mirror row_mask:0xf bank_mask:0xf bound_ctrl:1
	s_waitcnt lgkmcnt(6)
	v_pk_mul_f32 v[80:81], v[44:45], v[72:73] op_sel:[0,1] op_sel_hi:[1,1]
	v_pk_mul_f32 v[82:83], v[46:47], v[72:73] op_sel:[0,1] op_sel_hi:[1,1]
	v_pk_fma_f32 v[0:1], v[20:21], v[86:87], v[76:77] op_sel_hi:[1,0,1]
	v_pk_fma_f32 v[2:3], v[22:23], v[86:87], v[78:79] op_sel_hi:[1,0,1]
	v_pk_mul_f32 v[84:85], v[0:1], v[32:33]
	ds_read_b128 v[12:15], v8 offset:34560
	ds_read_b128 v[16:19], v8 offset:34816
	v_pk_fma_f32 v[84:85], v[2:3], v[34:35], v[84:85]
	v_pk_fma_f32 v[80:81], v[0:1], v[36:37], v[80:81]
	v_add_f32_e32 v86, v84, v85
	v_pk_mul_f32 v[88:89], v[0:1], v[28:29]
	v_pk_fma_f32 v[82:83], v[2:3], v[38:39], v[82:83]
	v_add_f32_dpp v86, v86, v86 quad_perm:[1,0,3,2] row_mask:0xf bank_mask:0xf bound_ctrl:1
	v_pk_fma_f32 v[88:89], v[2:3], v[30:31], v[88:89]
	ds_read_b128 v[28:31], v8 offset:35584
	v_add_f32_dpp v86, v86, v86 quad_perm:[2,3,0,1] row_mask:0xf bank_mask:0xf bound_ctrl:1
	v_add_f32_e32 v114, v88, v89
	ds_read_b128 v[20:23], v8 offset:35072
	v_add_f32_dpp v86, v86, v86 row_half_mirror row_mask:0xf bank_mask:0xf bound_ctrl:1
	ds_read_b128 v[24:27], v8 offset:35328
	s_waitcnt lgkmcnt(5)
	v_pk_mul_f32 v[76:77], v[64:65], v[74:75] op_sel_hi:[1,0]
	v_add_f32_dpp v86, v86, v86 row_mirror row_mask:0xf bank_mask:0xf bound_ctrl:1
	v_pk_mul_f32 v[78:79], v[66:67], v[74:75] op_sel_hi:[1,0]
	v_pk_fma_f32 v[0:1], v[40:41], v[86:87], v[80:81] op_sel_hi:[1,0,1]
	v_pk_fma_f32 v[2:3], v[42:43], v[86:87], v[82:83] op_sel_hi:[1,0,1]
	v_pk_mul_f32 v[84:85], v[0:1], v[52:53]
	ds_read_b128 v[32:35], v8 offset:35840
	ds_read_b128 v[36:39], v8 offset:36096
	v_pk_fma_f32 v[84:85], v[2:3], v[54:55], v[84:85]
	v_pk_fma_f32 v[76:77], v[0:1], v[56:57], v[76:77]
	v_cndmask_b32_e64 v128, v114, v106, s[4:5]
	v_add_f32_e32 v86, v84, v85
	v_pk_mul_f32 v[88:89], v[0:1], v[48:49]
	v_pk_fma_f32 v[78:79], v[2:3], v[58:59], v[78:79]
	v_add_f32_dpp v86, v86, v86 quad_perm:[1,0,3,2] row_mask:0xf bank_mask:0xf bound_ctrl:1
	v_pk_fma_f32 v[88:89], v[2:3], v[50:51], v[88:89]
	ds_read_b128 v[48:51], v8 offset:36864
	v_add_f32_dpp v86, v86, v86 quad_perm:[2,3,0,1] row_mask:0xf bank_mask:0xf bound_ctrl:1
	v_add_f32_e32 v115, v88, v89
	ds_read_b128 v[40:43], v8 offset:36352
	v_add_f32_dpp v86, v86, v86 row_half_mirror row_mask:0xf bank_mask:0xf bound_ctrl:1
	ds_read_b128 v[44:47], v8 offset:36608
	ds_read2_b32 v[72:73], v10 offset0:192 offset1:208
	v_cndmask_b32_e64 v129, v106, v114, s[4:5]
	v_add_f32_dpp v86, v86, v86 row_mirror row_mask:0xf bank_mask:0xf bound_ctrl:1
	s_waitcnt lgkmcnt(6)
	v_pk_mul_f32 v[80:81], v[24:25], v[74:75] op_sel:[0,1] op_sel_hi:[1,1]
	v_pk_mul_f32 v[82:83], v[26:27], v[74:75] op_sel:[0,1] op_sel_hi:[1,1]
	v_pk_fma_f32 v[0:1], v[60:61], v[86:87], v[76:77] op_sel_hi:[1,0,1]
	v_pk_fma_f32 v[2:3], v[62:63], v[86:87], v[78:79] op_sel_hi:[1,0,1]
	v_add_f32_dpp v106, v129, v128 row_mirror row_mask:0xf bank_mask:0xf bound_ctrl:1
	v_pk_mul_f32 v[84:85], v[0:1], v[12:13]
	ds_read_b128 v[52:55], v8 offset:37120
	ds_read_b128 v[56:59], v8 offset:37376
	v_pk_fma_f32 v[84:85], v[2:3], v[14:15], v[84:85]
	v_pk_fma_f32 v[80:81], v[0:1], v[16:17], v[80:81]
	v_cndmask_b32_e64 v130, v115, v107, s[4:5]
	v_add_f32_e32 v86, v84, v85
	v_pk_mul_f32 v[88:89], v[0:1], v[68:69]
	v_pk_fma_f32 v[82:83], v[2:3], v[18:19], v[82:83]
	v_add_f32_dpp v86, v86, v86 quad_perm:[1,0,3,2] row_mask:0xf bank_mask:0xf bound_ctrl:1
	v_pk_fma_f32 v[88:89], v[2:3], v[70:71], v[88:89]
	ds_read_b128 v[68:71], v8 offset:38144
	v_add_f32_dpp v86, v86, v86 quad_perm:[2,3,0,1] row_mask:0xf bank_mask:0xf bound_ctrl:1
	v_add_f32_e32 v116, v88, v89
	ds_read_b128 v[60:63], v8 offset:37632
	v_add_f32_dpp v86, v86, v86 row_half_mirror row_mask:0xf bank_mask:0xf bound_ctrl:1
	ds_read_b128 v[64:67], v8 offset:37888
	v_cndmask_b32_e64 v131, v107, v115, s[4:5]
	v_add_f32_dpp v86, v86, v86 row_mirror row_mask:0xf bank_mask:0xf bound_ctrl:1
	s_waitcnt lgkmcnt(5)
	v_pk_mul_f32 v[76:77], v[44:45], v[72:73] op_sel_hi:[1,0]
	v_pk_mul_f32 v[78:79], v[46:47], v[72:73] op_sel_hi:[1,0]
	v_pk_fma_f32 v[0:1], v[20:21], v[86:87], v[80:81] op_sel_hi:[1,0,1]
	v_pk_fma_f32 v[2:3], v[22:23], v[86:87], v[82:83] op_sel_hi:[1,0,1]
	v_add_f32_dpp v107, v131, v130 row_mirror row_mask:0xf bank_mask:0xf bound_ctrl:1
	v_pk_mul_f32 v[84:85], v[0:1], v[32:33]
	ds_read_b128 v[12:15], v8 offset:38400
	ds_read_b128 v[16:19], v8 offset:38656
	v_pk_fma_f32 v[84:85], v[2:3], v[34:35], v[84:85]
	v_pk_fma_f32 v[76:77], v[0:1], v[36:37], v[76:77]
	v_cndmask_b32_e64 v132, v116, v108, s[4:5]
	v_add_f32_e32 v86, v84, v85
	v_pk_mul_f32 v[88:89], v[0:1], v[28:29]
	v_pk_fma_f32 v[78:79], v[2:3], v[38:39], v[78:79]
	v_add_f32_dpp v86, v86, v86 quad_perm:[1,0,3,2] row_mask:0xf bank_mask:0xf bound_ctrl:1
	v_pk_fma_f32 v[88:89], v[2:3], v[30:31], v[88:89]
	ds_read_b128 v[28:31], v8 offset:39424
	v_add_f32_dpp v86, v86, v86 quad_perm:[2,3,0,1] row_mask:0xf bank_mask:0xf bound_ctrl:1
	v_add_f32_e32 v117, v88, v89
	ds_read_b128 v[20:23], v8 offset:38912
	v_add_f32_dpp v86, v86, v86 row_half_mirror row_mask:0xf bank_mask:0xf bound_ctrl:1
	ds_read_b128 v[24:27], v8 offset:39168
	ds_read2_b32 v[74:75], v10 offset0:224 offset1:240
	v_cndmask_b32_e64 v133, v108, v116, s[4:5]
	v_add_f32_dpp v86, v86, v86 row_mirror row_mask:0xf bank_mask:0xf bound_ctrl:1
	s_waitcnt lgkmcnt(6)
	v_pk_mul_f32 v[80:81], v[64:65], v[72:73] op_sel:[0,1] op_sel_hi:[1,1]
	v_pk_mul_f32 v[82:83], v[66:67], v[72:73] op_sel:[0,1] op_sel_hi:[1,1]
	v_pk_fma_f32 v[0:1], v[40:41], v[86:87], v[76:77] op_sel_hi:[1,0,1]
	v_pk_fma_f32 v[2:3], v[42:43], v[86:87], v[78:79] op_sel_hi:[1,0,1]
	v_add_f32_dpp v108, v133, v132 row_mirror row_mask:0xf bank_mask:0xf bound_ctrl:1
	v_pk_mul_f32 v[84:85], v[0:1], v[52:53]
	ds_read_b128 v[32:35], v8 offset:39680
	ds_read_b128 v[36:39], v8 offset:39936
	v_pk_fma_f32 v[84:85], v[2:3], v[54:55], v[84:85]
	v_pk_fma_f32 v[80:81], v[0:1], v[56:57], v[80:81]
	v_cndmask_b32_e64 v122, v117, v109, s[4:5]
	v_add_f32_e32 v86, v84, v85
	v_pk_mul_f32 v[88:89], v[0:1], v[48:49]
	v_pk_fma_f32 v[82:83], v[2:3], v[58:59], v[82:83]
	v_add_f32_dpp v86, v86, v86 quad_perm:[1,0,3,2] row_mask:0xf bank_mask:0xf bound_ctrl:1
	v_pk_fma_f32 v[88:89], v[2:3], v[50:51], v[88:89]
	ds_read_b128 v[48:51], v8 offset:40704
	v_add_f32_dpp v86, v86, v86 quad_perm:[2,3,0,1] row_mask:0xf bank_mask:0xf bound_ctrl:1
	v_add_f32_e32 v118, v88, v89
	ds_read_b128 v[40:43], v8 offset:40192
	v_add_f32_dpp v86, v86, v86 row_half_mirror row_mask:0xf bank_mask:0xf bound_ctrl:1
	ds_read_b128 v[44:47], v8 offset:40448
	v_cndmask_b32_e64 v123, v109, v117, s[4:5]
	v_add_f32_dpp v86, v86, v86 row_mirror row_mask:0xf bank_mask:0xf bound_ctrl:1
	s_waitcnt lgkmcnt(5)
	v_pk_mul_f32 v[76:77], v[24:25], v[74:75] op_sel_hi:[1,0]
	v_pk_mul_f32 v[78:79], v[26:27], v[74:75] op_sel_hi:[1,0]
	v_pk_fma_f32 v[0:1], v[60:61], v[86:87], v[80:81] op_sel_hi:[1,0,1]
	v_pk_fma_f32 v[2:3], v[62:63], v[86:87], v[82:83] op_sel_hi:[1,0,1]
	v_add_f32_dpp v109, v123, v122 row_mirror row_mask:0xf bank_mask:0xf bound_ctrl:1
	v_pk_mul_f32 v[84:85], v[0:1], v[12:13]
	v_pk_fma_f32 v[76:77], v[0:1], v[16:17], v[76:77]
	v_pk_fma_f32 v[84:85], v[2:3], v[14:15], v[84:85]
	v_cndmask_b32_e64 v124, v118, v110, s[4:5]
	v_add_f32_e32 v86, v84, v85
	v_pk_mul_f32 v[88:89], v[0:1], v[68:69]
	v_pk_fma_f32 v[78:79], v[2:3], v[18:19], v[78:79]
	v_cndmask_b32_e64 v125, v110, v118, s[4:5]
	v_add_f32_dpp v86, v86, v86 quad_perm:[1,0,3,2] row_mask:0xf bank_mask:0xf bound_ctrl:1
	v_pk_fma_f32 v[88:89], v[2:3], v[70:71], v[88:89]
	v_add_f32_dpp v110, v125, v124 row_mirror row_mask:0xf bank_mask:0xf bound_ctrl:1
	v_add_f32_dpp v86, v86, v86 quad_perm:[2,3,0,1] row_mask:0xf bank_mask:0xf bound_ctrl:1
	v_add_f32_e32 v119, v88, v89
	s_waitcnt lgkmcnt(0)
	v_pk_mul_f32 v[80:81], v[44:45], v[74:75] op_sel:[0,1] op_sel_hi:[1,1]
	v_add_f32_dpp v86, v86, v86 row_half_mirror row_mask:0xf bank_mask:0xf bound_ctrl:1
	v_pk_mul_f32 v[82:83], v[46:47], v[74:75] op_sel:[0,1] op_sel_hi:[1,1]
	v_cndmask_b32_e64 v132, v110, v106, s[6:7]
	v_add_f32_dpp v86, v86, v86 row_mirror row_mask:0xf bank_mask:0xf bound_ctrl:1
	v_cndmask_b32_e64 v133, v106, v110, s[6:7]
	v_pk_fma_f32 v[0:1], v[20:21], v[86:87], v[76:77] op_sel_hi:[1,0,1]
	v_pk_fma_f32 v[2:3], v[22:23], v[86:87], v[78:79] op_sel_hi:[1,0,1]
	v_add_f32_dpp v106, v133, v132 row_half_mirror row_mask:0xf bank_mask:0xf bound_ctrl:1
	v_pk_mul_f32 v[84:85], v[0:1], v[32:33]
	v_pk_fma_f32 v[80:81], v[0:1], v[36:37], v[80:81]
	v_pk_fma_f32 v[84:85], v[2:3], v[34:35], v[84:85]
	v_cndmask_b32_e64 v126, v119, v111, s[4:5]
	v_add_f32_e32 v86, v84, v85
	v_pk_mul_f32 v[88:89], v[0:1], v[28:29]
	v_pk_fma_f32 v[82:83], v[2:3], v[38:39], v[82:83]
	v_cndmask_b32_e64 v127, v111, v119, s[4:5]
	v_add_f32_dpp v86, v86, v86 quad_perm:[1,0,3,2] row_mask:0xf bank_mask:0xf bound_ctrl:1
	v_pk_fma_f32 v[88:89], v[2:3], v[30:31], v[88:89]
	v_add_f32_dpp v111, v127, v126 row_mirror row_mask:0xf bank_mask:0xf bound_ctrl:1
	v_add_f32_dpp v86, v86, v86 quad_perm:[2,3,0,1] row_mask:0xf bank_mask:0xf bound_ctrl:1
	v_add_f32_e32 v120, v88, v89
	v_cndmask_b32_e64 v122, v111, v107, s[6:7]
	v_add_f32_dpp v86, v86, v86 row_half_mirror row_mask:0xf bank_mask:0xf bound_ctrl:1
	v_cndmask_b32_e64 v123, v107, v111, s[6:7]
	v_cndmask_b32_e64 v128, v120, v112, s[4:5]
	v_add_f32_dpp v86, v86, v86 row_mirror row_mask:0xf bank_mask:0xf bound_ctrl:1
	v_add_f32_dpp v107, v123, v122 row_half_mirror row_mask:0xf bank_mask:0xf bound_ctrl:1
	v_pk_fma_f32 v[0:1], v[40:41], v[86:87], v[80:81] op_sel_hi:[1,0,1]
	v_pk_fma_f32 v[2:3], v[42:43], v[86:87], v[82:83] op_sel_hi:[1,0,1]
	v_pk_mul_f32 v[88:89], v[0:1], v[48:49]
	v_cndmask_b32_e64 v129, v112, v120, s[4:5]
	v_pk_fma_f32 v[88:89], v[2:3], v[50:51], v[88:89]
	v_add_f32_e32 v121, v88, v89
	v_add_f32_dpp v112, v129, v128 row_mirror row_mask:0xf bank_mask:0xf bound_ctrl:1
	v_cndmask_b32_e64 v130, v121, v113, s[4:5]
	v_cndmask_b32_e64 v124, v112, v108, s[6:7]
	v_cndmask_b32_e64 v125, v108, v112, s[6:7]
	v_cndmask_b32_e64 v131, v113, v121, s[4:5]
	s_nop 0
	v_add_f32_dpp v108, v125, v124 row_half_mirror row_mask:0xf bank_mask:0xf bound_ctrl:1
	v_add_f32_dpp v113, v131, v130 row_mirror row_mask:0xf bank_mask:0xf bound_ctrl:1
	v_cndmask_b32_e64 v128, v108, v106, s[8:9]
	v_cndmask_b32_e64 v129, v106, v108, s[8:9]
	v_cndmask_b32_e64 v126, v113, v109, s[6:7]
	v_cndmask_b32_e64 v127, v109, v113, s[6:7]
	v_add_f32_dpp v106, v129, v128 quad_perm:[2,3,0,1] row_mask:0xf bank_mask:0xf bound_ctrl:1
	s_nop 0
	v_add_f32_dpp v109, v127, v126 row_half_mirror row_mask:0xf bank_mask:0xf bound_ctrl:1
	v_cndmask_b32_e64 v130, v109, v107, s[8:9]
	v_cndmask_b32_e64 v131, v107, v109, s[8:9]
	s_nop 0
	s_nop 0
	v_add_f32_dpp v107, v131, v130 quad_perm:[2,3,0,1] row_mask:0xf bank_mask:0xf bound_ctrl:1
	v_cndmask_b32_e64 v132, v107, v106, s[10:11]
	v_cndmask_b32_e64 v133, v106, v107, s[10:11]
	s_nop 0
	s_nop 0
	v_add_f32_dpp v106, v133, v132 quad_perm:[1,0,3,2] row_mask:0xf bank_mask:0xf bound_ctrl:1
	ds_write_b32 v11, v106 offset:1024
	s_waitcnt lgkmcnt(0)
	s_and_saveexec_b64 s[14:15], s[12:13]
	v_mov_b32_e32 v8, s17
	v_mov_b32_e32 v9, s16
	ds_write_b32 v8, v9
	s_or_b64 exec, exec, s[14:15]
	s_cmp_eq_u32 s16, 64
	s_cbranch_scc0 .LBB0_723
	s_mov_b64 s[4:5], -1

.LBB0_1537:
	v_cndmask_b32_e64 v0, 0, 1, s[44:45]
	v_lshl_add_u32 v4, s21, 2, v145
	v_cmp_ne_u32_e64 s[10:11], 1, v0
	v_xor_b32_e32 v0, v153, v143
	s_mov_b64 s[62:63], -1
	s_andn2_b64 vcc, exec, s[44:45]
	v_lshl_add_u32 v156, v0, 4, v146
	v_or_b32_e32 v155, 1, v4
	s_cbranch_vccnz .LBB0_1539
	s_waitcnt vmcnt(62)
	v_mul_f32_e32 v0, 0x43800000, v12
	s_waitcnt vmcnt(62)
	v_mul_f32_e32 v1, 0x43800000, v14
	v_mov_b32_e32 v162, 0
	v_cvt_pk_fp8_f32 v162, v0, v1
	s_waitcnt vmcnt(59)
	v_mul_f32_e32 v0, 0x43800000, v20
	s_waitcnt vmcnt(58)
	v_mul_f32_e32 v1, 0x43800000, v22
	v_mov_b32_e32 v163, 0
	v_cvt_pk_fp8_f32 v163, v0, v1
	s_waitcnt vmcnt(57)
	v_mul_f32_e32 v0, 0x43800000, v24
	s_waitcnt vmcnt(56)
	v_mul_f32_e32 v1, 0x43800000, v26
	v_mov_b32_e32 v164, 0
	v_cvt_pk_fp8_f32 v163, v0, v1 op_sel:[0,0,1]
	s_waitcnt vmcnt(55)
	v_mul_f32_e32 v0, 0x43800000, v28
	s_waitcnt vmcnt(54)
	v_mul_f32_e32 v1, 0x43800000, v30
	v_cvt_pk_fp8_f32 v164, v0, v1
	s_waitcnt vmcnt(51)
	v_mul_f32_e32 v0, 0x43800000, v36
	s_waitcnt vmcnt(50)
	v_mul_f32_e32 v1, 0x43800000, v38
	v_mov_b32_e32 v165, 0
	v_cvt_pk_fp8_f32 v165, v0, v1
	v_mul_f32_e32 v2, 0x43800000, v16
	v_mul_f32_e32 v3, 0x43800000, v18
	v_cvt_pk_fp8_f32 v162, v2, v3 op_sel:[0,0,1]
	v_mul_f32_e32 v2, 0x43800000, v32
	v_mul_f32_e32 v3, 0x43800000, v34
	s_waitcnt vmcnt(49)
	v_mul_f32_e32 v0, 0x43800000, v40
	s_waitcnt vmcnt(48)
	v_mul_f32_e32 v1, 0x43800000, v42
	v_cvt_pk_fp8_f32 v164, v2, v3 op_sel:[0,0,1]
	v_cvt_pk_fp8_f32 v165, v0, v1 op_sel:[0,0,1]
	s_waitcnt vmcnt(47)
	v_mul_f32_e32 v1, 0x43800000, v44
	s_waitcnt vmcnt(46)
	v_mul_f32_e32 v2, 0x43800000, v46
	v_mov_b32_e32 v0, 0
	v_cvt_pk_fp8_f32 v0, v1, v2
	s_waitcnt vmcnt(43)
	v_mul_f32_e32 v2, 0x43800000, v52
	s_waitcnt vmcnt(42)
	v_mul_f32_e32 v6, 0x43800000, v54
	v_mov_b32_e32 v1, 0
	v_cvt_pk_fp8_f32 v1, v2, v6
	v_mul_f32_e32 v3, 0x43800000, v48
	v_mul_f32_e32 v5, 0x43800000, v50
	v_cvt_pk_fp8_f32 v0, v3, v5 op_sel:[0,0,1]
	s_waitcnt vmcnt(41)
	v_mul_f32_e32 v2, 0x43800000, v56
	s_waitcnt vmcnt(40)
	v_mul_f32_e32 v3, 0x43800000, v58
	v_cvt_pk_fp8_f32 v1, v2, v3 op_sel:[0,0,1]
	s_waitcnt vmcnt(39)
	v_mul_f32_e32 v3, 0x43800000, v60
	s_waitcnt vmcnt(38)
	v_mul_f32_e32 v5, 0x43800000, v62
	v_mov_b32_e32 v2, 0
	v_cvt_pk_fp8_f32 v2, v3, v5
	s_waitcnt vmcnt(35)
	v_mul_f32_e32 v5, 0x43800000, v76
	s_waitcnt vmcnt(34)
	v_mul_f32_e32 v157, 0x43800000, v78
	v_mov_b32_e32 v3, 0
	v_cvt_pk_fp8_f32 v3, v5, v157
	v_mul_f32_e32 v6, 0x43800000, v64
	v_mul_f32_e32 v7, 0x43800000, v74
	v_cvt_pk_fp8_f32 v2, v6, v7 op_sel:[0,0,1]
	s_waitcnt vmcnt(33)
	v_mul_f32_e32 v5, 0x43800000, v80
	s_waitcnt vmcnt(32)
	v_mul_f32_e32 v6, 0x43800000, v88
	v_cvt_pk_fp8_f32 v3, v5, v6 op_sel:[0,0,1]
	v_or_b32_e32 v5, 1, v4
	s_mov_b64 s[62:63], 0
	ds_write_b128 v156, v[162:165]
.LBB0_1539:
	s_andn2_b64 vcc, exec, s[62:63]
	v_add_u32_e32 v157, -8, v154
	s_cbranch_vccnz .LBB0_1553
	s_waitcnt vmcnt(62)
	v_cvt_pk_bf16_f32 v0, v12, v14
	s_waitcnt vmcnt(60)
	v_cvt_pk_bf16_f32 v1, v16, v18
	s_waitcnt vmcnt(58)
	v_cvt_pk_bf16_f32 v2, v20, v22
	v_cndmask_b32_e64 v0, 0, v0, s[6:7]
	v_cndmask_b32_e64 v1, 0, v1, s[6:7]
	v_cndmask_b32_e64 v2, 0, v2, s[6:7]
	s_and_saveexec_b64 s[0:1], s[8:9]
	s_xor_b64 s[62:63], exec, s[0:1]
	v_xor_b32_e32 v4, v157, v143
	v_mov_b32_e32 v3, s15
	v_lshl_add_u32 v4, v4, 4, v146
	ds_write_b128 v4, v[0:3]
	s_or_saveexec_b64 s[62:63], s[62:63]
	v_mov_b32_e32 v4, 0
	s_xor_b64 exec, exec, s[62:63]
	s_cbranch_execz .LBB0_1544
	v_xor_b32_e32 v4, v157, v143
	s_waitcnt vmcnt(56)
	v_cvt_pk_bf16_f32 v3, v24, v26
	v_lshl_add_u32 v4, v4, 4, v146
	ds_write_b128 v4, v[0:3]
	s_waitcnt vmcnt(54)
	v_cvt_pk_bf16_f32 v4, v28, v30
.LBB0_1544:
	s_or_b64 exec, exec, s[62:63]
	s_waitcnt vmcnt(52)
	v_cvt_pk_bf16_f32 v0, v32, v34
	v_cndmask_b32_e64 v5, 0, v0, s[6:7]
	s_waitcnt vmcnt(50)
	v_cvt_pk_bf16_f32 v0, v36, v38
	v_cndmask_b32_e64 v6, 0, v0, s[6:7]
	s_and_saveexec_b64 s[0:1], s[8:9]
	s_xor_b64 s[62:63], exec, s[0:1]
	v_add_u32_e32 v0, -7, v154
	v_xor_b32_e32 v0, v0, v143
	v_mov_b32_e32 v7, s15
	v_lshl_add_u32 v0, v0, 4, v146
	ds_write_b128 v0, v[4:7]
	s_or_saveexec_b64 s[62:63], s[62:63]
	v_mov_b32_e32 v2, 0
	s_xor_b64 exec, exec, s[62:63]
	s_cbranch_execz .LBB0_1548
	v_add_u32_e32 v0, -7, v154
	v_xor_b32_e32 v0, v0, v143
	s_waitcnt vmcnt(48)
	v_cvt_pk_bf16_f32 v7, v40, v42
	v_lshl_add_u32 v0, v0, 4, v146
	s_waitcnt vmcnt(46)
	v_cvt_pk_bf16_f32 v2, v44, v46
	ds_write_b128 v0, v[4:7]
.LBB0_1548:
	s_or_b64 exec, exec, s[62:63]
	s_waitcnt vmcnt(44)
	v_cvt_pk_bf16_f32 v0, v48, v50
	v_cndmask_b32_e64 v3, 0, v0, s[6:7]
	s_waitcnt vmcnt(42)
	v_cvt_pk_bf16_f32 v0, v52, v54
	v_cndmask_b32_e64 v4, 0, v0, s[6:7]
	s_and_saveexec_b64 s[0:1], s[8:9]
	s_xor_b64 s[62:63], exec, s[0:1]
	v_add_u32_e32 v0, -6, v154
	v_xor_b32_e32 v0, v0, v143
	v_mov_b32_e32 v5, s15
	v_lshl_add_u32 v0, v0, 4, v146
	ds_write_b128 v0, v[2:5]
	s_or_saveexec_b64 s[62:63], s[62:63]
	v_mov_b32_e32 v0, 0
	s_xor_b64 exec, exec, s[62:63]
	s_cbranch_execz .LBB0_1552
	v_add_u32_e32 v0, -6, v154
	v_xor_b32_e32 v0, v0, v143
	s_waitcnt vmcnt(40)
	v_cvt_pk_bf16_f32 v5, v56, v58
	v_lshl_add_u32 v0, v0, 4, v146
	ds_write_b128 v0, v[2:5]
	s_waitcnt vmcnt(38)
	v_cvt_pk_bf16_f32 v0, v60, v62
.LBB0_1552:
	s_or_b64 exec, exec, s[62:63]
	s_waitcnt vmcnt(36)
	v_cvt_pk_bf16_f32 v1, v64, v74
	s_waitcnt vmcnt(34)
	v_cvt_pk_bf16_f32 v2, v76, v78
	s_waitcnt vmcnt(32)
	v_cvt_pk_bf16_f32 v3, v80, v88
	v_cndmask_b32_e64 v1, 0, v1, s[6:7]
	v_cndmask_b32_e64 v2, 0, v2, s[6:7]
	v_cndmask_b32_e64 v3, 0, v3, s[6:7]
	v_add_u32_e32 v5, -5, v154
.LBB0_1553:
	v_xor_b32_e32 v4, v5, v143
	v_lshl_add_u32 v4, v4, 4, v146
	s_and_b64 vcc, exec, s[10:11]
	s_mov_b64 s[62:63], -1
	ds_write_b128 v4, v[0:3]
	s_cbranch_vccnz .LBB0_1555
	s_waitcnt vmcnt(62)
	v_mul_f32_e32 v0, 0x43800000, v13
	s_waitcnt vmcnt(62)
	v_mul_f32_e32 v1, 0x43800000, v15
	v_mov_b32_e32 v4, 0
	v_cvt_pk_fp8_f32 v4, v0, v1
	s_waitcnt vmcnt(59)
	v_mul_f32_e32 v0, 0x43800000, v21
	s_waitcnt vmcnt(58)
	v_mul_f32_e32 v1, 0x43800000, v23
	v_mov_b32_e32 v5, 0
	v_cvt_pk_fp8_f32 v5, v0, v1
	s_waitcnt vmcnt(57)
	v_mul_f32_e32 v0, 0x43800000, v25
	s_waitcnt vmcnt(56)
	v_mul_f32_e32 v1, 0x43800000, v27
	v_mov_b32_e32 v6, 0
	v_cvt_pk_fp8_f32 v5, v0, v1 op_sel:[0,0,1]
	s_waitcnt vmcnt(55)
	v_mul_f32_e32 v0, 0x43800000, v29
	s_waitcnt vmcnt(54)
	v_mul_f32_e32 v1, 0x43800000, v31
	v_cvt_pk_fp8_f32 v6, v0, v1
	s_waitcnt vmcnt(51)
	v_mul_f32_e32 v0, 0x43800000, v37
	s_waitcnt vmcnt(50)
	v_mul_f32_e32 v1, 0x43800000, v39
	v_mov_b32_e32 v7, 0
	v_cvt_pk_fp8_f32 v7, v0, v1
	v_mul_f32_e32 v2, 0x43800000, v17
	v_mul_f32_e32 v3, 0x43800000, v19
	v_cvt_pk_fp8_f32 v4, v2, v3 op_sel:[0,0,1]
	v_mul_f32_e32 v2, 0x43800000, v33
	v_mul_f32_e32 v3, 0x43800000, v35
	s_waitcnt vmcnt(49)
	v_mul_f32_e32 v0, 0x43800000, v41
	s_waitcnt vmcnt(48)
	v_mul_f32_e32 v1, 0x43800000, v43
	v_cvt_pk_fp8_f32 v6, v2, v3 op_sel:[0,0,1]
	v_cvt_pk_fp8_f32 v7, v0, v1 op_sel:[0,0,1]
	s_waitcnt vmcnt(47)
	v_mul_f32_e32 v1, 0x43800000, v45
	s_waitcnt vmcnt(46)
	v_mul_f32_e32 v2, 0x43800000, v47
	v_mov_b32_e32 v0, 0
	v_cvt_pk_fp8_f32 v0, v1, v2
	s_waitcnt vmcnt(43)
	v_mul_f32_e32 v2, 0x43800000, v53
	s_waitcnt vmcnt(42)
	v_mul_f32_e32 v159, 0x43800000, v55
	v_mov_b32_e32 v1, 0
	v_cvt_pk_fp8_f32 v1, v2, v159
	v_mul_f32_e32 v3, 0x43800000, v49
	v_mul_f32_e32 v158, 0x43800000, v51
	v_cvt_pk_fp8_f32 v0, v3, v158 op_sel:[0,0,1]
	s_waitcnt vmcnt(41)
	v_mul_f32_e32 v2, 0x43800000, v57
	s_waitcnt vmcnt(40)
	v_mul_f32_e32 v3, 0x43800000, v59
	v_cvt_pk_fp8_f32 v1, v2, v3 op_sel:[0,0,1]
	s_waitcnt vmcnt(39)
	v_mul_f32_e32 v3, 0x43800000, v61
	s_waitcnt vmcnt(38)
	v_mul_f32_e32 v158, 0x43800000, v63
	v_mov_b32_e32 v2, 0
	v_cvt_pk_fp8_f32 v2, v3, v158
	s_waitcnt vmcnt(35)
	v_mul_f32_e32 v158, 0x43800000, v77
	s_waitcnt vmcnt(34)
	v_mul_f32_e32 v163, 0x43800000, v79
	v_mov_b32_e32 v3, 0
	v_cvt_pk_fp8_f32 v3, v158, v163
	v_mul_f32_e32 v159, 0x43800000, v65
	v_mul_f32_e32 v162, 0x43800000, v75
	v_cvt_pk_fp8_f32 v2, v159, v162 op_sel:[0,0,1]
	s_waitcnt vmcnt(33)
	v_mul_f32_e32 v158, 0x43800000, v81
	s_waitcnt vmcnt(32)
	v_mul_f32_e32 v159, 0x43800000, v89
	v_cvt_pk_fp8_f32 v3, v158, v159 op_sel:[0,0,1]
	s_mov_b64 s[62:63], 0
	ds_write_b128 v156, v[4:7] offset:512
.LBB0_1555:
	s_andn2_b64 vcc, exec, s[62:63]
	s_cbranch_vccnz .LBB0_1569
	s_waitcnt vmcnt(62)
	v_cvt_pk_bf16_f32 v0, v13, v15
	s_waitcnt vmcnt(60)
	v_cvt_pk_bf16_f32 v1, v17, v19
	s_waitcnt vmcnt(58)
	v_cvt_pk_bf16_f32 v2, v21, v23
	v_xor_b32_e32 v3, v157, v143
	v_cndmask_b32_e64 v0, 0, v0, s[6:7]
	v_cndmask_b32_e64 v1, 0, v1, s[6:7]
	v_cndmask_b32_e64 v2, 0, v2, s[6:7]
	v_lshl_add_u32 v5, v3, 4, v146
	s_and_saveexec_b64 s[0:1], s[8:9]
	s_xor_b64 s[62:63], exec, s[0:1]
	v_mov_b32_e32 v3, s15
	ds_write_b128 v5, v[0:3] offset:512
	s_or_saveexec_b64 s[62:63], s[62:63]
	v_mov_b32_e32 v4, 0
	s_xor_b64 exec, exec, s[62:63]
	s_cbranch_execz .LBB0_1560
	s_waitcnt vmcnt(56)
	v_cvt_pk_bf16_f32 v3, v25, v27
	s_waitcnt vmcnt(54)
	v_cvt_pk_bf16_f32 v4, v29, v31
	ds_write_b128 v5, v[0:3] offset:512
.LBB0_1560:
	s_or_b64 exec, exec, s[62:63]
	s_waitcnt vmcnt(52)
	v_cvt_pk_bf16_f32 v0, v33, v35
	v_cndmask_b32_e64 v5, 0, v0, s[6:7]
	s_waitcnt vmcnt(50)
	v_cvt_pk_bf16_f32 v0, v37, v39
	v_cndmask_b32_e64 v6, 0, v0, s[6:7]
	v_add_u32_e32 v0, -7, v154
	v_xor_b32_e32 v0, v0, v143
	s_and_saveexec_b64 s[0:1], s[8:9]
	s_xor_b64 s[62:63], exec, s[0:1]
	v_mov_b32_e32 v7, s15
	v_lshl_add_u32 v0, v0, 4, v146
	ds_write_b128 v0, v[4:7] offset:512
	s_or_saveexec_b64 s[62:63], s[62:63]
	v_mov_b32_e32 v2, 0
	s_xor_b64 exec, exec, s[62:63]
	s_cbranch_execz .LBB0_1564
	s_waitcnt vmcnt(48)
	v_cvt_pk_bf16_f32 v7, v41, v43
	v_lshl_add_u32 v0, v0, 4, v146
	s_waitcnt vmcnt(46)
	v_cvt_pk_bf16_f32 v2, v45, v47
	ds_write_b128 v0, v[4:7] offset:512
.LBB0_1564:
	s_or_b64 exec, exec, s[62:63]
	s_waitcnt vmcnt(44)
	v_cvt_pk_bf16_f32 v0, v49, v51
	v_cndmask_b32_e64 v3, 0, v0, s[6:7]
	s_waitcnt vmcnt(42)
	v_cvt_pk_bf16_f32 v0, v53, v55
	v_cndmask_b32_e64 v4, 0, v0, s[6:7]
	v_add_u32_e32 v0, -6, v154
	v_xor_b32_e32 v1, v0, v143
	s_and_saveexec_b64 s[0:1], s[8:9]
	s_xor_b64 s[62:63], exec, s[0:1]
	v_mov_b32_e32 v5, s15
	v_lshl_add_u32 v0, v1, 4, v146
	ds_write_b128 v0, v[2:5] offset:512
	s_or_saveexec_b64 s[62:63], s[62:63]
	v_mov_b32_e32 v0, 0
	s_xor_b64 exec, exec, s[62:63]
	s_cbranch_execz .LBB0_1568
	s_waitcnt vmcnt(40)
	v_cvt_pk_bf16_f32 v5, v57, v59
	v_lshl_add_u32 v0, v1, 4, v146
	ds_write_b128 v0, v[2:5] offset:512
	s_waitcnt vmcnt(38)
	v_cvt_pk_bf16_f32 v0, v61, v63
.LBB0_1568:
	s_or_b64 exec, exec, s[62:63]
	s_waitcnt vmcnt(36)
	v_cvt_pk_bf16_f32 v1, v65, v75
	s_waitcnt vmcnt(34)
	v_cvt_pk_bf16_f32 v2, v77, v79
	s_waitcnt vmcnt(32)
	v_cvt_pk_bf16_f32 v3, v81, v89
	v_cndmask_b32_e64 v1, 0, v1, s[6:7]
	v_cndmask_b32_e64 v2, 0, v2, s[6:7]
	v_cndmask_b32_e64 v3, 0, v3, s[6:7]
	v_add_u32_e32 v155, -5, v154

.LBB0_1571:
	s_lshl_b32 s0, s21, 2
	v_add_u32_e32 v0, 4, v153
	v_add3_u32 v4, v145, s0, 4
	v_xor_b32_e32 v0, v0, v143
	s_mov_b64 s[62:63], -1
	s_and_b64 vcc, exec, s[10:11]
	v_lshl_add_u32 v156, v0, 4, v146
	v_or_b32_e32 v155, 1, v4
	s_cbranch_vccnz .LBB0_1573
	s_waitcnt vmcnt(62)
	v_mul_f32_e32 v0, 0x43800000, v66
	s_waitcnt vmcnt(62)
	v_mul_f32_e32 v1, 0x43800000, v68
	v_mov_b32_e32 v162, 0
	v_cvt_pk_fp8_f32 v162, v0, v1
	s_waitcnt vmcnt(59)
	v_mul_f32_e32 v0, 0x43800000, v82
	s_waitcnt vmcnt(58)
	v_mul_f32_e32 v1, 0x43800000, v84
	v_mov_b32_e32 v163, 0
	v_cvt_pk_fp8_f32 v163, v0, v1
	s_waitcnt vmcnt(57)
	v_mul_f32_e32 v0, 0x43800000, v86
	s_waitcnt vmcnt(56)
	v_mul_f32_e32 v1, 0x43800000, v90
	v_mov_b32_e32 v164, 0
	v_cvt_pk_fp8_f32 v163, v0, v1 op_sel:[0,0,1]
	s_waitcnt vmcnt(55)
	v_mul_f32_e32 v0, 0x43800000, v92
	s_waitcnt vmcnt(54)
	v_mul_f32_e32 v1, 0x43800000, v94
	v_cvt_pk_fp8_f32 v164, v0, v1
	s_waitcnt vmcnt(51)
	v_mul_f32_e32 v0, 0x43800000, v100
	s_waitcnt vmcnt(50)
	v_mul_f32_e32 v1, 0x43800000, v102
	v_mov_b32_e32 v165, 0
	v_cvt_pk_fp8_f32 v165, v0, v1
	v_mul_f32_e32 v2, 0x43800000, v70
	v_mul_f32_e32 v3, 0x43800000, v72
	v_cvt_pk_fp8_f32 v162, v2, v3 op_sel:[0,0,1]
	v_mul_f32_e32 v2, 0x43800000, v96
	v_mul_f32_e32 v3, 0x43800000, v98
	s_waitcnt vmcnt(49)
	v_mul_f32_e32 v0, 0x43800000, v104
	s_waitcnt vmcnt(48)
	v_mul_f32_e32 v1, 0x43800000, v106
	v_cvt_pk_fp8_f32 v164, v2, v3 op_sel:[0,0,1]
	v_cvt_pk_fp8_f32 v165, v0, v1 op_sel:[0,0,1]
	s_waitcnt vmcnt(47)
	v_mul_f32_e32 v1, 0x43800000, v108
	s_waitcnt vmcnt(46)
	v_mul_f32_e32 v2, 0x43800000, v110
	v_mov_b32_e32 v0, 0
	v_cvt_pk_fp8_f32 v0, v1, v2
	s_waitcnt vmcnt(43)
	v_mul_f32_e32 v2, 0x43800000, v116
	s_waitcnt vmcnt(42)
	v_mul_f32_e32 v6, 0x43800000, v118
	v_mov_b32_e32 v1, 0
	v_cvt_pk_fp8_f32 v1, v2, v6
	v_mul_f32_e32 v3, 0x43800000, v112
	v_mul_f32_e32 v5, 0x43800000, v114
	v_cvt_pk_fp8_f32 v0, v3, v5 op_sel:[0,0,1]
	s_waitcnt vmcnt(41)
	v_mul_f32_e32 v2, 0x43800000, v120
	s_waitcnt vmcnt(40)
	v_mul_f32_e32 v3, 0x43800000, v122
	v_cvt_pk_fp8_f32 v1, v2, v3 op_sel:[0,0,1]
	s_waitcnt vmcnt(39)
	v_mul_f32_e32 v3, 0x43800000, v124
	s_waitcnt vmcnt(38)
	v_mul_f32_e32 v5, 0x43800000, v126
	v_mov_b32_e32 v2, 0
	v_cvt_pk_fp8_f32 v2, v3, v5
	s_waitcnt vmcnt(35)
	v_mul_f32_e32 v5, 0x43800000, v132
	s_waitcnt vmcnt(34)
	v_mul_f32_e32 v157, 0x43800000, v134
	v_mov_b32_e32 v3, 0
	v_cvt_pk_fp8_f32 v3, v5, v157
	v_mul_f32_e32 v6, 0x43800000, v128
	v_mul_f32_e32 v7, 0x43800000, v130
	v_cvt_pk_fp8_f32 v2, v6, v7 op_sel:[0,0,1]
	s_waitcnt vmcnt(33)
	v_mul_f32_e32 v5, 0x43800000, v136
	s_waitcnt vmcnt(32)
	v_mul_f32_e32 v6, 0x43800000, v138
	v_cvt_pk_fp8_f32 v3, v5, v6 op_sel:[0,0,1]
	v_or_b32_e32 v5, 1, v4
	s_mov_b64 s[62:63], 0
	ds_write_b128 v156, v[162:165]
.LBB0_1573:
	s_andn2_b64 vcc, exec, s[62:63]
	s_cbranch_vccnz .LBB0_1587
	s_waitcnt vmcnt(62)
	v_cvt_pk_bf16_f32 v0, v66, v68
	s_waitcnt vmcnt(60)
	v_cvt_pk_bf16_f32 v1, v70, v72
	s_waitcnt vmcnt(58)
	v_cvt_pk_bf16_f32 v2, v82, v84
	v_cndmask_b32_e64 v0, 0, v0, s[6:7]
	v_cndmask_b32_e64 v1, 0, v1, s[6:7]
	v_cndmask_b32_e64 v2, 0, v2, s[6:7]
	s_and_saveexec_b64 s[0:1], s[8:9]
	s_xor_b64 s[62:63], exec, s[0:1]
	v_xor_b32_e32 v4, v154, v143
	v_mov_b32_e32 v3, s15
	v_lshl_add_u32 v4, v4, 4, v146
	ds_write_b128 v4, v[0:3]
	s_or_saveexec_b64 s[62:63], s[62:63]
	v_mov_b32_e32 v4, 0
	s_xor_b64 exec, exec, s[62:63]
	s_cbranch_execz .LBB0_1578
	v_xor_b32_e32 v4, v154, v143
	s_waitcnt vmcnt(56)
	v_cvt_pk_bf16_f32 v3, v86, v90
	v_lshl_add_u32 v4, v4, 4, v146
	ds_write_b128 v4, v[0:3]
	s_waitcnt vmcnt(54)
	v_cvt_pk_bf16_f32 v4, v92, v94
.LBB0_1578:
	s_or_b64 exec, exec, s[62:63]
	s_waitcnt vmcnt(52)
	v_cvt_pk_bf16_f32 v0, v96, v98
	v_cndmask_b32_e64 v5, 0, v0, s[6:7]
	s_waitcnt vmcnt(50)
	v_cvt_pk_bf16_f32 v0, v100, v102
	v_cndmask_b32_e64 v6, 0, v0, s[6:7]
	s_and_saveexec_b64 s[0:1], s[8:9]
	s_xor_b64 s[62:63], exec, s[0:1]
	v_add_u32_e32 v0, 1, v154
	v_xor_b32_e32 v0, v0, v143
	v_mov_b32_e32 v7, s15
	v_lshl_add_u32 v0, v0, 4, v146
	ds_write_b128 v0, v[4:7]
	s_or_saveexec_b64 s[62:63], s[62:63]
	v_mov_b32_e32 v2, 0
	s_xor_b64 exec, exec, s[62:63]
	s_cbranch_execz .LBB0_1582
	v_add_u32_e32 v0, 1, v154
	v_xor_b32_e32 v0, v0, v143
	s_waitcnt vmcnt(48)
	v_cvt_pk_bf16_f32 v7, v104, v106
	v_lshl_add_u32 v0, v0, 4, v146
	s_waitcnt vmcnt(46)
	v_cvt_pk_bf16_f32 v2, v108, v110
	ds_write_b128 v0, v[4:7]
.LBB0_1582:
	s_or_b64 exec, exec, s[62:63]
	s_waitcnt vmcnt(44)
	v_cvt_pk_bf16_f32 v0, v112, v114
	v_cndmask_b32_e64 v3, 0, v0, s[6:7]
	s_waitcnt vmcnt(42)
	v_cvt_pk_bf16_f32 v0, v116, v118
	v_cndmask_b32_e64 v4, 0, v0, s[6:7]
	s_and_saveexec_b64 s[0:1], s[8:9]
	s_xor_b64 s[62:63], exec, s[0:1]
	v_add_u32_e32 v0, 2, v154
	v_xor_b32_e32 v0, v0, v143
	v_mov_b32_e32 v5, s15
	v_lshl_add_u32 v0, v0, 4, v146
	ds_write_b128 v0, v[2:5]
	s_or_saveexec_b64 s[62:63], s[62:63]
	v_mov_b32_e32 v0, 0
	s_xor_b64 exec, exec, s[62:63]
	s_cbranch_execz .LBB0_1586
	v_add_u32_e32 v0, 2, v154
	v_xor_b32_e32 v0, v0, v143
	s_waitcnt vmcnt(40)
	v_cvt_pk_bf16_f32 v5, v120, v122
	v_lshl_add_u32 v0, v0, 4, v146
	ds_write_b128 v0, v[2:5]
	s_waitcnt vmcnt(38)
	v_cvt_pk_bf16_f32 v0, v124, v126
.LBB0_1586:
	s_or_b64 exec, exec, s[62:63]
	s_waitcnt vmcnt(36)
	v_cvt_pk_bf16_f32 v1, v128, v130
	s_waitcnt vmcnt(34)
	v_cvt_pk_bf16_f32 v2, v132, v134
	s_waitcnt vmcnt(32)
	v_cvt_pk_bf16_f32 v3, v136, v138
	v_cndmask_b32_e64 v1, 0, v1, s[6:7]
	v_cndmask_b32_e64 v2, 0, v2, s[6:7]
	v_cndmask_b32_e64 v3, 0, v3, s[6:7]
	v_add_u32_e32 v5, 3, v154
.LBB0_1587:
	v_xor_b32_e32 v4, v5, v143
	v_lshl_add_u32 v4, v4, 4, v146
	s_and_b64 vcc, exec, s[10:11]
	s_mov_b64 s[10:11], -1
	ds_write_b128 v4, v[0:3]
	s_cbranch_vccnz .LBB0_1589
	s_waitcnt vmcnt(62)
	v_mul_f32_e32 v0, 0x43800000, v67
	s_waitcnt vmcnt(62)
	v_mul_f32_e32 v1, 0x43800000, v69
	v_mov_b32_e32 v4, 0
	v_cvt_pk_fp8_f32 v4, v0, v1
	s_waitcnt vmcnt(59)
	v_mul_f32_e32 v0, 0x43800000, v83
	s_waitcnt vmcnt(58)
	v_mul_f32_e32 v1, 0x43800000, v85
	v_mov_b32_e32 v5, 0
	v_cvt_pk_fp8_f32 v5, v0, v1
	s_waitcnt vmcnt(57)
	v_mul_f32_e32 v0, 0x43800000, v87
	s_waitcnt vmcnt(56)
	v_mul_f32_e32 v1, 0x43800000, v91
	v_mov_b32_e32 v6, 0
	v_cvt_pk_fp8_f32 v5, v0, v1 op_sel:[0,0,1]
	s_waitcnt vmcnt(55)
	v_mul_f32_e32 v0, 0x43800000, v93
	s_waitcnt vmcnt(54)
	v_mul_f32_e32 v1, 0x43800000, v95
	v_cvt_pk_fp8_f32 v6, v0, v1
	s_waitcnt vmcnt(51)
	v_mul_f32_e32 v0, 0x43800000, v101
	s_waitcnt vmcnt(50)
	v_mul_f32_e32 v1, 0x43800000, v103
	v_mov_b32_e32 v7, 0
	v_cvt_pk_fp8_f32 v7, v0, v1
	v_mul_f32_e32 v2, 0x43800000, v71
	v_mul_f32_e32 v3, 0x43800000, v73
	v_cvt_pk_fp8_f32 v4, v2, v3 op_sel:[0,0,1]
	v_mul_f32_e32 v2, 0x43800000, v97
	v_mul_f32_e32 v3, 0x43800000, v99
	s_waitcnt vmcnt(49)
	v_mul_f32_e32 v0, 0x43800000, v105
	s_waitcnt vmcnt(48)
	v_mul_f32_e32 v1, 0x43800000, v107
	v_cvt_pk_fp8_f32 v6, v2, v3 op_sel:[0,0,1]
	v_cvt_pk_fp8_f32 v7, v0, v1 op_sel:[0,0,1]
	s_waitcnt vmcnt(47)
	v_mul_f32_e32 v1, 0x43800000, v109
	s_waitcnt vmcnt(46)
	v_mul_f32_e32 v2, 0x43800000, v111
	v_mov_b32_e32 v0, 0
	v_cvt_pk_fp8_f32 v0, v1, v2
	s_waitcnt vmcnt(43)
	v_mul_f32_e32 v2, 0x43800000, v117
	s_waitcnt vmcnt(42)
	v_mul_f32_e32 v158, 0x43800000, v119
	v_mov_b32_e32 v1, 0
	v_cvt_pk_fp8_f32 v1, v2, v158
	v_mul_f32_e32 v3, 0x43800000, v113
	v_mul_f32_e32 v157, 0x43800000, v115
	v_cvt_pk_fp8_f32 v0, v3, v157 op_sel:[0,0,1]
	s_waitcnt vmcnt(41)
	v_mul_f32_e32 v2, 0x43800000, v121
	s_waitcnt vmcnt(40)
	v_mul_f32_e32 v3, 0x43800000, v123
	v_cvt_pk_fp8_f32 v1, v2, v3 op_sel:[0,0,1]
	s_waitcnt vmcnt(39)
	v_mul_f32_e32 v3, 0x43800000, v125
	s_waitcnt vmcnt(38)
	v_mul_f32_e32 v157, 0x43800000, v127
	v_mov_b32_e32 v2, 0
	v_cvt_pk_fp8_f32 v2, v3, v157
	s_waitcnt vmcnt(35)
	v_mul_f32_e32 v157, 0x43800000, v133
	s_waitcnt vmcnt(34)
	v_mul_f32_e32 v162, 0x43800000, v135
	v_mov_b32_e32 v3, 0
	v_cvt_pk_fp8_f32 v3, v157, v162
	v_mul_f32_e32 v158, 0x43800000, v129
	v_mul_f32_e32 v159, 0x43800000, v131
	v_cvt_pk_fp8_f32 v2, v158, v159 op_sel:[0,0,1]
	s_waitcnt vmcnt(33)
	v_mul_f32_e32 v157, 0x43800000, v137
	s_waitcnt vmcnt(32)
	v_mul_f32_e32 v158, 0x43800000, v139
	v_cvt_pk_fp8_f32 v3, v157, v158 op_sel:[0,0,1]
	s_mov_b64 s[10:11], 0
	ds_write_b128 v156, v[4:7] offset:512
.LBB0_1589:
	s_andn2_b64 vcc, exec, s[10:11]
	s_cbranch_vccnz .LBB0_1603
	s_waitcnt vmcnt(62)
	v_cvt_pk_bf16_f32 v0, v67, v69
	s_waitcnt vmcnt(60)
	v_cvt_pk_bf16_f32 v1, v71, v73
	s_waitcnt vmcnt(58)
	v_cvt_pk_bf16_f32 v2, v83, v85
	v_xor_b32_e32 v3, v154, v143
	v_cndmask_b32_e64 v0, 0, v0, s[6:7]
	v_cndmask_b32_e64 v1, 0, v1, s[6:7]
	v_cndmask_b32_e64 v2, 0, v2, s[6:7]
	v_lshl_add_u32 v5, v3, 4, v146
	s_and_saveexec_b64 s[0:1], s[8:9]
	s_xor_b64 s[10:11], exec, s[0:1]
	v_mov_b32_e32 v3, s15
	ds_write_b128 v5, v[0:3] offset:512
	s_or_saveexec_b64 s[10:11], s[10:11]
	v_mov_b32_e32 v4, 0
	s_xor_b64 exec, exec, s[10:11]
	s_cbranch_execz .LBB0_1594
	s_waitcnt vmcnt(56)
	v_cvt_pk_bf16_f32 v3, v87, v91
	s_waitcnt vmcnt(54)
	v_cvt_pk_bf16_f32 v4, v93, v95
	ds_write_b128 v5, v[0:3] offset:512
.LBB0_1594:
	s_or_b64 exec, exec, s[10:11]
	s_waitcnt vmcnt(52)
	v_cvt_pk_bf16_f32 v0, v97, v99
	v_cndmask_b32_e64 v5, 0, v0, s[6:7]
	s_waitcnt vmcnt(50)
	v_cvt_pk_bf16_f32 v0, v101, v103
	v_cndmask_b32_e64 v6, 0, v0, s[6:7]
	v_add_u32_e32 v0, 1, v154
	v_xor_b32_e32 v0, v0, v143
	s_and_saveexec_b64 s[0:1], s[8:9]
	s_xor_b64 s[10:11], exec, s[0:1]
	v_mov_b32_e32 v7, s15
	v_lshl_add_u32 v0, v0, 4, v146
	ds_write_b128 v0, v[4:7] offset:512
	s_or_saveexec_b64 s[10:11], s[10:11]
	v_mov_b32_e32 v2, 0
	s_xor_b64 exec, exec, s[10:11]
	s_cbranch_execz .LBB0_1598
	s_waitcnt vmcnt(48)
	v_cvt_pk_bf16_f32 v7, v105, v107
	v_lshl_add_u32 v0, v0, 4, v146
	s_waitcnt vmcnt(46)
	v_cvt_pk_bf16_f32 v2, v109, v111
	ds_write_b128 v0, v[4:7] offset:512
.LBB0_1598:
	s_or_b64 exec, exec, s[10:11]
	s_waitcnt vmcnt(44)
	v_cvt_pk_bf16_f32 v0, v113, v115
	v_cndmask_b32_e64 v3, 0, v0, s[6:7]
	s_waitcnt vmcnt(42)
	v_cvt_pk_bf16_f32 v0, v117, v119
	v_cndmask_b32_e64 v4, 0, v0, s[6:7]
	v_add_u32_e32 v0, 2, v154
	v_xor_b32_e32 v1, v0, v143
	s_and_saveexec_b64 s[0:1], s[8:9]
	s_xor_b64 s[10:11], exec, s[0:1]
	v_mov_b32_e32 v5, s15
	v_lshl_add_u32 v0, v1, 4, v146
	ds_write_b128 v0, v[2:5] offset:512
	s_or_saveexec_b64 s[10:11], s[10:11]
	v_mov_b32_e32 v0, 0
	s_xor_b64 exec, exec, s[10:11]
	s_cbranch_execz .LBB0_1602
	s_waitcnt vmcnt(40)
	v_cvt_pk_bf16_f32 v5, v121, v123
	v_lshl_add_u32 v0, v1, 4, v146
	ds_write_b128 v0, v[2:5] offset:512
	s_waitcnt vmcnt(38)
	v_cvt_pk_bf16_f32 v0, v125, v127
.LBB0_1602:
	s_or_b64 exec, exec, s[10:11]
	s_waitcnt vmcnt(36)
	v_cvt_pk_bf16_f32 v1, v129, v131
	s_waitcnt vmcnt(34)
	v_cvt_pk_bf16_f32 v2, v133, v135
	s_waitcnt vmcnt(32)
	v_cvt_pk_bf16_f32 v3, v137, v139
	v_cndmask_b32_e64 v1, 0, v1, s[6:7]
	v_cndmask_b32_e64 v2, 0, v2, s[6:7]
	v_cndmask_b32_e64 v3, 0, v3, s[6:7]
	v_add_u32_e32 v155, 3, v154

.LBB0_1819:
	s_and_b32 s0, s16, 1
	s_mul_i32 s1, s0, 0xa000
	v_add_u32_e32 v8, s1, v4
	s_lshl_b32 s4, s0, 11
	v_add_u32_e32 v9, s4, v5
	s_add_i32 s16, s16, 1
	ds_read_b128 v[12:15], v8 offset:0
	ds_read_b128 v[16:19], v8 offset:256
	ds_read_b128 v[20:23], v8 offset:512
	ds_read_b128 v[24:27], v8 offset:768
	ds_read2_b32 v[72:73], v9 offset1:16
	ds_read_b128 v[32:35], v8 offset:1280
	ds_read_b128 v[36:39], v8 offset:1536
	ds_read_b128 v[40:43], v8 offset:1792
	ds_read_b128 v[44:47], v8 offset:2048
	v_add_u32_e32 v10, 0x400, v9
	v_add_u32_e32 v11, s4, v6
	ds_read_b128 v[28:31], v8 offset:1024
	ds_read_b128 v[48:51], v8 offset:2304
	s_waitcnt lgkmcnt(6)
	v_pk_mul_f32 v[76:77], v[24:25], v[72:73] op_sel_hi:[1,0]
	v_pk_mul_f32 v[78:79], v[26:27], v[72:73] op_sel_hi:[1,0]
	v_pk_mul_f32 v[84:85], v[0:1], v[12:13]
	ds_read_b128 v[52:55], v8 offset:2560
	ds_read_b128 v[56:59], v8 offset:2816
	v_pk_fma_f32 v[84:85], v[2:3], v[14:15], v[84:85]
	v_pk_fma_f32 v[76:77], v[0:1], v[16:17], v[76:77]
	v_add_f32_e32 v86, v84, v85
	v_pk_fma_f32 v[78:79], v[2:3], v[18:19], v[78:79]
	ds_read_b128 v[68:71], v8 offset:3584
	v_add_f32_dpp v86, v86, v86 quad_perm:[1,0,3,2] row_mask:0xf bank_mask:0xf bound_ctrl:1
	ds_read_b128 v[60:63], v8 offset:3072
	ds_read_b128 v[64:67], v8 offset:3328
	v_add_f32_dpp v86, v86, v86 quad_perm:[2,3,0,1] row_mask:0xf bank_mask:0xf bound_ctrl:1
	ds_read2_b32 v[74:75], v9 offset0:32 offset1:48
	s_waitcnt lgkmcnt(8)
	v_pk_mul_f32 v[80:81], v[44:45], v[72:73] op_sel:[0,1] op_sel_hi:[1,1]
	v_add_f32_dpp v86, v86, v86 row_half_mirror row_mask:0xf bank_mask:0xf bound_ctrl:1
	v_pk_mul_f32 v[82:83], v[46:47], v[72:73] op_sel:[0,1] op_sel_hi:[1,1]
	ds_read_b128 v[12:15], v8 offset:3840
	v_add_f32_dpp v86, v86, v86 row_mirror row_mask:0xf bank_mask:0xf bound_ctrl:1
	ds_read_b128 v[16:19], v8 offset:4096
	v_pk_fma_f32 v[0:1], v[20:21], v[86:87], v[76:77] op_sel_hi:[1,0,1]
	v_pk_fma_f32 v[2:3], v[22:23], v[86:87], v[78:79] op_sel_hi:[1,0,1]
	v_pk_mul_f32 v[84:85], v[0:1], v[32:33]
	v_pk_fma_f32 v[80:81], v[0:1], v[36:37], v[80:81]
	v_pk_fma_f32 v[84:85], v[2:3], v[34:35], v[84:85]
	s_waitcnt lgkmcnt(9)
	v_pk_mul_f32 v[88:89], v[0:1], v[28:29]
	v_add_f32_e32 v86, v84, v85
	v_pk_fma_f32 v[82:83], v[2:3], v[38:39], v[82:83]
	v_pk_fma_f32 v[88:89], v[2:3], v[30:31], v[88:89]
	v_add_f32_dpp v86, v86, v86 quad_perm:[1,0,3,2] row_mask:0xf bank_mask:0xf bound_ctrl:1
	ds_read_b128 v[28:31], v8 offset:4864
	v_add_f32_e32 v90, v88, v89
	v_add_f32_dpp v86, v86, v86 quad_perm:[2,3,0,1] row_mask:0xf bank_mask:0xf bound_ctrl:1
	ds_read_b128 v[20:23], v8 offset:4352
	ds_read_b128 v[24:27], v8 offset:4608
	v_add_f32_dpp v86, v86, v86 row_half_mirror row_mask:0xf bank_mask:0xf bound_ctrl:1
	s_waitcnt lgkmcnt(5)
	v_pk_mul_f32 v[76:77], v[64:65], v[74:75] op_sel_hi:[1,0]
	v_pk_mul_f32 v[78:79], v[66:67], v[74:75] op_sel_hi:[1,0]
	v_add_f32_dpp v86, v86, v86 row_mirror row_mask:0xf bank_mask:0xf bound_ctrl:1
	ds_read_b128 v[32:35], v8 offset:5120
	v_pk_fma_f32 v[0:1], v[40:41], v[86:87], v[80:81] op_sel_hi:[1,0,1]
	v_pk_fma_f32 v[2:3], v[42:43], v[86:87], v[82:83] op_sel_hi:[1,0,1]
	v_pk_mul_f32 v[84:85], v[0:1], v[52:53]
	ds_read_b128 v[36:39], v8 offset:5376
	v_pk_fma_f32 v[84:85], v[2:3], v[54:55], v[84:85]
	v_pk_fma_f32 v[76:77], v[0:1], v[56:57], v[76:77]
	v_add_f32_e32 v86, v84, v85
	v_pk_mul_f32 v[88:89], v[0:1], v[48:49]
	v_pk_fma_f32 v[78:79], v[2:3], v[58:59], v[78:79]
	v_add_f32_dpp v86, v86, v86 quad_perm:[1,0,3,2] row_mask:0xf bank_mask:0xf bound_ctrl:1
	v_pk_fma_f32 v[88:89], v[2:3], v[50:51], v[88:89]
	ds_read_b128 v[48:51], v8 offset:6144
	v_add_f32_dpp v86, v86, v86 quad_perm:[2,3,0,1] row_mask:0xf bank_mask:0xf bound_ctrl:1
	v_add_f32_e32 v91, v88, v89
	ds_read_b128 v[40:43], v8 offset:5632
	v_add_f32_dpp v86, v86, v86 row_half_mirror row_mask:0xf bank_mask:0xf bound_ctrl:1
	ds_read_b128 v[44:47], v8 offset:5888
	ds_read2_b32 v[72:73], v9 offset0:64 offset1:80
	v_add_f32_dpp v86, v86, v86 row_mirror row_mask:0xf bank_mask:0xf bound_ctrl:1
	s_waitcnt lgkmcnt(6)
	v_pk_mul_f32 v[80:81], v[24:25], v[74:75] op_sel:[0,1] op_sel_hi:[1,1]
	v_pk_mul_f32 v[82:83], v[26:27], v[74:75] op_sel:[0,1] op_sel_hi:[1,1]
	v_pk_fma_f32 v[0:1], v[60:61], v[86:87], v[76:77] op_sel_hi:[1,0,1]
	v_pk_fma_f32 v[2:3], v[62:63], v[86:87], v[78:79] op_sel_hi:[1,0,1]
	v_pk_mul_f32 v[84:85], v[0:1], v[12:13]
	ds_read_b128 v[52:55], v8 offset:6400
	ds_read_b128 v[56:59], v8 offset:6656
	v_pk_fma_f32 v[84:85], v[2:3], v[14:15], v[84:85]
	v_pk_fma_f32 v[80:81], v[0:1], v[16:17], v[80:81]
	v_add_f32_e32 v86, v84, v85
	v_pk_mul_f32 v[88:89], v[0:1], v[68:69]
	v_pk_fma_f32 v[82:83], v[2:3], v[18:19], v[82:83]
	v_add_f32_dpp v86, v86, v86 quad_perm:[1,0,3,2] row_mask:0xf bank_mask:0xf bound_ctrl:1
	v_pk_fma_f32 v[88:89], v[2:3], v[70:71], v[88:89]
	ds_read_b128 v[68:71], v8 offset:7424
	v_add_f32_dpp v86, v86, v86 quad_perm:[2,3,0,1] row_mask:0xf bank_mask:0xf bound_ctrl:1
	v_add_f32_e32 v92, v88, v89
	ds_read_b128 v[60:63], v8 offset:6912
	v_add_f32_dpp v86, v86, v86 row_half_mirror row_mask:0xf bank_mask:0xf bound_ctrl:1
	ds_read_b128 v[64:67], v8 offset:7168
	s_waitcnt lgkmcnt(5)
	v_pk_mul_f32 v[76:77], v[44:45], v[72:73] op_sel_hi:[1,0]
	v_add_f32_dpp v86, v86, v86 row_mirror row_mask:0xf bank_mask:0xf bound_ctrl:1
	v_pk_mul_f32 v[78:79], v[46:47], v[72:73] op_sel_hi:[1,0]
	v_pk_fma_f32 v[0:1], v[20:21], v[86:87], v[80:81] op_sel_hi:[1,0,1]
	v_pk_fma_f32 v[2:3], v[22:23], v[86:87], v[82:83] op_sel_hi:[1,0,1]
	v_pk_mul_f32 v[84:85], v[0:1], v[32:33]
	ds_read_b128 v[12:15], v8 offset:7680
	ds_read_b128 v[16:19], v8 offset:7936
	v_pk_fma_f32 v[84:85], v[2:3], v[34:35], v[84:85]
	v_pk_fma_f32 v[76:77], v[0:1], v[36:37], v[76:77]
	v_add_f32_e32 v86, v84, v85
	v_pk_mul_f32 v[88:89], v[0:1], v[28:29]
	v_pk_fma_f32 v[78:79], v[2:3], v[38:39], v[78:79]
	v_add_f32_dpp v86, v86, v86 quad_perm:[1,0,3,2] row_mask:0xf bank_mask:0xf bound_ctrl:1
	v_pk_fma_f32 v[88:89], v[2:3], v[30:31], v[88:89]
	ds_read_b128 v[28:31], v8 offset:8704
	v_add_f32_dpp v86, v86, v86 quad_perm:[2,3,0,1] row_mask:0xf bank_mask:0xf bound_ctrl:1
	v_add_f32_e32 v93, v88, v89
	ds_read_b128 v[20:23], v8 offset:8192
	v_add_f32_dpp v86, v86, v86 row_half_mirror row_mask:0xf bank_mask:0xf bound_ctrl:1
	ds_read_b128 v[24:27], v8 offset:8448
	ds_read2_b32 v[74:75], v9 offset0:96 offset1:112
	v_add_f32_dpp v86, v86, v86 row_mirror row_mask:0xf bank_mask:0xf bound_ctrl:1
	s_waitcnt lgkmcnt(6)
	v_pk_mul_f32 v[80:81], v[64:65], v[72:73] op_sel:[0,1] op_sel_hi:[1,1]
	v_pk_mul_f32 v[82:83], v[66:67], v[72:73] op_sel:[0,1] op_sel_hi:[1,1]
	v_pk_fma_f32 v[0:1], v[40:41], v[86:87], v[76:77] op_sel_hi:[1,0,1]
	v_pk_fma_f32 v[2:3], v[42:43], v[86:87], v[78:79] op_sel_hi:[1,0,1]
	v_pk_mul_f32 v[84:85], v[0:1], v[52:53]
	ds_read_b128 v[32:35], v8 offset:8960
	ds_read_b128 v[36:39], v8 offset:9216
	v_pk_fma_f32 v[84:85], v[2:3], v[54:55], v[84:85]
	v_pk_fma_f32 v[80:81], v[0:1], v[56:57], v[80:81]
	v_add_f32_e32 v86, v84, v85
	v_pk_mul_f32 v[88:89], v[0:1], v[48:49]
	v_pk_fma_f32 v[82:83], v[2:3], v[58:59], v[82:83]
	v_add_f32_dpp v86, v86, v86 quad_perm:[1,0,3,2] row_mask:0xf bank_mask:0xf bound_ctrl:1
	v_pk_fma_f32 v[88:89], v[2:3], v[50:51], v[88:89]
	ds_read_b128 v[48:51], v8 offset:9984
	v_add_f32_dpp v86, v86, v86 quad_perm:[2,3,0,1] row_mask:0xf bank_mask:0xf bound_ctrl:1
	v_add_f32_e32 v94, v88, v89
	ds_read_b128 v[40:43], v8 offset:9472
	v_add_f32_dpp v86, v86, v86 row_half_mirror row_mask:0xf bank_mask:0xf bound_ctrl:1
	ds_read_b128 v[44:47], v8 offset:9728
	s_waitcnt lgkmcnt(5)
	v_pk_mul_f32 v[76:77], v[24:25], v[74:75] op_sel_hi:[1,0]
	v_add_f32_dpp v86, v86, v86 row_mirror row_mask:0xf bank_mask:0xf bound_ctrl:1
	v_pk_mul_f32 v[78:79], v[26:27], v[74:75] op_sel_hi:[1,0]
	v_pk_fma_f32 v[0:1], v[60:61], v[86:87], v[80:81] op_sel_hi:[1,0,1]
	v_pk_fma_f32 v[2:3], v[62:63], v[86:87], v[82:83] op_sel_hi:[1,0,1]
	v_pk_mul_f32 v[84:85], v[0:1], v[12:13]
	ds_read_b128 v[52:55], v8 offset:10240
	ds_read_b128 v[56:59], v8 offset:10496
	v_pk_fma_f32 v[84:85], v[2:3], v[14:15], v[84:85]
	v_pk_fma_f32 v[76:77], v[0:1], v[16:17], v[76:77]
	v_add_f32_e32 v86, v84, v85
	v_pk_mul_f32 v[88:89], v[0:1], v[68:69]
	v_pk_fma_f32 v[78:79], v[2:3], v[18:19], v[78:79]
	v_add_f32_dpp v86, v86, v86 quad_perm:[1,0,3,2] row_mask:0xf bank_mask:0xf bound_ctrl:1
	v_pk_fma_f32 v[88:89], v[2:3], v[70:71], v[88:89]
	ds_read_b128 v[68:71], v8 offset:11264
	v_add_f32_dpp v86, v86, v86 quad_perm:[2,3,0,1] row_mask:0xf bank_mask:0xf bound_ctrl:1
	v_add_f32_e32 v95, v88, v89
	ds_read_b128 v[60:63], v8 offset:10752
	v_add_f32_dpp v86, v86, v86 row_half_mirror row_mask:0xf bank_mask:0xf bound_ctrl:1
	ds_read_b128 v[64:67], v8 offset:11008
	ds_read2_b32 v[72:73], v9 offset0:128 offset1:144
	v_add_f32_dpp v86, v86, v86 row_mirror row_mask:0xf bank_mask:0xf bound_ctrl:1
	s_waitcnt lgkmcnt(6)
	v_pk_mul_f32 v[80:81], v[44:45], v[74:75] op_sel:[0,1] op_sel_hi:[1,1]
	v_pk_mul_f32 v[82:83], v[46:47], v[74:75] op_sel:[0,1] op_sel_hi:[1,1]
	v_pk_fma_f32 v[0:1], v[20:21], v[86:87], v[76:77] op_sel_hi:[1,0,1]
	v_pk_fma_f32 v[2:3], v[22:23], v[86:87], v[78:79] op_sel_hi:[1,0,1]
	v_pk_mul_f32 v[84:85], v[0:1], v[32:33]
	ds_read_b128 v[12:15], v8 offset:11520
	ds_read_b128 v[16:19], v8 offset:11776
	v_pk_fma_f32 v[84:85], v[2:3], v[34:35], v[84:85]
	v_pk_fma_f32 v[80:81], v[0:1], v[36:37], v[80:81]
	v_add_f32_e32 v86, v84, v85
	v_pk_mul_f32 v[88:89], v[0:1], v[28:29]
	v_pk_fma_f32 v[82:83], v[2:3], v[38:39], v[82:83]
	v_add_f32_dpp v86, v86, v86 quad_perm:[1,0,3,2] row_mask:0xf bank_mask:0xf bound_ctrl:1
	v_pk_fma_f32 v[88:89], v[2:3], v[30:31], v[88:89]
	ds_read_b128 v[28:31], v8 offset:12544
	v_add_f32_dpp v86, v86, v86 quad_perm:[2,3,0,1] row_mask:0xf bank_mask:0xf bound_ctrl:1
	v_add_f32_e32 v96, v88, v89
	ds_read_b128 v[20:23], v8 offset:12032
	v_add_f32_dpp v86, v86, v86 row_half_mirror row_mask:0xf bank_mask:0xf bound_ctrl:1
	ds_read_b128 v[24:27], v8 offset:12288
	s_waitcnt lgkmcnt(5)
	v_pk_mul_f32 v[76:77], v[64:65], v[72:73] op_sel_hi:[1,0]
	v_add_f32_dpp v86, v86, v86 row_mirror row_mask:0xf bank_mask:0xf bound_ctrl:1
	v_pk_mul_f32 v[78:79], v[66:67], v[72:73] op_sel_hi:[1,0]
	v_pk_fma_f32 v[0:1], v[40:41], v[86:87], v[80:81] op_sel_hi:[1,0,1]
	v_pk_fma_f32 v[2:3], v[42:43], v[86:87], v[82:83] op_sel_hi:[1,0,1]
	v_pk_mul_f32 v[84:85], v[0:1], v[52:53]
	ds_read_b128 v[32:35], v8 offset:12800
	ds_read_b128 v[36:39], v8 offset:13056
	v_pk_fma_f32 v[84:85], v[2:3], v[54:55], v[84:85]
	v_pk_fma_f32 v[76:77], v[0:1], v[56:57], v[76:77]
	v_add_f32_e32 v86, v84, v85
	v_pk_mul_f32 v[88:89], v[0:1], v[48:49]
	v_pk_fma_f32 v[78:79], v[2:3], v[58:59], v[78:79]
	v_add_f32_dpp v86, v86, v86 quad_perm:[1,0,3,2] row_mask:0xf bank_mask:0xf bound_ctrl:1
	v_pk_fma_f32 v[88:89], v[2:3], v[50:51], v[88:89]
	ds_read_b128 v[48:51], v8 offset:13824
	v_add_f32_dpp v86, v86, v86 quad_perm:[2,3,0,1] row_mask:0xf bank_mask:0xf bound_ctrl:1
	v_add_f32_e32 v97, v88, v89
	ds_read_b128 v[40:43], v8 offset:13312
	v_add_f32_dpp v86, v86, v86 row_half_mirror row_mask:0xf bank_mask:0xf bound_ctrl:1
	ds_read_b128 v[44:47], v8 offset:13568
	ds_read2_b32 v[74:75], v9 offset0:160 offset1:176
	v_add_f32_dpp v86, v86, v86 row_mirror row_mask:0xf bank_mask:0xf bound_ctrl:1
	s_waitcnt lgkmcnt(6)
	v_pk_mul_f32 v[80:81], v[24:25], v[72:73] op_sel:[0,1] op_sel_hi:[1,1]
	v_pk_mul_f32 v[82:83], v[26:27], v[72:73] op_sel:[0,1] op_sel_hi:[1,1]
	v_pk_fma_f32 v[0:1], v[60:61], v[86:87], v[76:77] op_sel_hi:[1,0,1]
	v_pk_fma_f32 v[2:3], v[62:63], v[86:87], v[78:79] op_sel_hi:[1,0,1]
	v_pk_mul_f32 v[84:85], v[0:1], v[12:13]
	ds_read_b128 v[52:55], v8 offset:14080
	ds_read_b128 v[56:59], v8 offset:14336
	v_pk_fma_f32 v[84:85], v[2:3], v[14:15], v[84:85]
	v_pk_fma_f32 v[80:81], v[0:1], v[16:17], v[80:81]
	v_add_f32_e32 v86, v84, v85
	v_pk_mul_f32 v[88:89], v[0:1], v[68:69]
	v_pk_fma_f32 v[82:83], v[2:3], v[18:19], v[82:83]
	v_add_f32_dpp v86, v86, v86 quad_perm:[1,0,3,2] row_mask:0xf bank_mask:0xf bound_ctrl:1
	v_pk_fma_f32 v[88:89], v[2:3], v[70:71], v[88:89]
	ds_read_b128 v[68:71], v8 offset:15104
	v_add_f32_dpp v86, v86, v86 quad_perm:[2,3,0,1] row_mask:0xf bank_mask:0xf bound_ctrl:1
	v_add_f32_e32 v98, v88, v89
	ds_read_b128 v[60:63], v8 offset:14592
	v_add_f32_dpp v86, v86, v86 row_half_mirror row_mask:0xf bank_mask:0xf bound_ctrl:1
	ds_read_b128 v[64:67], v8 offset:14848
	s_waitcnt lgkmcnt(5)
	v_pk_mul_f32 v[76:77], v[44:45], v[74:75] op_sel_hi:[1,0]
	v_add_f32_dpp v86, v86, v86 row_mirror row_mask:0xf bank_mask:0xf bound_ctrl:1
	v_pk_mul_f32 v[78:79], v[46:47], v[74:75] op_sel_hi:[1,0]
	v_pk_fma_f32 v[0:1], v[20:21], v[86:87], v[80:81] op_sel_hi:[1,0,1]
	v_pk_fma_f32 v[2:3], v[22:23], v[86:87], v[82:83] op_sel_hi:[1,0,1]
	v_pk_mul_f32 v[84:85], v[0:1], v[32:33]
	ds_read_b128 v[12:15], v8 offset:15360
	ds_read_b128 v[16:19], v8 offset:15616
	v_pk_fma_f32 v[84:85], v[2:3], v[34:35], v[84:85]
	v_pk_fma_f32 v[76:77], v[0:1], v[36:37], v[76:77]
	v_cndmask_b32_e64 v122, v98, v90, s[6:7]
	v_add_f32_e32 v86, v84, v85
	v_pk_mul_f32 v[88:89], v[0:1], v[28:29]
	v_pk_fma_f32 v[78:79], v[2:3], v[38:39], v[78:79]
	v_add_f32_dpp v86, v86, v86 quad_perm:[1,0,3,2] row_mask:0xf bank_mask:0xf bound_ctrl:1
	v_pk_fma_f32 v[88:89], v[2:3], v[30:31], v[88:89]
	ds_read_b128 v[28:31], v8 offset:16384
	v_add_f32_dpp v86, v86, v86 quad_perm:[2,3,0,1] row_mask:0xf bank_mask:0xf bound_ctrl:1
	v_add_f32_e32 v99, v88, v89
	ds_read_b128 v[20:23], v8 offset:15872
	v_add_f32_dpp v86, v86, v86 row_half_mirror row_mask:0xf bank_mask:0xf bound_ctrl:1
	ds_read_b128 v[24:27], v8 offset:16128
	ds_read2_b32 v[72:73], v9 offset0:192 offset1:208
	v_cndmask_b32_e64 v123, v90, v98, s[6:7]
	v_add_f32_dpp v86, v86, v86 row_mirror row_mask:0xf bank_mask:0xf bound_ctrl:1
	s_waitcnt lgkmcnt(6)
	v_pk_mul_f32 v[80:81], v[64:65], v[74:75] op_sel:[0,1] op_sel_hi:[1,1]
	v_pk_mul_f32 v[82:83], v[66:67], v[74:75] op_sel:[0,1] op_sel_hi:[1,1]
	v_pk_fma_f32 v[0:1], v[40:41], v[86:87], v[76:77] op_sel_hi:[1,0,1]
	v_pk_fma_f32 v[2:3], v[42:43], v[86:87], v[78:79] op_sel_hi:[1,0,1]
	v_add_f32_dpp v90, v123, v122 row_mirror row_mask:0xf bank_mask:0xf bound_ctrl:1
	v_pk_mul_f32 v[84:85], v[0:1], v[52:53]
	ds_read_b128 v[32:35], v8 offset:16640
	ds_read_b128 v[36:39], v8 offset:16896
	v_pk_fma_f32 v[84:85], v[2:3], v[54:55], v[84:85]
	v_pk_fma_f32 v[80:81], v[0:1], v[56:57], v[80:81]
	v_cndmask_b32_e64 v124, v99, v91, s[6:7]
	v_add_f32_e32 v86, v84, v85
	v_pk_mul_f32 v[88:89], v[0:1], v[48:49]
	v_pk_fma_f32 v[82:83], v[2:3], v[58:59], v[82:83]
	v_add_f32_dpp v86, v86, v86 quad_perm:[1,0,3,2] row_mask:0xf bank_mask:0xf bound_ctrl:1
	v_pk_fma_f32 v[88:89], v[2:3], v[50:51], v[88:89]
	ds_read_b128 v[48:51], v8 offset:17664
	v_add_f32_dpp v86, v86, v86 quad_perm:[2,3,0,1] row_mask:0xf bank_mask:0xf bound_ctrl:1
	v_add_f32_e32 v100, v88, v89
	ds_read_b128 v[40:43], v8 offset:17152
	v_add_f32_dpp v86, v86, v86 row_half_mirror row_mask:0xf bank_mask:0xf bound_ctrl:1
	ds_read_b128 v[44:47], v8 offset:17408
	v_cndmask_b32_e64 v125, v91, v99, s[6:7]
	v_add_f32_dpp v86, v86, v86 row_mirror row_mask:0xf bank_mask:0xf bound_ctrl:1
	s_waitcnt lgkmcnt(5)
	v_pk_mul_f32 v[76:77], v[24:25], v[72:73] op_sel_hi:[1,0]
	v_pk_mul_f32 v[78:79], v[26:27], v[72:73] op_sel_hi:[1,0]
	v_pk_fma_f32 v[0:1], v[60:61], v[86:87], v[80:81] op_sel_hi:[1,0,1]
	v_pk_fma_f32 v[2:3], v[62:63], v[86:87], v[82:83] op_sel_hi:[1,0,1]
	v_add_f32_dpp v91, v125, v124 row_mirror row_mask:0xf bank_mask:0xf bound_ctrl:1
	v_pk_mul_f32 v[84:85], v[0:1], v[12:13]
	ds_read_b128 v[52:55], v8 offset:17920
	ds_read_b128 v[56:59], v8 offset:18176
	v_pk_fma_f32 v[84:85], v[2:3], v[14:15], v[84:85]
	v_pk_fma_f32 v[76:77], v[0:1], v[16:17], v[76:77]
	v_cndmask_b32_e64 v126, v100, v92, s[6:7]
	v_add_f32_e32 v86, v84, v85
	v_pk_mul_f32 v[88:89], v[0:1], v[68:69]
	v_pk_fma_f32 v[78:79], v[2:3], v[18:19], v[78:79]
	v_add_f32_dpp v86, v86, v86 quad_perm:[1,0,3,2] row_mask:0xf bank_mask:0xf bound_ctrl:1
	v_pk_fma_f32 v[88:89], v[2:3], v[70:71], v[88:89]
	ds_read_b128 v[68:71], v8 offset:18944
	v_add_f32_dpp v86, v86, v86 quad_perm:[2,3,0,1] row_mask:0xf bank_mask:0xf bound_ctrl:1
	v_add_f32_e32 v101, v88, v89
	ds_read_b128 v[60:63], v8 offset:18432
	v_add_f32_dpp v86, v86, v86 row_half_mirror row_mask:0xf bank_mask:0xf bound_ctrl:1
	ds_read_b128 v[64:67], v8 offset:18688
	ds_read2_b32 v[74:75], v9 offset0:224 offset1:240
	v_cndmask_b32_e64 v127, v92, v100, s[6:7]
	v_add_f32_dpp v86, v86, v86 row_mirror row_mask:0xf bank_mask:0xf bound_ctrl:1
	s_waitcnt lgkmcnt(6)
	v_pk_mul_f32 v[80:81], v[44:45], v[72:73] op_sel:[0,1] op_sel_hi:[1,1]
	v_pk_mul_f32 v[82:83], v[46:47], v[72:73] op_sel:[0,1] op_sel_hi:[1,1]
	v_pk_fma_f32 v[0:1], v[20:21], v[86:87], v[76:77] op_sel_hi:[1,0,1]
	v_pk_fma_f32 v[2:3], v[22:23], v[86:87], v[78:79] op_sel_hi:[1,0,1]
	v_add_f32_dpp v92, v127, v126 row_mirror row_mask:0xf bank_mask:0xf bound_ctrl:1
	v_pk_mul_f32 v[84:85], v[0:1], v[32:33]
	ds_read_b128 v[12:15], v8 offset:19200
	ds_read_b128 v[16:19], v8 offset:19456
	v_pk_fma_f32 v[84:85], v[2:3], v[34:35], v[84:85]
	v_pk_fma_f32 v[80:81], v[0:1], v[36:37], v[80:81]
	v_cndmask_b32_e64 v128, v101, v93, s[6:7]
	v_add_f32_e32 v86, v84, v85
	v_pk_mul_f32 v[88:89], v[0:1], v[28:29]
	v_pk_fma_f32 v[82:83], v[2:3], v[38:39], v[82:83]
	v_add_f32_dpp v86, v86, v86 quad_perm:[1,0,3,2] row_mask:0xf bank_mask:0xf bound_ctrl:1
	v_pk_fma_f32 v[88:89], v[2:3], v[30:31], v[88:89]
	ds_read_b128 v[28:31], v8 offset:20224
	v_add_f32_dpp v86, v86, v86 quad_perm:[2,3,0,1] row_mask:0xf bank_mask:0xf bound_ctrl:1
	v_add_f32_e32 v102, v88, v89
	ds_read_b128 v[20:23], v8 offset:19712
	v_add_f32_dpp v86, v86, v86 row_half_mirror row_mask:0xf bank_mask:0xf bound_ctrl:1
	ds_read_b128 v[24:27], v8 offset:19968
	v_cndmask_b32_e64 v129, v93, v101, s[6:7]
	v_add_f32_dpp v86, v86, v86 row_mirror row_mask:0xf bank_mask:0xf bound_ctrl:1
	s_waitcnt lgkmcnt(5)
	v_pk_mul_f32 v[76:77], v[64:65], v[74:75] op_sel_hi:[1,0]
	v_pk_mul_f32 v[78:79], v[66:67], v[74:75] op_sel_hi:[1,0]
	v_pk_fma_f32 v[0:1], v[40:41], v[86:87], v[80:81] op_sel_hi:[1,0,1]
	v_pk_fma_f32 v[2:3], v[42:43], v[86:87], v[82:83] op_sel_hi:[1,0,1]
	v_add_f32_dpp v93, v129, v128 row_mirror row_mask:0xf bank_mask:0xf bound_ctrl:1
	v_pk_mul_f32 v[84:85], v[0:1], v[52:53]
	ds_read_b128 v[32:35], v8 offset:20480
	ds_read_b128 v[36:39], v8 offset:20736
	v_pk_fma_f32 v[84:85], v[2:3], v[54:55], v[84:85]
	v_pk_fma_f32 v[76:77], v[0:1], v[56:57], v[76:77]
	v_cndmask_b32_e64 v130, v102, v94, s[6:7]
	v_add_f32_e32 v86, v84, v85
	v_pk_mul_f32 v[88:89], v[0:1], v[48:49]
	v_pk_fma_f32 v[78:79], v[2:3], v[58:59], v[78:79]
	v_cndmask_b32_e64 v131, v94, v102, s[6:7]
	v_add_f32_dpp v86, v86, v86 quad_perm:[1,0,3,2] row_mask:0xf bank_mask:0xf bound_ctrl:1
	v_pk_fma_f32 v[88:89], v[2:3], v[50:51], v[88:89]
	ds_read_b128 v[48:51], v8 offset:21504
	v_add_f32_dpp v86, v86, v86 quad_perm:[2,3,0,1] row_mask:0xf bank_mask:0xf bound_ctrl:1
	v_add_f32_e32 v103, v88, v89
	ds_read_b128 v[40:43], v8 offset:20992
	v_add_f32_dpp v86, v86, v86 row_half_mirror row_mask:0xf bank_mask:0xf bound_ctrl:1
	ds_read_b128 v[44:47], v8 offset:21248
	ds_read2_b32 v[72:73], v10 offset1:16
	v_add_f32_dpp v94, v131, v130 row_mirror row_mask:0xf bank_mask:0xf bound_ctrl:1
	v_add_f32_dpp v86, v86, v86 row_mirror row_mask:0xf bank_mask:0xf bound_ctrl:1
	s_waitcnt lgkmcnt(6)
	v_pk_mul_f32 v[80:81], v[24:25], v[74:75] op_sel:[0,1] op_sel_hi:[1,1]
	v_pk_mul_f32 v[82:83], v[26:27], v[74:75] op_sel:[0,1] op_sel_hi:[1,1]
	v_cndmask_b32_e64 v126, v94, v90, s[8:9]
	v_pk_fma_f32 v[0:1], v[60:61], v[86:87], v[76:77] op_sel_hi:[1,0,1]
	v_pk_fma_f32 v[2:3], v[62:63], v[86:87], v[78:79] op_sel_hi:[1,0,1]
	v_cndmask_b32_e64 v127, v90, v94, s[8:9]
	v_pk_mul_f32 v[84:85], v[0:1], v[12:13]
	ds_read_b128 v[52:55], v8 offset:21760
	v_add_f32_dpp v90, v127, v126 row_half_mirror row_mask:0xf bank_mask:0xf bound_ctrl:1
	ds_read_b128 v[56:59], v8 offset:22016
	v_pk_fma_f32 v[84:85], v[2:3], v[14:15], v[84:85]
	v_pk_fma_f32 v[80:81], v[0:1], v[16:17], v[80:81]
	v_cndmask_b32_e64 v132, v103, v95, s[6:7]
	v_add_f32_e32 v86, v84, v85
	v_pk_mul_f32 v[88:89], v[0:1], v[68:69]
	v_pk_fma_f32 v[82:83], v[2:3], v[18:19], v[82:83]
	v_cndmask_b32_e64 v133, v95, v103, s[6:7]
	v_add_f32_dpp v86, v86, v86 quad_perm:[1,0,3,2] row_mask:0xf bank_mask:0xf bound_ctrl:1
	v_pk_fma_f32 v[88:89], v[2:3], v[70:71], v[88:89]
	ds_read_b128 v[68:71], v8 offset:22784
	v_add_f32_dpp v86, v86, v86 quad_perm:[2,3,0,1] row_mask:0xf bank_mask:0xf bound_ctrl:1
	v_add_f32_e32 v104, v88, v89
	ds_read_b128 v[60:63], v8 offset:22272
	v_add_f32_dpp v86, v86, v86 row_half_mirror row_mask:0xf bank_mask:0xf bound_ctrl:1
	ds_read_b128 v[64:67], v8 offset:22528
	v_add_f32_dpp v95, v133, v132 row_mirror row_mask:0xf bank_mask:0xf bound_ctrl:1
	v_add_f32_dpp v86, v86, v86 row_mirror row_mask:0xf bank_mask:0xf bound_ctrl:1
	s_waitcnt lgkmcnt(5)
	v_pk_mul_f32 v[76:77], v[44:45], v[72:73] op_sel_hi:[1,0]
	v_pk_mul_f32 v[78:79], v[46:47], v[72:73] op_sel_hi:[1,0]
	v_cndmask_b32_e64 v128, v95, v91, s[8:9]
	v_pk_fma_f32 v[0:1], v[20:21], v[86:87], v[80:81] op_sel_hi:[1,0,1]
	v_pk_fma_f32 v[2:3], v[22:23], v[86:87], v[82:83] op_sel_hi:[1,0,1]
	v_cndmask_b32_e64 v129, v91, v95, s[8:9]
	v_pk_mul_f32 v[84:85], v[0:1], v[32:33]
	ds_read_b128 v[12:15], v8 offset:23040
	v_add_f32_dpp v91, v129, v128 row_half_mirror row_mask:0xf bank_mask:0xf bound_ctrl:1
	ds_read_b128 v[16:19], v8 offset:23296
	v_pk_fma_f32 v[84:85], v[2:3], v[34:35], v[84:85]
	v_pk_fma_f32 v[76:77], v[0:1], v[36:37], v[76:77]
	v_cndmask_b32_e64 v122, v104, v96, s[6:7]
	v_add_f32_e32 v86, v84, v85
	v_pk_mul_f32 v[88:89], v[0:1], v[28:29]
	v_pk_fma_f32 v[78:79], v[2:3], v[38:39], v[78:79]
	v_cndmask_b32_e64 v123, v96, v104, s[6:7]
	v_add_f32_dpp v86, v86, v86 quad_perm:[1,0,3,2] row_mask:0xf bank_mask:0xf bound_ctrl:1
	v_pk_fma_f32 v[88:89], v[2:3], v[30:31], v[88:89]
	ds_read_b128 v[28:31], v8 offset:24064
	v_add_f32_dpp v96, v123, v122 row_mirror row_mask:0xf bank_mask:0xf bound_ctrl:1
	v_add_f32_dpp v86, v86, v86 quad_perm:[2,3,0,1] row_mask:0xf bank_mask:0xf bound_ctrl:1
	v_add_f32_e32 v105, v88, v89
	ds_read_b128 v[20:23], v8 offset:23552
	v_cndmask_b32_e64 v130, v96, v92, s[8:9]
	v_add_f32_dpp v86, v86, v86 row_half_mirror row_mask:0xf bank_mask:0xf bound_ctrl:1
	ds_read_b128 v[24:27], v8 offset:23808
	ds_read2_b32 v[74:75], v10 offset0:32 offset1:48
	v_cndmask_b32_e64 v131, v92, v96, s[8:9]
	v_add_f32_dpp v86, v86, v86 row_mirror row_mask:0xf bank_mask:0xf bound_ctrl:1
	s_waitcnt lgkmcnt(6)
	v_pk_mul_f32 v[80:81], v[64:65], v[72:73] op_sel:[0,1] op_sel_hi:[1,1]
	v_pk_mul_f32 v[82:83], v[66:67], v[72:73] op_sel:[0,1] op_sel_hi:[1,1]
	v_add_f32_dpp v92, v131, v130 row_half_mirror row_mask:0xf bank_mask:0xf bound_ctrl:1
	v_pk_fma_f32 v[0:1], v[40:41], v[86:87], v[76:77] op_sel_hi:[1,0,1]
	v_pk_fma_f32 v[2:3], v[42:43], v[86:87], v[78:79] op_sel_hi:[1,0,1]
	v_cndmask_b32_e64 v122, v92, v90, s[10:11]
	v_cndmask_b32_e64 v123, v90, v92, s[10:11]
	v_pk_mul_f32 v[84:85], v[0:1], v[52:53]
	ds_read_b128 v[32:35], v8 offset:24320
	v_add_f32_dpp v90, v123, v122 quad_perm:[2,3,0,1] row_mask:0xf bank_mask:0xf bound_ctrl:1
	ds_read_b128 v[36:39], v8 offset:24576
	v_cndmask_b32_e64 v124, v105, v97, s[6:7]
	v_pk_fma_f32 v[84:85], v[2:3], v[54:55], v[84:85]
	v_pk_fma_f32 v[80:81], v[0:1], v[56:57], v[80:81]
	v_cndmask_b32_e64 v125, v97, v105, s[6:7]
	v_add_f32_e32 v86, v84, v85
	v_pk_mul_f32 v[88:89], v[0:1], v[48:49]
	v_add_f32_dpp v97, v125, v124 row_mirror row_mask:0xf bank_mask:0xf bound_ctrl:1
	v_pk_fma_f32 v[82:83], v[2:3], v[58:59], v[82:83]
	v_cndmask_b32_e64 v132, v97, v93, s[8:9]
	v_add_f32_dpp v86, v86, v86 quad_perm:[1,0,3,2] row_mask:0xf bank_mask:0xf bound_ctrl:1
	v_pk_fma_f32 v[88:89], v[2:3], v[50:51], v[88:89]
	ds_read_b128 v[48:51], v8 offset:25344
	v_cndmask_b32_e64 v133, v93, v97, s[8:9]
	v_add_f32_dpp v86, v86, v86 quad_perm:[2,3,0,1] row_mask:0xf bank_mask:0xf bound_ctrl:1
	v_add_f32_e32 v106, v88, v89
	ds_read_b128 v[40:43], v8 offset:24832
	v_add_f32_dpp v93, v133, v132 row_half_mirror row_mask:0xf bank_mask:0xf bound_ctrl:1
	v_add_f32_dpp v86, v86, v86 row_half_mirror row_mask:0xf bank_mask:0xf bound_ctrl:1
	ds_read_b128 v[44:47], v8 offset:25088
	v_cndmask_b32_e64 v124, v93, v91, s[10:11]
	v_cndmask_b32_e64 v125, v91, v93, s[10:11]
	v_add_f32_dpp v86, v86, v86 row_mirror row_mask:0xf bank_mask:0xf bound_ctrl:1
	s_waitcnt lgkmcnt(5)
	v_pk_mul_f32 v[76:77], v[24:25], v[74:75] op_sel_hi:[1,0]
	v_pk_mul_f32 v[78:79], v[26:27], v[74:75] op_sel_hi:[1,0]
	v_add_f32_dpp v91, v125, v124 quad_perm:[2,3,0,1] row_mask:0xf bank_mask:0xf bound_ctrl:1
	v_pk_fma_f32 v[0:1], v[60:61], v[86:87], v[80:81] op_sel_hi:[1,0,1]
	v_pk_fma_f32 v[2:3], v[62:63], v[86:87], v[82:83] op_sel_hi:[1,0,1]
	v_cndmask_b32_e64 v126, v91, v90, s[12:13]
	v_cndmask_b32_e64 v127, v90, v91, s[12:13]
	v_pk_mul_f32 v[84:85], v[0:1], v[12:13]
	v_pk_fma_f32 v[76:77], v[0:1], v[16:17], v[76:77]
	v_add_f32_dpp v90, v127, v126 quad_perm:[1,0,3,2] row_mask:0xf bank_mask:0xf bound_ctrl:1
	ds_write_b32 v11, v90
	ds_read_b128 v[52:55], v8 offset:25600
	ds_read_b128 v[56:59], v8 offset:25856
	v_pk_fma_f32 v[84:85], v[2:3], v[14:15], v[84:85]
	v_pk_mul_f32 v[88:89], v[0:1], v[68:69]
	v_add_f32_e32 v86, v84, v85
	v_pk_fma_f32 v[78:79], v[2:3], v[18:19], v[78:79]
	v_pk_fma_f32 v[88:89], v[2:3], v[70:71], v[88:89]
	v_add_f32_dpp v86, v86, v86 quad_perm:[1,0,3,2] row_mask:0xf bank_mask:0xf bound_ctrl:1
	ds_read_b128 v[68:71], v8 offset:26624
	v_add_f32_e32 v107, v88, v89
	v_add_f32_dpp v86, v86, v86 quad_perm:[2,3,0,1] row_mask:0xf bank_mask:0xf bound_ctrl:1
	ds_read_b128 v[60:63], v8 offset:26112
	ds_read_b128 v[64:67], v8 offset:26368
	v_add_f32_dpp v86, v86, v86 row_half_mirror row_mask:0xf bank_mask:0xf bound_ctrl:1
	ds_read2_b32 v[72:73], v10 offset0:64 offset1:80
	s_waitcnt lgkmcnt(7)
	v_pk_mul_f32 v[80:81], v[44:45], v[74:75] op_sel:[0,1] op_sel_hi:[1,1]
	v_add_f32_dpp v86, v86, v86 row_mirror row_mask:0xf bank_mask:0xf bound_ctrl:1
	v_pk_mul_f32 v[82:83], v[46:47], v[74:75] op_sel:[0,1] op_sel_hi:[1,1]
	v_pk_fma_f32 v[0:1], v[20:21], v[86:87], v[76:77] op_sel_hi:[1,0,1]
	v_pk_fma_f32 v[2:3], v[22:23], v[86:87], v[78:79] op_sel_hi:[1,0,1]
	v_pk_mul_f32 v[84:85], v[0:1], v[32:33]
	ds_read_b128 v[12:15], v8 offset:26880
	ds_read_b128 v[16:19], v8 offset:27136
	v_pk_fma_f32 v[84:85], v[2:3], v[34:35], v[84:85]
	v_pk_fma_f32 v[80:81], v[0:1], v[36:37], v[80:81]
	v_add_f32_e32 v86, v84, v85
	v_pk_mul_f32 v[88:89], v[0:1], v[28:29]
	v_pk_fma_f32 v[82:83], v[2:3], v[38:39], v[82:83]
	v_add_f32_dpp v86, v86, v86 quad_perm:[1,0,3,2] row_mask:0xf bank_mask:0xf bound_ctrl:1
	v_pk_fma_f32 v[88:89], v[2:3], v[30:31], v[88:89]
	ds_read_b128 v[28:31], v8 offset:27904
	v_add_f32_dpp v86, v86, v86 quad_perm:[2,3,0,1] row_mask:0xf bank_mask:0xf bound_ctrl:1
	v_add_f32_e32 v108, v88, v89
	ds_read_b128 v[20:23], v8 offset:27392
	v_add_f32_dpp v86, v86, v86 row_half_mirror row_mask:0xf bank_mask:0xf bound_ctrl:1
	ds_read_b128 v[24:27], v8 offset:27648
	s_waitcnt lgkmcnt(5)
	v_pk_mul_f32 v[76:77], v[64:65], v[72:73] op_sel_hi:[1,0]
	v_add_f32_dpp v86, v86, v86 row_mirror row_mask:0xf bank_mask:0xf bound_ctrl:1
	v_pk_mul_f32 v[78:79], v[66:67], v[72:73] op_sel_hi:[1,0]
	v_pk_fma_f32 v[0:1], v[40:41], v[86:87], v[80:81] op_sel_hi:[1,0,1]
	v_pk_fma_f32 v[2:3], v[42:43], v[86:87], v[82:83] op_sel_hi:[1,0,1]
	v_pk_mul_f32 v[84:85], v[0:1], v[52:53]
	ds_read_b128 v[32:35], v8 offset:28160
	ds_read_b128 v[36:39], v8 offset:28416
	v_pk_fma_f32 v[84:85], v[2:3], v[54:55], v[84:85]
	v_pk_fma_f32 v[76:77], v[0:1], v[56:57], v[76:77]
	v_add_f32_e32 v86, v84, v85
	v_pk_mul_f32 v[88:89], v[0:1], v[48:49]
	v_pk_fma_f32 v[78:79], v[2:3], v[58:59], v[78:79]
	v_add_f32_dpp v86, v86, v86 quad_perm:[1,0,3,2] row_mask:0xf bank_mask:0xf bound_ctrl:1
	v_pk_fma_f32 v[88:89], v[2:3], v[50:51], v[88:89]
	ds_read_b128 v[48:51], v8 offset:29184
	v_add_f32_dpp v86, v86, v86 quad_perm:[2,3,0,1] row_mask:0xf bank_mask:0xf bound_ctrl:1
	v_add_f32_e32 v109, v88, v89
	ds_read_b128 v[40:43], v8 offset:28672
	v_add_f32_dpp v86, v86, v86 row_half_mirror row_mask:0xf bank_mask:0xf bound_ctrl:1
	ds_read_b128 v[44:47], v8 offset:28928
	ds_read2_b32 v[74:75], v10 offset0:96 offset1:112
	v_add_f32_dpp v86, v86, v86 row_mirror row_mask:0xf bank_mask:0xf bound_ctrl:1
	s_waitcnt lgkmcnt(6)
	v_pk_mul_f32 v[80:81], v[24:25], v[72:73] op_sel:[0,1] op_sel_hi:[1,1]
	v_pk_mul_f32 v[82:83], v[26:27], v[72:73] op_sel:[0,1] op_sel_hi:[1,1]
	v_pk_fma_f32 v[0:1], v[60:61], v[86:87], v[76:77] op_sel_hi:[1,0,1]
	v_pk_fma_f32 v[2:3], v[62:63], v[86:87], v[78:79] op_sel_hi:[1,0,1]
	v_pk_mul_f32 v[84:85], v[0:1], v[12:13]
	ds_read_b128 v[52:55], v8 offset:29440
	ds_read_b128 v[56:59], v8 offset:29696
	v_pk_fma_f32 v[84:85], v[2:3], v[14:15], v[84:85]
	v_pk_fma_f32 v[80:81], v[0:1], v[16:17], v[80:81]
	v_add_f32_e32 v86, v84, v85
	v_pk_mul_f32 v[88:89], v[0:1], v[68:69]
	v_pk_fma_f32 v[82:83], v[2:3], v[18:19], v[82:83]
	v_add_f32_dpp v86, v86, v86 quad_perm:[1,0,3,2] row_mask:0xf bank_mask:0xf bound_ctrl:1
	v_pk_fma_f32 v[88:89], v[2:3], v[70:71], v[88:89]
	ds_read_b128 v[68:71], v8 offset:30464
	v_add_f32_dpp v86, v86, v86 quad_perm:[2,3,0,1] row_mask:0xf bank_mask:0xf bound_ctrl:1
	v_add_f32_e32 v110, v88, v89
	ds_read_b128 v[60:63], v8 offset:29952
	v_add_f32_dpp v86, v86, v86 row_half_mirror row_mask:0xf bank_mask:0xf bound_ctrl:1
	ds_read_b128 v[64:67], v8 offset:30208
	s_waitcnt lgkmcnt(5)
	v_pk_mul_f32 v[76:77], v[44:45], v[74:75] op_sel_hi:[1,0]
	v_add_f32_dpp v86, v86, v86 row_mirror row_mask:0xf bank_mask:0xf bound_ctrl:1
	v_pk_mul_f32 v[78:79], v[46:47], v[74:75] op_sel_hi:[1,0]
	v_pk_fma_f32 v[0:1], v[20:21], v[86:87], v[80:81] op_sel_hi:[1,0,1]
	v_pk_fma_f32 v[2:3], v[22:23], v[86:87], v[82:83] op_sel_hi:[1,0,1]
	v_pk_mul_f32 v[84:85], v[0:1], v[32:33]
	ds_read_b128 v[12:15], v8 offset:30720
	ds_read_b128 v[16:19], v8 offset:30976
	v_pk_fma_f32 v[84:85], v[2:3], v[34:35], v[84:85]
	v_pk_fma_f32 v[76:77], v[0:1], v[36:37], v[76:77]
	v_add_f32_e32 v86, v84, v85
	v_pk_mul_f32 v[88:89], v[0:1], v[28:29]
	v_pk_fma_f32 v[78:79], v[2:3], v[38:39], v[78:79]
	v_add_f32_dpp v86, v86, v86 quad_perm:[1,0,3,2] row_mask:0xf bank_mask:0xf bound_ctrl:1
	v_pk_fma_f32 v[88:89], v[2:3], v[30:31], v[88:89]
	ds_read_b128 v[28:31], v8 offset:31744
	v_add_f32_dpp v86, v86, v86 quad_perm:[2,3,0,1] row_mask:0xf bank_mask:0xf bound_ctrl:1
	v_add_f32_e32 v111, v88, v89
	ds_read_b128 v[20:23], v8 offset:31232
	v_add_f32_dpp v86, v86, v86 row_half_mirror row_mask:0xf bank_mask:0xf bound_ctrl:1
	ds_read_b128 v[24:27], v8 offset:31488
	ds_read2_b32 v[72:73], v10 offset0:128 offset1:144
	v_add_f32_dpp v86, v86, v86 row_mirror row_mask:0xf bank_mask:0xf bound_ctrl:1
	s_waitcnt lgkmcnt(6)
	v_pk_mul_f32 v[80:81], v[64:65], v[74:75] op_sel:[0,1] op_sel_hi:[1,1]
	v_pk_mul_f32 v[82:83], v[66:67], v[74:75] op_sel:[0,1] op_sel_hi:[1,1]
	v_pk_fma_f32 v[0:1], v[40:41], v[86:87], v[76:77] op_sel_hi:[1,0,1]
	v_pk_fma_f32 v[2:3], v[42:43], v[86:87], v[78:79] op_sel_hi:[1,0,1]
	v_pk_mul_f32 v[84:85], v[0:1], v[52:53]
	ds_read_b128 v[32:35], v8 offset:32000
	ds_read_b128 v[36:39], v8 offset:32256
	v_pk_fma_f32 v[84:85], v[2:3], v[54:55], v[84:85]
	v_pk_fma_f32 v[80:81], v[0:1], v[56:57], v[80:81]
	v_add_f32_e32 v86, v84, v85
	v_pk_mul_f32 v[88:89], v[0:1], v[48:49]
	v_pk_fma_f32 v[82:83], v[2:3], v[58:59], v[82:83]
	v_add_f32_dpp v86, v86, v86 quad_perm:[1,0,3,2] row_mask:0xf bank_mask:0xf bound_ctrl:1
	v_pk_fma_f32 v[88:89], v[2:3], v[50:51], v[88:89]
	ds_read_b128 v[48:51], v8 offset:33024
	v_add_f32_dpp v86, v86, v86 quad_perm:[2,3,0,1] row_mask:0xf bank_mask:0xf bound_ctrl:1
	v_add_f32_e32 v112, v88, v89
	ds_read_b128 v[40:43], v8 offset:32512
	v_add_f32_dpp v86, v86, v86 row_half_mirror row_mask:0xf bank_mask:0xf bound_ctrl:1
	ds_read_b128 v[44:47], v8 offset:32768
	s_waitcnt lgkmcnt(5)
	v_pk_mul_f32 v[76:77], v[24:25], v[72:73] op_sel_hi:[1,0]
	v_add_f32_dpp v86, v86, v86 row_mirror row_mask:0xf bank_mask:0xf bound_ctrl:1
	v_pk_mul_f32 v[78:79], v[26:27], v[72:73] op_sel_hi:[1,0]
	v_pk_fma_f32 v[0:1], v[60:61], v[86:87], v[80:81] op_sel_hi:[1,0,1]
	v_pk_fma_f32 v[2:3], v[62:63], v[86:87], v[82:83] op_sel_hi:[1,0,1]
	v_pk_mul_f32 v[84:85], v[0:1], v[12:13]
	ds_read_b128 v[52:55], v8 offset:33280
	ds_read_b128 v[56:59], v8 offset:33536
	v_pk_fma_f32 v[84:85], v[2:3], v[14:15], v[84:85]
	v_pk_fma_f32 v[76:77], v[0:1], v[16:17], v[76:77]
	v_add_f32_e32 v86, v84, v85
	v_pk_mul_f32 v[88:89], v[0:1], v[68:69]
	v_pk_fma_f32 v[78:79], v[2:3], v[18:19], v[78:79]
	v_add_f32_dpp v86, v86, v86 quad_perm:[1,0,3,2] row_mask:0xf bank_mask:0xf bound_ctrl:1
	v_pk_fma_f32 v[88:89], v[2:3], v[70:71], v[88:89]
	ds_read_b128 v[68:71], v8 offset:34304
	v_add_f32_dpp v86, v86, v86 quad_perm:[2,3,0,1] row_mask:0xf bank_mask:0xf bound_ctrl:1
	v_add_f32_e32 v113, v88, v89
	ds_read_b128 v[60:63], v8 offset:33792
	v_add_f32_dpp v86, v86, v86 row_half_mirror row_mask:0xf bank_mask:0xf bound_ctrl:1
	ds_read_b128 v[64:67], v8 offset:34048
	ds_read2_b32 v[74:75], v10 offset0:160 offset1:176
	v_add_f32_dpp v86, v86, v86 row_mirror row_mask:0xf bank_mask:0xf bound_ctrl:1
	s_waitcnt lgkmcnt(6)
	v_pk_mul_f32 v[80:81], v[44:45], v[72:73] op_sel:[0,1] op_sel_hi:[1,1]
	v_pk_mul_f32 v[82:83], v[46:47], v[72:73] op_sel:[0,1] op_sel_hi:[1,1]
	v_pk_fma_f32 v[0:1], v[20:21], v[86:87], v[76:77] op_sel_hi:[1,0,1]
	v_pk_fma_f32 v[2:3], v[22:23], v[86:87], v[78:79] op_sel_hi:[1,0,1]
	v_pk_mul_f32 v[84:85], v[0:1], v[32:33]
	ds_read_b128 v[12:15], v8 offset:34560
	ds_read_b128 v[16:19], v8 offset:34816
	v_pk_fma_f32 v[84:85], v[2:3], v[34:35], v[84:85]
	v_pk_fma_f32 v[80:81], v[0:1], v[36:37], v[80:81]
	v_add_f32_e32 v86, v84, v85
	v_pk_mul_f32 v[88:89], v[0:1], v[28:29]
	v_pk_fma_f32 v[82:83], v[2:3], v[38:39], v[82:83]
	v_add_f32_dpp v86, v86, v86 quad_perm:[1,0,3,2] row_mask:0xf bank_mask:0xf bound_ctrl:1
	v_pk_fma_f32 v[88:89], v[2:3], v[30:31], v[88:89]
	ds_read_b128 v[28:31], v8 offset:35584
	v_add_f32_dpp v86, v86, v86 quad_perm:[2,3,0,1] row_mask:0xf bank_mask:0xf bound_ctrl:1
	v_add_f32_e32 v114, v88, v89
	ds_read_b128 v[20:23], v8 offset:35072
	v_add_f32_dpp v86, v86, v86 row_half_mirror row_mask:0xf bank_mask:0xf bound_ctrl:1
	ds_read_b128 v[24:27], v8 offset:35328
	s_waitcnt lgkmcnt(5)
	v_pk_mul_f32 v[76:77], v[64:65], v[74:75] op_sel_hi:[1,0]
	v_add_f32_dpp v86, v86, v86 row_mirror row_mask:0xf bank_mask:0xf bound_ctrl:1
	v_pk_mul_f32 v[78:79], v[66:67], v[74:75] op_sel_hi:[1,0]
	v_pk_fma_f32 v[0:1], v[40:41], v[86:87], v[80:81] op_sel_hi:[1,0,1]
	v_pk_fma_f32 v[2:3], v[42:43], v[86:87], v[82:83] op_sel_hi:[1,0,1]
	v_pk_mul_f32 v[84:85], v[0:1], v[52:53]
	ds_read_b128 v[32:35], v8 offset:35840
	ds_read_b128 v[36:39], v8 offset:36096
	v_pk_fma_f32 v[84:85], v[2:3], v[54:55], v[84:85]
	v_pk_fma_f32 v[76:77], v[0:1], v[56:57], v[76:77]
	v_cndmask_b32_e64 v128, v114, v106, s[6:7]
	v_add_f32_e32 v86, v84, v85
	v_pk_mul_f32 v[88:89], v[0:1], v[48:49]
	v_pk_fma_f32 v[78:79], v[2:3], v[58:59], v[78:79]
	v_add_f32_dpp v86, v86, v86 quad_perm:[1,0,3,2] row_mask:0xf bank_mask:0xf bound_ctrl:1
	v_pk_fma_f32 v[88:89], v[2:3], v[50:51], v[88:89]
	ds_read_b128 v[48:51], v8 offset:36864
	v_add_f32_dpp v86, v86, v86 quad_perm:[2,3,0,1] row_mask:0xf bank_mask:0xf bound_ctrl:1
	v_add_f32_e32 v115, v88, v89
	ds_read_b128 v[40:43], v8 offset:36352
	v_add_f32_dpp v86, v86, v86 row_half_mirror row_mask:0xf bank_mask:0xf bound_ctrl:1
	ds_read_b128 v[44:47], v8 offset:36608
	ds_read2_b32 v[72:73], v10 offset0:192 offset1:208
	v_cndmask_b32_e64 v129, v106, v114, s[6:7]
	v_add_f32_dpp v86, v86, v86 row_mirror row_mask:0xf bank_mask:0xf bound_ctrl:1
	s_waitcnt lgkmcnt(6)
	v_pk_mul_f32 v[80:81], v[24:25], v[74:75] op_sel:[0,1] op_sel_hi:[1,1]
	v_pk_mul_f32 v[82:83], v[26:27], v[74:75] op_sel:[0,1] op_sel_hi:[1,1]
	v_pk_fma_f32 v[0:1], v[60:61], v[86:87], v[76:77] op_sel_hi:[1,0,1]
	v_pk_fma_f32 v[2:3], v[62:63], v[86:87], v[78:79] op_sel_hi:[1,0,1]
	v_add_f32_dpp v106, v129, v128 row_mirror row_mask:0xf bank_mask:0xf bound_ctrl:1
	v_pk_mul_f32 v[84:85], v[0:1], v[12:13]
	ds_read_b128 v[52:55], v8 offset:37120
	ds_read_b128 v[56:59], v8 offset:37376
	v_pk_fma_f32 v[84:85], v[2:3], v[14:15], v[84:85]
	v_pk_fma_f32 v[80:81], v[0:1], v[16:17], v[80:81]
	v_cndmask_b32_e64 v130, v115, v107, s[6:7]
	v_add_f32_e32 v86, v84, v85
	v_pk_mul_f32 v[88:89], v[0:1], v[68:69]
	v_pk_fma_f32 v[82:83], v[2:3], v[18:19], v[82:83]
	v_add_f32_dpp v86, v86, v86 quad_perm:[1,0,3,2] row_mask:0xf bank_mask:0xf bound_ctrl:1
	v_pk_fma_f32 v[88:89], v[2:3], v[70:71], v[88:89]
	ds_read_b128 v[68:71], v8 offset:38144
	v_add_f32_dpp v86, v86, v86 quad_perm:[2,3,0,1] row_mask:0xf bank_mask:0xf bound_ctrl:1
	v_add_f32_e32 v116, v88, v89
	ds_read_b128 v[60:63], v8 offset:37632
	v_add_f32_dpp v86, v86, v86 row_half_mirror row_mask:0xf bank_mask:0xf bound_ctrl:1
	ds_read_b128 v[64:67], v8 offset:37888
	v_cndmask_b32_e64 v131, v107, v115, s[6:7]
	v_add_f32_dpp v86, v86, v86 row_mirror row_mask:0xf bank_mask:0xf bound_ctrl:1
	s_waitcnt lgkmcnt(5)
	v_pk_mul_f32 v[76:77], v[44:45], v[72:73] op_sel_hi:[1,0]
	v_pk_mul_f32 v[78:79], v[46:47], v[72:73] op_sel_hi:[1,0]
	v_pk_fma_f32 v[0:1], v[20:21], v[86:87], v[80:81] op_sel_hi:[1,0,1]
	v_pk_fma_f32 v[2:3], v[22:23], v[86:87], v[82:83] op_sel_hi:[1,0,1]
	v_add_f32_dpp v107, v131, v130 row_mirror row_mask:0xf bank_mask:0xf bound_ctrl:1
	v_pk_mul_f32 v[84:85], v[0:1], v[32:33]
	ds_read_b128 v[12:15], v8 offset:38400
	ds_read_b128 v[16:19], v8 offset:38656
	v_pk_fma_f32 v[84:85], v[2:3], v[34:35], v[84:85]
	v_pk_fma_f32 v[76:77], v[0:1], v[36:37], v[76:77]
	v_cndmask_b32_e64 v132, v116, v108, s[6:7]
	v_add_f32_e32 v86, v84, v85
	v_pk_mul_f32 v[88:89], v[0:1], v[28:29]
	v_pk_fma_f32 v[78:79], v[2:3], v[38:39], v[78:79]
	v_add_f32_dpp v86, v86, v86 quad_perm:[1,0,3,2] row_mask:0xf bank_mask:0xf bound_ctrl:1
	v_pk_fma_f32 v[88:89], v[2:3], v[30:31], v[88:89]
	ds_read_b128 v[28:31], v8 offset:39424
	v_add_f32_dpp v86, v86, v86 quad_perm:[2,3,0,1] row_mask:0xf bank_mask:0xf bound_ctrl:1
	v_add_f32_e32 v117, v88, v89
	ds_read_b128 v[20:23], v8 offset:38912
	v_add_f32_dpp v86, v86, v86 row_half_mirror row_mask:0xf bank_mask:0xf bound_ctrl:1
	ds_read_b128 v[24:27], v8 offset:39168
	ds_read2_b32 v[74:75], v10 offset0:224 offset1:240
	v_cndmask_b32_e64 v133, v108, v116, s[6:7]
	v_add_f32_dpp v86, v86, v86 row_mirror row_mask:0xf bank_mask:0xf bound_ctrl:1
	s_waitcnt lgkmcnt(6)
	v_pk_mul_f32 v[80:81], v[64:65], v[72:73] op_sel:[0,1] op_sel_hi:[1,1]
	v_pk_mul_f32 v[82:83], v[66:67], v[72:73] op_sel:[0,1] op_sel_hi:[1,1]
	v_pk_fma_f32 v[0:1], v[40:41], v[86:87], v[76:77] op_sel_hi:[1,0,1]
	v_pk_fma_f32 v[2:3], v[42:43], v[86:87], v[78:79] op_sel_hi:[1,0,1]
	v_add_f32_dpp v108, v133, v132 row_mirror row_mask:0xf bank_mask:0xf bound_ctrl:1
	v_pk_mul_f32 v[84:85], v[0:1], v[52:53]
	ds_read_b128 v[32:35], v8 offset:39680
	ds_read_b128 v[36:39], v8 offset:39936
	v_pk_fma_f32 v[84:85], v[2:3], v[54:55], v[84:85]
	v_pk_fma_f32 v[80:81], v[0:1], v[56:57], v[80:81]
	v_cndmask_b32_e64 v122, v117, v109, s[6:7]
	v_add_f32_e32 v86, v84, v85
	v_pk_mul_f32 v[88:89], v[0:1], v[48:49]
	v_pk_fma_f32 v[82:83], v[2:3], v[58:59], v[82:83]
	v_add_f32_dpp v86, v86, v86 quad_perm:[1,0,3,2] row_mask:0xf bank_mask:0xf bound_ctrl:1
	v_pk_fma_f32 v[88:89], v[2:3], v[50:51], v[88:89]
	ds_read_b128 v[48:51], v8 offset:40704
	v_add_f32_dpp v86, v86, v86 quad_perm:[2,3,0,1] row_mask:0xf bank_mask:0xf bound_ctrl:1
	v_add_f32_e32 v118, v88, v89
	ds_read_b128 v[40:43], v8 offset:40192
	v_add_f32_dpp v86, v86, v86 row_half_mirror row_mask:0xf bank_mask:0xf bound_ctrl:1
	ds_read_b128 v[44:47], v8 offset:40448
	v_cndmask_b32_e64 v123, v109, v117, s[6:7]
	v_add_f32_dpp v86, v86, v86 row_mirror row_mask:0xf bank_mask:0xf bound_ctrl:1
	s_waitcnt lgkmcnt(5)
	v_pk_mul_f32 v[76:77], v[24:25], v[74:75] op_sel_hi:[1,0]
	v_pk_mul_f32 v[78:79], v[26:27], v[74:75] op_sel_hi:[1,0]
	v_pk_fma_f32 v[0:1], v[60:61], v[86:87], v[80:81] op_sel_hi:[1,0,1]
	v_pk_fma_f32 v[2:3], v[62:63], v[86:87], v[82:83] op_sel_hi:[1,0,1]
	v_add_f32_dpp v109, v123, v122 row_mirror row_mask:0xf bank_mask:0xf bound_ctrl:1
	v_pk_mul_f32 v[84:85], v[0:1], v[12:13]
	v_pk_fma_f32 v[76:77], v[0:1], v[16:17], v[76:77]
	v_pk_fma_f32 v[84:85], v[2:3], v[14:15], v[84:85]
	v_cndmask_b32_e64 v124, v118, v110, s[6:7]
	v_add_f32_e32 v86, v84, v85
	v_pk_mul_f32 v[88:89], v[0:1], v[68:69]
	v_pk_fma_f32 v[78:79], v[2:3], v[18:19], v[78:79]
	v_cndmask_b32_e64 v125, v110, v118, s[6:7]
	v_add_f32_dpp v86, v86, v86 quad_perm:[1,0,3,2] row_mask:0xf bank_mask:0xf bound_ctrl:1
	v_pk_fma_f32 v[88:89], v[2:3], v[70:71], v[88:89]
	v_add_f32_dpp v110, v125, v124 row_mirror row_mask:0xf bank_mask:0xf bound_ctrl:1
	v_add_f32_dpp v86, v86, v86 quad_perm:[2,3,0,1] row_mask:0xf bank_mask:0xf bound_ctrl:1
	v_add_f32_e32 v119, v88, v89
	s_waitcnt lgkmcnt(0)
	v_pk_mul_f32 v[80:81], v[44:45], v[74:75] op_sel:[0,1] op_sel_hi:[1,1]
	v_add_f32_dpp v86, v86, v86 row_half_mirror row_mask:0xf bank_mask:0xf bound_ctrl:1
	v_pk_mul_f32 v[82:83], v[46:47], v[74:75] op_sel:[0,1] op_sel_hi:[1,1]
	v_cndmask_b32_e64 v132, v110, v106, s[8:9]
	v_add_f32_dpp v86, v86, v86 row_mirror row_mask:0xf bank_mask:0xf bound_ctrl:1
	v_cndmask_b32_e64 v133, v106, v110, s[8:9]
	v_pk_fma_f32 v[0:1], v[20:21], v[86:87], v[76:77] op_sel_hi:[1,0,1]
	v_pk_fma_f32 v[2:3], v[22:23], v[86:87], v[78:79] op_sel_hi:[1,0,1]
	v_add_f32_dpp v106, v133, v132 row_half_mirror row_mask:0xf bank_mask:0xf bound_ctrl:1
	v_pk_mul_f32 v[84:85], v[0:1], v[32:33]
	v_pk_fma_f32 v[80:81], v[0:1], v[36:37], v[80:81]
	v_pk_fma_f32 v[84:85], v[2:3], v[34:35], v[84:85]
	v_cndmask_b32_e64 v126, v119, v111, s[6:7]
	v_add_f32_e32 v86, v84, v85
	v_pk_mul_f32 v[88:89], v[0:1], v[28:29]
	v_pk_fma_f32 v[82:83], v[2:3], v[38:39], v[82:83]
	v_cndmask_b32_e64 v127, v111, v119, s[6:7]
	v_add_f32_dpp v86, v86, v86 quad_perm:[1,0,3,2] row_mask:0xf bank_mask:0xf bound_ctrl:1
	v_pk_fma_f32 v[88:89], v[2:3], v[30:31], v[88:89]
	v_add_f32_dpp v111, v127, v126 row_mirror row_mask:0xf bank_mask:0xf bound_ctrl:1
	v_add_f32_dpp v86, v86, v86 quad_perm:[2,3,0,1] row_mask:0xf bank_mask:0xf bound_ctrl:1
	v_add_f32_e32 v120, v88, v89
	v_cndmask_b32_e64 v122, v111, v107, s[8:9]
	v_add_f32_dpp v86, v86, v86 row_half_mirror row_mask:0xf bank_mask:0xf bound_ctrl:1
	v_cndmask_b32_e64 v123, v107, v111, s[8:9]
	v_cndmask_b32_e64 v128, v120, v112, s[6:7]
	v_add_f32_dpp v86, v86, v86 row_mirror row_mask:0xf bank_mask:0xf bound_ctrl:1
	v_add_f32_dpp v107, v123, v122 row_half_mirror row_mask:0xf bank_mask:0xf bound_ctrl:1
	v_pk_fma_f32 v[0:1], v[40:41], v[86:87], v[80:81] op_sel_hi:[1,0,1]
	v_pk_fma_f32 v[2:3], v[42:43], v[86:87], v[82:83] op_sel_hi:[1,0,1]
	v_pk_mul_f32 v[88:89], v[0:1], v[48:49]
	v_cndmask_b32_e64 v129, v112, v120, s[6:7]
	v_pk_fma_f32 v[88:89], v[2:3], v[50:51], v[88:89]
	v_add_f32_e32 v121, v88, v89
	v_add_f32_dpp v112, v129, v128 row_mirror row_mask:0xf bank_mask:0xf bound_ctrl:1
	v_cndmask_b32_e64 v130, v121, v113, s[6:7]
	v_cndmask_b32_e64 v124, v112, v108, s[8:9]
	v_cndmask_b32_e64 v125, v108, v112, s[8:9]
	v_cndmask_b32_e64 v131, v113, v121, s[6:7]
	s_nop 0
	v_add_f32_dpp v108, v125, v124 row_half_mirror row_mask:0xf bank_mask:0xf bound_ctrl:1
	v_add_f32_dpp v113, v131, v130 row_mirror row_mask:0xf bank_mask:0xf bound_ctrl:1
	v_cndmask_b32_e64 v128, v108, v106, s[10:11]
	v_cndmask_b32_e64 v129, v106, v108, s[10:11]
	v_cndmask_b32_e64 v126, v113, v109, s[8:9]
	v_cndmask_b32_e64 v127, v109, v113, s[8:9]
	v_add_f32_dpp v106, v129, v128 quad_perm:[2,3,0,1] row_mask:0xf bank_mask:0xf bound_ctrl:1
	s_nop 0
	v_add_f32_dpp v109, v127, v126 row_half_mirror row_mask:0xf bank_mask:0xf bound_ctrl:1
	v_cndmask_b32_e64 v130, v109, v107, s[10:11]
	v_cndmask_b32_e64 v131, v107, v109, s[10:11]
	s_nop 0
	s_nop 0
	v_add_f32_dpp v107, v131, v130 quad_perm:[2,3,0,1] row_mask:0xf bank_mask:0xf bound_ctrl:1
	v_cndmask_b32_e64 v132, v107, v106, s[12:13]
	v_cndmask_b32_e64 v133, v106, v107, s[12:13]
	s_nop 0
	s_nop 0
	v_add_f32_dpp v106, v133, v132 quad_perm:[1,0,3,2] row_mask:0xf bank_mask:0xf bound_ctrl:1
	ds_write_b32 v11, v106 offset:1024
	s_waitcnt lgkmcnt(0)
	s_and_saveexec_b64 s[4:5], s[14:15]
	v_mov_b32_e32 v8, s17
	v_mov_b32_e32 v9, s16
	ds_write_b32 v8, v9
	s_or_b64 exec, exec, s[4:5]
	s_cmp_eq_u32 s16, 64
	s_cbranch_scc0 .LBB0_1817
	s_mov_b64 s[6:7], -1
